# v23 + redundant lgkmcnt waits inside the bf16 GEMM compute intervals removed
# baseline (speedup 1.0000x reference)
; #define PG8_STAGE(bufoff, gbase, voff) do { _Pragma("unroll") for (int _i = 0; _i < 2; ++_i) glds16_s((const void*)((const char*)(gbase) + _i * r64), (voff), ldsb + (unsigned)(bufoff) + ldsw + _i * 8192u); } while (0)
; #define PG8_LDA(b, h) do { _Pragma("unroll") for (int m = 0; m < 4; ++m) { const int o_ = PG8_SA(b, h) + aoff + m * 2048; \
;         if constexpr (FP8) A8[m] = PG8_CAT8(o_); else { At[m][0] = PG8_LD16(o_); At[m][1] = PG8_LD16(o_ + 1024); } } } while (0)
; #define PG8_LDB(X, X8, b, h) do { _Pragma("unroll") for (int n = 0; n < 2; ++n) { const int o_ = PG8_SB(b, h) + boff + n * 2048; \
;         if constexpr (FP8) X8[n] = PG8_CAT8(o_); else { X[n][0] = PG8_LD16(o_); X[n][1] = PG8_LD16(o_ + 1024); } } } while (0)
; #define PG8_WAIT_L(n) asm volatile("s_waitcnt lgkmcnt(" #n ")" ::: "memory")
; #define PG8_BAR __builtin_amdgcn_s_barrier()
; #define PG8_SCHED __builtin_amdgcn_sched_barrier(0)
; #define PG8_HI do { if constexpr (FP8) asm volatile("s_setprio 1"); } while (0)
; #define PG8_LO do { if constexpr (FP8) asm volatile("s_setprio 0"); } while (0)
; template <class Epi, class Sched, bool FP8 = false>
; __device__ __forceinline__ void gemm_phase(LAS unsigned char* lds, const int Kb, const int nt  , const Sched& S, const Epi& E) {
;     ...
;         for (int t = 0; t < nt; t += 2) {
;             const bool last = (t == nt - 2);
;             const char* a1 = cA + (size_t)(t + 1) * kstep;
;             const char* a2 = last ? nA : cA + (size_t)(t + 2) * kstep; const char* b2 = last ? nB : cB + (size_t)(t + 2) * kstep;
;             const char* a3 = a2 + kstep; const char* b3 = b2 + kstep;
;             PG8_LDB(B0, B08, 0, 0); PG8_SCHED; PG8_LDA(0, 0); PG8_STAGE(PG8_SA(1, 1), a1 + hstep, voffA);
;             PG8_WAIT_L(8); PG8_BAR; PG8_HI; PG8_WAIT_L(0); PG8_MMA(0, 0, B0, B08); PG8_BAR; PG8_LO; PG8_SCHED;
;             PG8_LDB(B1, B18, 0, 1); PG8_STAGE(PG8_SB(0, 0), b2, voffB);
;             PG8_BAR; PG8_HI; PG8_WAIT_L(0); PG8_MMA(0, 1, B1, B18); PG8_BAR; PG8_LO;
;             PG8_LDA(0, 1); PG8_STAGE(PG8_SA(0, 0), a2, voffA);
;             PG8_BAR; PG8_HI; PG8_WAIT_L(0); PG8_MMA(1, 0, B0, B08); PG8_BAR; PG8_LO; PG8_SCHED;
.LBB0_299:
	ds_read_b128 v[132:135], v148
	ds_read_b128 v[136:139], v149
	ds_read_b128 v[140:143], v150
	ds_read_b128 v[166:169], v151
	s_add_u32 s22, s20, 0x100
	s_addc_u32 s23, s21, 0
	s_cmp_eq_u32 s59, 28
	s_cselect_b32 s26, s16, s22
	s_cselect_b32 s27, s17, s23
	s_cselect_b32 s24, s18, s13
	s_cselect_b32 s25, s19, s58
	s_add_u32 s28, s26, 0x80
	s_addc_u32 s29, s27, 0
	ds_read_b128 v[170:173], v164
	ds_read_b128 v[174:177], v164 offset:1024
	ds_read_b128 v[178:181], v164 offset:2048
	ds_read_b128 v[182:185], v164 offset:3072
	ds_read_b128 v[186:189], v164 offset:4096
	ds_read_b128 v[190:193], v164 offset:5120
	ds_read_b128 v[194:197], v164 offset:6144
	ds_read_b128 v[198:201], v164 offset:7168
	s_add_u32 s60, s20, 0x80080
	s_addc_u32 s61, s21, 0
	s_mov_b32 s62, m0
	s_mov_b32 m0, s52
	s_nop 0
	global_load_lds_dwordx4 v1, s[60:61]
	s_mov_b32 m0, s62
	s_add_u32 s20, s20, 0xc0080
	s_addc_u32 s21, s21, 0
	s_mov_b32 s60, m0
	s_mov_b32 m0, s53
	s_nop 0
	global_load_lds_dwordx4 v1, s[20:21]
	s_mov_b32 m0, s60
	s_waitcnt lgkmcnt(8)
	s_barrier
	s_waitcnt lgkmcnt(0)
	s_setprio 1
	v_mfma_f32_16x16x32_bf16 v[126:129], v[132:135], v[170:173], v[126:129]
	v_mfma_f32_16x16x32_bf16 v[122:125], v[140:143], v[170:173], v[122:125]
	v_mfma_f32_16x16x32_bf16 v[110:113], v[132:135], v[178:181], v[110:113]
	v_mfma_f32_16x16x32_bf16 v[106:109], v[140:143], v[178:181], v[106:109]
	v_mfma_f32_16x16x32_bf16 v[94:97], v[132:135], v[186:189], v[94:97]
	v_mfma_f32_16x16x32_bf16 v[90:93], v[140:143], v[186:189], v[90:93]
	v_mfma_f32_16x16x32_bf16 v[78:81], v[132:135], v[194:197], v[78:81]
	v_mfma_f32_16x16x32_bf16 v[74:77], v[140:143], v[194:197], v[74:77]
	v_mfma_f32_16x16x32_bf16 v[126:129], v[136:139], v[174:177], v[126:129]
	v_mfma_f32_16x16x32_bf16 v[122:125], v[166:169], v[174:177], v[122:125]
	v_mfma_f32_16x16x32_bf16 v[110:113], v[136:139], v[182:185], v[110:113]
	v_mfma_f32_16x16x32_bf16 v[106:109], v[166:169], v[182:185], v[106:109]
	v_mfma_f32_16x16x32_bf16 v[94:97], v[136:139], v[190:193], v[94:97]
	v_mfma_f32_16x16x32_bf16 v[90:93], v[166:169], v[190:193], v[90:93]
	v_mfma_f32_16x16x32_bf16 v[78:81], v[136:139], v[198:201], v[78:81]
	v_mfma_f32_16x16x32_bf16 v[74:77], v[166:169], v[198:201], v[74:77]
	s_setprio 0
	s_barrier
	ds_read_b128 v[202:205], v152
	ds_read_b128 v[206:209], v153
	ds_read_b128 v[210:213], v154
	ds_read_b128 v[214:217], v155
	s_mov_b32 s20, m0
	s_mov_b32 m0, s37
	s_nop 0
	global_load_lds_dwordx4 v147, s[24:25]
	s_mov_b32 m0, s20
	s_add_u32 s20, s24, 0x40000
	s_addc_u32 s21, s25, 0
	s_mov_b32 s60, m0
	s_mov_b32 m0, s38
	s_nop 0
	global_load_lds_dwordx4 v147, s[20:21]
	s_mov_b32 m0, s60
	s_barrier
	s_waitcnt lgkmcnt(0)
	s_setprio 1
	v_mfma_f32_16x16x32_bf16 v[118:121], v[202:205], v[170:173], v[118:121]
	v_mfma_f32_16x16x32_bf16 v[114:117], v[210:213], v[170:173], v[114:117]
	v_mfma_f32_16x16x32_bf16 v[102:105], v[202:205], v[178:181], v[102:105]
	v_mfma_f32_16x16x32_bf16 v[98:101], v[210:213], v[178:181], v[98:101]
	v_mfma_f32_16x16x32_bf16 v[86:89], v[202:205], v[186:189], v[86:89]
	v_mfma_f32_16x16x32_bf16 v[82:85], v[210:213], v[186:189], v[82:85]
	v_mfma_f32_16x16x32_bf16 v[70:73], v[202:205], v[194:197], v[70:73]
	v_mfma_f32_16x16x32_bf16 v[66:69], v[210:213], v[194:197], v[66:69]
	v_mfma_f32_16x16x32_bf16 v[118:121], v[206:209], v[174:177], v[118:121]
	v_mfma_f32_16x16x32_bf16 v[114:117], v[214:217], v[174:177], v[114:117]
	v_mfma_f32_16x16x32_bf16 v[102:105], v[206:209], v[182:185], v[102:105]
	v_mfma_f32_16x16x32_bf16 v[98:101], v[214:217], v[182:185], v[98:101]
	v_mfma_f32_16x16x32_bf16 v[86:89], v[206:209], v[190:193], v[86:89]
	v_mfma_f32_16x16x32_bf16 v[82:85], v[214:217], v[190:193], v[82:85]
	v_mfma_f32_16x16x32_bf16 v[70:73], v[206:209], v[198:201], v[70:73]
	v_mfma_f32_16x16x32_bf16 v[66:69], v[214:217], v[198:201], v[66:69]
	s_setprio 0
	s_barrier
	ds_read_b128 v[170:173], v164 offset:16384
	ds_read_b128 v[174:177], v164 offset:17408
	ds_read_b128 v[178:181], v164 offset:18432
	ds_read_b128 v[182:185], v164 offset:19456
	ds_read_b128 v[186:189], v164 offset:20480
	ds_read_b128 v[190:193], v164 offset:21504
	ds_read_b128 v[194:197], v164 offset:22528
	ds_read_b128 v[198:201], v164 offset:23552
	s_mov_b32 s20, m0
	s_mov_b32 m0, s36
	s_nop 0
	global_load_lds_dwordx4 v1, s[26:27]
	s_mov_b32 m0, s20
	s_add_u32 s20, s26, 0x40000
	s_addc_u32 s21, s27, 0
	s_mov_b32 s60, m0
	s_mov_b32 m0, s39
	s_nop 0
	global_load_lds_dwordx4 v1, s[20:21]
	s_mov_b32 m0, s60
	s_barrier
	s_waitcnt lgkmcnt(0)
	s_setprio 1
	v_mfma_f32_16x16x32_bf16 v[62:65], v[132:135], v[170:173], v[62:65]
	v_mfma_f32_16x16x32_bf16 v[58:61], v[140:143], v[170:173], v[58:61]
	v_mfma_f32_16x16x32_bf16 v[46:49], v[132:135], v[178:181], v[46:49]
	v_mfma_f32_16x16x32_bf16 v[42:45], v[140:143], v[178:181], v[42:45]
	v_mfma_f32_16x16x32_bf16 v[30:33], v[132:135], v[186:189], v[30:33]
	v_mfma_f32_16x16x32_bf16 v[26:29], v[140:143], v[186:189], v[26:29]
	v_mfma_f32_16x16x32_bf16 v[14:17], v[132:135], v[194:197], v[14:17]
	v_mfma_f32_16x16x32_bf16 v[10:13], v[140:143], v[194:197], v[10:13]
	v_mfma_f32_16x16x32_bf16 v[62:65], v[136:139], v[174:177], v[62:65]
	v_mfma_f32_16x16x32_bf16 v[58:61], v[166:169], v[174:177], v[58:61]
	v_mfma_f32_16x16x32_bf16 v[46:49], v[136:139], v[182:185], v[46:49]
	v_mfma_f32_16x16x32_bf16 v[42:45], v[166:169], v[182:185], v[42:45]
	v_mfma_f32_16x16x32_bf16 v[30:33], v[136:139], v[190:193], v[30:33]
	v_mfma_f32_16x16x32_bf16 v[26:29], v[166:169], v[190:193], v[26:29]
	v_mfma_f32_16x16x32_bf16 v[14:17], v[136:139], v[198:201], v[14:17]
	v_mfma_f32_16x16x32_bf16 v[10:13], v[166:169], v[198:201], v[10:13]
	s_setprio 0
	s_barrier
; #define PG8_STAGE(bufoff, gbase, voff) do { _Pragma("unroll") for (int _i = 0; _i < 2; ++_i) glds16_s((const void*)((const char*)(gbase) + _i * r64), (voff), ldsb + (unsigned)(bufoff) + ldsw + _i * 8192u); } while (0)
; #define PG8_LDA(b, h) do { _Pragma("unroll") for (int m = 0; m < 4; ++m) { const int o_ = PG8_SA(b, h) + aoff + m * 2048; \
;         if constexpr (FP8) A8[m] = PG8_CAT8(o_); else { At[m][0] = PG8_LD16(o_); At[m][1] = PG8_LD16(o_ + 1024); } } } while (0)
; #define PG8_LDB(X, X8, b, h) do { _Pragma("unroll") for (int n = 0; n < 2; ++n) { const int o_ = PG8_SB(b, h) + boff + n * 2048; \
;         if constexpr (FP8) X8[n] = PG8_CAT8(o_); else { X[n][0] = PG8_LD16(o_); X[n][1] = PG8_LD16(o_ + 1024); } } } while (0)
; #define PG8_WAIT_V(n) asm volatile("s_waitcnt vmcnt(" #n ")" ::: "memory")
; #define PG8_WAIT_L(n) asm volatile("s_waitcnt lgkmcnt(" #n ")" ::: "memory")
; #define PG8_BAR __builtin_amdgcn_s_barrier()
; #define PG8_SCHED __builtin_amdgcn_sched_barrier(0)
; #define PG8_HI do { if constexpr (FP8) asm volatile("s_setprio 1"); } while (0)
; #define PG8_LO do { if constexpr (FP8) asm volatile("s_setprio 0"); } while (0)
; template <class Epi, class Sched, bool FP8 = false>
; __device__ __forceinline__ void gemm_phase(LAS unsigned char* lds, const int Kb, const int nt  , const Sched& S, const Epi& E) {
;     ...
;             PG8_STAGE(PG8_SB(0, 1), b2 + hstep, voffB);
;             PG8_WAIT_V(6); PG8_BAR; PG8_HI; PG8_MMA(1, 1, B1, B18); PG8_BAR; PG8_LO;
;             PG8_LDB(B0, B08, 1, 0); PG8_SCHED; PG8_LDA(1, 0); PG8_STAGE(PG8_SA(0, 1), a2 + hstep, voffA);
;             PG8_WAIT_L(8); PG8_BAR; PG8_HI; PG8_WAIT_L(0); PG8_MMA(0, 0, B0, B08); PG8_BAR; PG8_LO; PG8_SCHED;
;             PG8_LDB(B1, B18, 1, 1); PG8_STAGE(PG8_SB(1, 0), b3, voffB);
	s_add_u32 s20, s24, 0x80000
	s_addc_u32 s21, s25, 0
	s_mov_b32 s60, m0
	s_mov_b32 m0, s40
	s_nop 0
	global_load_lds_dwordx4 v147, s[20:21]
	s_mov_b32 m0, s60
	s_add_u32 s20, s24, 0xc0000
	s_addc_u32 s21, s25, 0
	s_mov_b32 s60, m0
	s_mov_b32 m0, s41
	s_nop 0
	global_load_lds_dwordx4 v147, s[20:21]
	s_mov_b32 m0, s60
	s_waitcnt vmcnt(6)
	s_barrier
	s_setprio 1
	v_mfma_f32_16x16x32_bf16 v[54:57], v[202:205], v[170:173], v[54:57]
	v_mfma_f32_16x16x32_bf16 v[50:53], v[210:213], v[170:173], v[50:53]
	v_mfma_f32_16x16x32_bf16 v[38:41], v[202:205], v[178:181], v[38:41]
	v_mfma_f32_16x16x32_bf16 v[34:37], v[210:213], v[178:181], v[34:37]
	v_mfma_f32_16x16x32_bf16 v[22:25], v[202:205], v[186:189], v[22:25]
	v_mfma_f32_16x16x32_bf16 v[18:21], v[210:213], v[186:189], v[18:21]
	v_mfma_f32_16x16x32_bf16 v[6:9], v[202:205], v[194:197], v[6:9]
	v_mfma_f32_16x16x32_bf16 v[2:5], v[210:213], v[194:197], v[2:5]
	v_mfma_f32_16x16x32_bf16 v[54:57], v[206:209], v[174:177], v[54:57]
	v_mfma_f32_16x16x32_bf16 v[50:53], v[214:217], v[174:177], v[50:53]
	v_mfma_f32_16x16x32_bf16 v[38:41], v[206:209], v[182:185], v[38:41]
	v_mfma_f32_16x16x32_bf16 v[34:37], v[214:217], v[182:185], v[34:37]
	v_mfma_f32_16x16x32_bf16 v[22:25], v[206:209], v[190:193], v[22:25]
	v_mfma_f32_16x16x32_bf16 v[18:21], v[214:217], v[190:193], v[18:21]
	v_mfma_f32_16x16x32_bf16 v[6:9], v[206:209], v[198:201], v[6:9]
	v_mfma_f32_16x16x32_bf16 v[2:5], v[214:217], v[198:201], v[2:5]
	s_setprio 0
	s_barrier
	ds_read_b128 v[132:135], v156
	ds_read_b128 v[136:139], v157
	ds_read_b128 v[140:143], v158
	ds_read_b128 v[166:169], v159
	ds_read_b128 v[170:173], v164 offset:32768
	ds_read_b128 v[174:177], v164 offset:33792
	ds_read_b128 v[178:181], v164 offset:34816
	ds_read_b128 v[182:185], v164 offset:35840
	ds_read_b128 v[186:189], v164 offset:36864
	ds_read_b128 v[190:193], v164 offset:37888
	ds_read_b128 v[194:197], v164 offset:38912
	ds_read_b128 v[198:201], v164 offset:39936
	s_add_u32 s20, s26, 0x80000
	s_addc_u32 s21, s27, 0
	s_mov_b32 s60, m0
	s_mov_b32 m0, s42
	s_nop 0
	global_load_lds_dwordx4 v1, s[20:21]
	s_mov_b32 m0, s60
	s_add_u32 s20, s26, 0xc0000
	s_addc_u32 s21, s27, 0
	s_mov_b32 s60, m0
	s_mov_b32 m0, s43
	s_nop 0
	global_load_lds_dwordx4 v1, s[20:21]
	s_mov_b32 m0, s60
	s_waitcnt lgkmcnt(8)
	s_barrier
	s_waitcnt lgkmcnt(0)
	s_setprio 1
	v_mfma_f32_16x16x32_bf16 v[126:129], v[132:135], v[170:173], v[126:129]
	v_mfma_f32_16x16x32_bf16 v[122:125], v[140:143], v[170:173], v[122:125]
	v_mfma_f32_16x16x32_bf16 v[110:113], v[132:135], v[178:181], v[110:113]
	v_mfma_f32_16x16x32_bf16 v[106:109], v[140:143], v[178:181], v[106:109]
	v_mfma_f32_16x16x32_bf16 v[94:97], v[132:135], v[186:189], v[94:97]
	v_mfma_f32_16x16x32_bf16 v[90:93], v[140:143], v[186:189], v[90:93]
	v_mfma_f32_16x16x32_bf16 v[78:81], v[132:135], v[194:197], v[78:81]
	v_mfma_f32_16x16x32_bf16 v[74:77], v[140:143], v[194:197], v[74:77]
	v_mfma_f32_16x16x32_bf16 v[126:129], v[136:139], v[174:177], v[126:129]
	v_mfma_f32_16x16x32_bf16 v[122:125], v[166:169], v[174:177], v[122:125]
	v_mfma_f32_16x16x32_bf16 v[110:113], v[136:139], v[182:185], v[110:113]
	v_mfma_f32_16x16x32_bf16 v[106:109], v[166:169], v[182:185], v[106:109]
	v_mfma_f32_16x16x32_bf16 v[94:97], v[136:139], v[190:193], v[94:97]
	v_mfma_f32_16x16x32_bf16 v[90:93], v[166:169], v[190:193], v[90:93]
	v_mfma_f32_16x16x32_bf16 v[78:81], v[136:139], v[198:201], v[78:81]
	v_mfma_f32_16x16x32_bf16 v[74:77], v[166:169], v[198:201], v[74:77]
	s_setprio 0
	s_barrier
	ds_read_b128 v[202:205], v160
	ds_read_b128 v[206:209], v161
	ds_read_b128 v[210:213], v162
	ds_read_b128 v[214:217], v163
	s_add_u32 s20, s24, 0x80
	s_addc_u32 s21, s25, 0
	s_mov_b32 s60, m0
	s_mov_b32 m0, s46
	s_nop 0
	global_load_lds_dwordx4 v147, s[20:21]
	s_mov_b32 m0, s60
	s_add_u32 s20, s24, 0x40080
	s_addc_u32 s21, s25, 0
	s_mov_b32 s60, m0
	s_mov_b32 m0, s47
	s_nop 0
	global_load_lds_dwordx4 v147, s[20:21]
	s_mov_b32 m0, s60
	s_barrier
; #define PG8_STAGE(bufoff, gbase, voff) do { _Pragma("unroll") for (int _i = 0; _i < 2; ++_i) glds16_s((const void*)((const char*)(gbase) + _i * r64), (voff), ldsb + (unsigned)(bufoff) + ldsw + _i * 8192u); } while (0)
; #define PG8_LDA(b, h) do { _Pragma("unroll") for (int m = 0; m < 4; ++m) { const int o_ = PG8_SA(b, h) + aoff + m * 2048; \
;         if constexpr (FP8) A8[m] = PG8_CAT8(o_); else { At[m][0] = PG8_LD16(o_); At[m][1] = PG8_LD16(o_ + 1024); } } } while (0)
; #define PG8_WAIT_V(n) asm volatile("s_waitcnt vmcnt(" #n ")" ::: "memory")
; #define PG8_WAIT_L(n) asm volatile("s_waitcnt lgkmcnt(" #n ")" ::: "memory")
; #define PG8_BAR __builtin_amdgcn_s_barrier()
; #define PG8_SCHED __builtin_amdgcn_sched_barrier(0)
; #define PG8_HI do { if constexpr (FP8) asm volatile("s_setprio 1"); } while (0)
; #define PG8_LO do { if constexpr (FP8) asm volatile("s_setprio 0"); } while (0)
;     __device__ __forceinline__ void operator()(const f32x4 (&acc)[2][2][4][2], const Unit& u, int wr, int wc, int fr, int fq) const {
;         const int row0 = u.pm * BM + wr * 64 + fr, seg = u.pn >> 2, scol0 = (u.pn & 3) * BM + wc * 32 + 8 * fq;
;         const int kind = (seg == 2 || seg == 6) ? 1 : ((seg == 7) ? 2 : 0);
;         bf16_t* const Vb = (seg == 2) ? VAo : VBo;
; template <class Epi, class Sched, bool FP8 = false>
; __device__ __forceinline__ void gemm_phase(LAS unsigned char* lds, const int Kb, const int nt  , const Sched& S, const Epi& E) {
;     ...
;             PG8_BAR; PG8_HI; PG8_WAIT_L(0); PG8_MMA(0, 1, B1, B18); PG8_BAR; PG8_LO;
;             PG8_LDA(1, 1); PG8_STAGE(PG8_SA(1, 0), a3, voffA);
;             PG8_BAR; PG8_HI; PG8_WAIT_L(0); PG8_MMA(1, 0, B0, B08); PG8_BAR; PG8_LO; PG8_SCHED;
;             PG8_STAGE(PG8_SB(1, 1), b3 + hstep, voffB);
;             PG8_WAIT_V(6); PG8_BAR; PG8_HI; PG8_MMA(1, 1, B1, B18); PG8_BAR; PG8_LO;
;         }
;         { int l_; asm volatile("v_mbcnt_lo_u32_b32 %0, -1, 0\n\tv_mbcnt_hi_u32_b32 %0, -1, %0" : "=v"(l_));
;           E(acc, cur, wr, wc, l_ & 15, l_ >> 4); }
	s_waitcnt lgkmcnt(0)
	s_setprio 1
	v_mfma_f32_16x16x32_bf16 v[118:121], v[202:205], v[170:173], v[118:121]
	v_mfma_f32_16x16x32_bf16 v[114:117], v[210:213], v[170:173], v[114:117]
	v_mfma_f32_16x16x32_bf16 v[102:105], v[202:205], v[178:181], v[102:105]
	v_mfma_f32_16x16x32_bf16 v[98:101], v[210:213], v[178:181], v[98:101]
	v_mfma_f32_16x16x32_bf16 v[86:89], v[202:205], v[186:189], v[86:89]
	v_mfma_f32_16x16x32_bf16 v[82:85], v[210:213], v[186:189], v[82:85]
	v_mfma_f32_16x16x32_bf16 v[70:73], v[202:205], v[194:197], v[70:73]
	v_mfma_f32_16x16x32_bf16 v[66:69], v[210:213], v[194:197], v[66:69]
	v_mfma_f32_16x16x32_bf16 v[118:121], v[206:209], v[174:177], v[118:121]
	v_mfma_f32_16x16x32_bf16 v[114:117], v[214:217], v[174:177], v[114:117]
	v_mfma_f32_16x16x32_bf16 v[102:105], v[206:209], v[182:185], v[102:105]
	v_mfma_f32_16x16x32_bf16 v[98:101], v[214:217], v[182:185], v[98:101]
	v_mfma_f32_16x16x32_bf16 v[86:89], v[206:209], v[190:193], v[86:89]
	v_mfma_f32_16x16x32_bf16 v[82:85], v[214:217], v[190:193], v[82:85]
	v_mfma_f32_16x16x32_bf16 v[70:73], v[206:209], v[198:201], v[70:73]
	v_mfma_f32_16x16x32_bf16 v[66:69], v[214:217], v[198:201], v[66:69]
	s_setprio 0
	s_barrier
	ds_read_b128 v[170:173], v164 offset:49152
	ds_read_b128 v[174:177], v164 offset:50176
	ds_read_b128 v[178:181], v164 offset:51200
	ds_read_b128 v[182:185], v164 offset:52224
	ds_read_b128 v[186:189], v164 offset:53248
	ds_read_b128 v[190:193], v164 offset:54272
	ds_read_b128 v[194:197], v164 offset:55296
	ds_read_b128 v[198:201], v164 offset:56320
	s_mov_b32 s20, m0
	s_mov_b32 m0, s48
	s_nop 0
	global_load_lds_dwordx4 v1, s[28:29]
	s_mov_b32 m0, s20
	s_add_u32 s20, s26, 0x40080
	s_addc_u32 s21, s27, 0
	s_mov_b32 s26, m0
	s_mov_b32 m0, s49
	s_nop 0
	global_load_lds_dwordx4 v1, s[20:21]
	s_mov_b32 m0, s26
	s_barrier
	s_waitcnt lgkmcnt(0)
	s_setprio 1
	v_mfma_f32_16x16x32_bf16 v[62:65], v[132:135], v[170:173], v[62:65]
	v_mfma_f32_16x16x32_bf16 v[58:61], v[140:143], v[170:173], v[58:61]
	v_mfma_f32_16x16x32_bf16 v[46:49], v[132:135], v[178:181], v[46:49]
	v_mfma_f32_16x16x32_bf16 v[42:45], v[140:143], v[178:181], v[42:45]
	v_mfma_f32_16x16x32_bf16 v[30:33], v[132:135], v[186:189], v[30:33]
	v_mfma_f32_16x16x32_bf16 v[26:29], v[140:143], v[186:189], v[26:29]
	v_mfma_f32_16x16x32_bf16 v[14:17], v[132:135], v[194:197], v[14:17]
	v_mfma_f32_16x16x32_bf16 v[10:13], v[140:143], v[194:197], v[10:13]
	v_mfma_f32_16x16x32_bf16 v[62:65], v[136:139], v[174:177], v[62:65]
	v_mfma_f32_16x16x32_bf16 v[58:61], v[166:169], v[174:177], v[58:61]
	v_mfma_f32_16x16x32_bf16 v[46:49], v[136:139], v[182:185], v[46:49]
	v_mfma_f32_16x16x32_bf16 v[42:45], v[166:169], v[182:185], v[42:45]
	v_mfma_f32_16x16x32_bf16 v[30:33], v[136:139], v[190:193], v[30:33]
	v_mfma_f32_16x16x32_bf16 v[26:29], v[166:169], v[190:193], v[26:29]
	v_mfma_f32_16x16x32_bf16 v[14:17], v[136:139], v[198:201], v[14:17]
	v_mfma_f32_16x16x32_bf16 v[10:13], v[166:169], v[198:201], v[10:13]
	s_setprio 0
	s_barrier
	s_add_u32 s20, s24, 0x80080
	s_addc_u32 s21, s25, 0
	s_mov_b32 s26, m0
	s_mov_b32 m0, s50
	s_nop 0
	global_load_lds_dwordx4 v147, s[20:21]
	s_mov_b32 m0, s26
	s_add_u32 s20, s24, 0xc0080
	s_addc_u32 s21, s25, 0
	s_mov_b32 s24, m0
	s_mov_b32 m0, s51
	s_nop 0
	global_load_lds_dwordx4 v147, s[20:21]
	s_mov_b32 m0, s24
	s_waitcnt vmcnt(6)
	s_barrier
	s_setprio 1
	v_mfma_f32_16x16x32_bf16 v[54:57], v[202:205], v[170:173], v[54:57]
	v_mfma_f32_16x16x32_bf16 v[50:53], v[210:213], v[170:173], v[50:53]
	v_mfma_f32_16x16x32_bf16 v[38:41], v[202:205], v[178:181], v[38:41]
	v_mfma_f32_16x16x32_bf16 v[34:37], v[210:213], v[178:181], v[34:37]
	v_mfma_f32_16x16x32_bf16 v[22:25], v[202:205], v[186:189], v[22:25]
	v_mfma_f32_16x16x32_bf16 v[18:21], v[210:213], v[186:189], v[18:21]
	v_mfma_f32_16x16x32_bf16 v[6:9], v[202:205], v[194:197], v[6:9]
	v_mfma_f32_16x16x32_bf16 v[2:5], v[210:213], v[194:197], v[2:5]
	v_mfma_f32_16x16x32_bf16 v[54:57], v[206:209], v[174:177], v[54:57]
	v_mfma_f32_16x16x32_bf16 v[50:53], v[214:217], v[174:177], v[50:53]
	v_mfma_f32_16x16x32_bf16 v[38:41], v[206:209], v[182:185], v[38:41]
	v_mfma_f32_16x16x32_bf16 v[34:37], v[214:217], v[182:185], v[34:37]
	v_mfma_f32_16x16x32_bf16 v[22:25], v[206:209], v[190:193], v[22:25]
	v_mfma_f32_16x16x32_bf16 v[18:21], v[214:217], v[190:193], v[18:21]
	v_mfma_f32_16x16x32_bf16 v[6:9], v[206:209], v[198:201], v[6:9]
	v_mfma_f32_16x16x32_bf16 v[2:5], v[214:217], v[198:201], v[2:5]
	s_setprio 0
	s_add_i32 s59, s59, 2
	s_add_u32 s13, s13, 0x100
	s_addc_u32 s58, s58, 0
	s_cmp_gt_u32 s59, 29
	s_mov_b64 s[20:21], s[22:23]
	s_barrier
	s_cbranch_scc0 .LBB0_299
	s_ashr_i32 s24, s57, 2
	s_cmp_lt_i32 s24, 6
	v_mbcnt_lo_u32_b32 v130, -1, 0
	v_mbcnt_hi_u32_b32 v130, -1, v130
	s_cbranch_scc1 .LBB0_302
	s_cmp_lg_u32 s24, 6
	s_cselect_b64 s[20:21], -1, 0
	s_cbranch_execz .LBB0_303
	s_branch .LBB0_304

; #define PG8_STAGE(bufoff, gbase, voff) do { _Pragma("unroll") for (int _i = 0; _i < 2; ++_i) glds16_s((const void*)((const char*)(gbase) + _i * r64), (voff), ldsb + (unsigned)(bufoff) + ldsw + _i * 8192u); } while (0)
; #define PG8_LDA(b, h) do { _Pragma("unroll") for (int m = 0; m < 4; ++m) { const int o_ = PG8_SA(b, h) + aoff + m * 2048; \
;         if constexpr (FP8) A8[m] = PG8_CAT8(o_); else { At[m][0] = PG8_LD16(o_); At[m][1] = PG8_LD16(o_ + 1024); } } } while (0)
; #define PG8_LDB(X, X8, b, h) do { _Pragma("unroll") for (int n = 0; n < 2; ++n) { const int o_ = PG8_SB(b, h) + boff + n * 2048; \
;         if constexpr (FP8) X8[n] = PG8_CAT8(o_); else { X[n][0] = PG8_LD16(o_); X[n][1] = PG8_LD16(o_ + 1024); } } } while (0)
; #define PG8_WAIT_L(n) asm volatile("s_waitcnt lgkmcnt(" #n ")" ::: "memory")
; #define PG8_BAR __builtin_amdgcn_s_barrier()
; #define PG8_SCHED __builtin_amdgcn_sched_barrier(0)
; #define PG8_HI do { if constexpr (FP8) asm volatile("s_setprio 1"); } while (0)
; #define PG8_LO do { if constexpr (FP8) asm volatile("s_setprio 0"); } while (0)
; template <class Epi, class Sched, bool FP8 = false>
; __device__ __forceinline__ void gemm_phase(LAS unsigned char* lds, const int Kb, const int nt  , const Sched& S, const Epi& E) {
;     ...
;         for (int t = 0; t < nt; t += 2) {
;             const bool last = (t == nt - 2);
;             const char* a1 = cA + (size_t)(t + 1) * kstep;
;             const char* a2 = last ? nA : cA + (size_t)(t + 2) * kstep; const char* b2 = last ? nB : cB + (size_t)(t + 2) * kstep;
;             const char* a3 = a2 + kstep; const char* b3 = b2 + kstep;
;             PG8_LDB(B0, B08, 0, 0); PG8_SCHED; PG8_LDA(0, 0); PG8_STAGE(PG8_SA(1, 1), a1 + hstep, voffA);
;             PG8_WAIT_L(8); PG8_BAR; PG8_HI; PG8_WAIT_L(0); PG8_MMA(0, 0, B0, B08); PG8_BAR; PG8_LO; PG8_SCHED;
;             PG8_LDB(B1, B18, 0, 1); PG8_STAGE(PG8_SB(0, 0), b2, voffB);
;             PG8_BAR; PG8_HI; PG8_WAIT_L(0); PG8_MMA(0, 1, B1, B18); PG8_BAR; PG8_LO;
;             PG8_LDA(0, 1); PG8_STAGE(PG8_SA(0, 0), a2, voffA);
;             PG8_BAR; PG8_HI; PG8_WAIT_L(0); PG8_MMA(1, 0, B0, B08); PG8_BAR; PG8_LO; PG8_SCHED;
.LBB0_1715:
	ds_read_b128 v[130:133], v138
	ds_read_b128 v[134:137], v139
	ds_read_b128 v[156:159], v140
	ds_read_b128 v[160:163], v141
	s_add_u32 s24, s22, 0xfff80080
	s_addc_u32 s25, s23, -1
	s_cmp_eq_u32 s57, 28
	s_cselect_b32 s26, s18, s24
	s_cselect_b32 s27, s19, s25
	s_cselect_b32 s24, s20, s3
	s_cselect_b32 s25, s21, s17
	s_add_u32 s28, s26, 0x80
	s_addc_u32 s29, s27, 0
	ds_read_b128 v[164:167], v154
	ds_read_b128 v[168:171], v154 offset:1024
	ds_read_b128 v[172:175], v154 offset:2048
	ds_read_b128 v[176:179], v154 offset:3072
	ds_read_b128 v[180:183], v154 offset:4096
	ds_read_b128 v[184:187], v154 offset:5120
	ds_read_b128 v[194:197], v154 offset:6144
	ds_read_b128 v[198:201], v154 offset:7168
	s_mov_b32 s58, m0
	s_mov_b32 m0, s53
	s_nop 0
	global_load_lds_dwordx4 v1, s[22:23]
	s_mov_b32 m0, s58
	s_add_u32 s58, s22, 0x40000
	s_addc_u32 s59, s23, 0
	s_mov_b32 s60, m0
	s_mov_b32 m0, s54
	s_nop 0
	global_load_lds_dwordx4 v1, s[58:59]
	s_mov_b32 m0, s60
	s_waitcnt lgkmcnt(8)
	s_barrier
	s_waitcnt lgkmcnt(0)
	s_setprio 1
	v_mfma_f32_16x16x32_bf16 v[126:129], v[130:133], v[164:167], v[126:129]
	v_mfma_f32_16x16x32_bf16 v[122:125], v[156:159], v[164:167], v[122:125]
	v_mfma_f32_16x16x32_bf16 v[110:113], v[130:133], v[172:175], v[110:113]
	v_mfma_f32_16x16x32_bf16 v[106:109], v[156:159], v[172:175], v[106:109]
	v_mfma_f32_16x16x32_bf16 v[94:97], v[130:133], v[180:183], v[94:97]
	v_mfma_f32_16x16x32_bf16 v[90:93], v[156:159], v[180:183], v[90:93]
	v_mfma_f32_16x16x32_bf16 v[78:81], v[130:133], v[194:197], v[78:81]
	v_mfma_f32_16x16x32_bf16 v[74:77], v[156:159], v[194:197], v[74:77]
	v_mfma_f32_16x16x32_bf16 v[126:129], v[134:137], v[168:171], v[126:129]
	v_mfma_f32_16x16x32_bf16 v[122:125], v[160:163], v[168:171], v[122:125]
	v_mfma_f32_16x16x32_bf16 v[110:113], v[134:137], v[176:179], v[110:113]
	v_mfma_f32_16x16x32_bf16 v[106:109], v[160:163], v[176:179], v[106:109]
	v_mfma_f32_16x16x32_bf16 v[94:97], v[134:137], v[184:187], v[94:97]
	v_mfma_f32_16x16x32_bf16 v[90:93], v[160:163], v[184:187], v[90:93]
	v_mfma_f32_16x16x32_bf16 v[78:81], v[134:137], v[198:201], v[78:81]
	v_mfma_f32_16x16x32_bf16 v[74:77], v[160:163], v[198:201], v[74:77]
	s_setprio 0
	s_barrier
	ds_read_b128 v[202:205], v142
	ds_read_b128 v[206:209], v143
	ds_read_b128 v[210:213], v144
	ds_read_b128 v[214:217], v145
	s_mov_b32 s58, m0
	s_mov_b32 m0, s38
	s_nop 0
	global_load_lds_dwordx4 v1, s[24:25]
	s_mov_b32 m0, s58
	s_add_u32 s58, s24, 0x40000
	s_addc_u32 s59, s25, 0
	s_mov_b32 s60, m0
	s_mov_b32 m0, s39
	s_nop 0
	global_load_lds_dwordx4 v1, s[58:59]
	s_mov_b32 m0, s60
	s_barrier
	s_waitcnt lgkmcnt(0)
	s_setprio 1
	v_mfma_f32_16x16x32_bf16 v[118:121], v[202:205], v[164:167], v[118:121]
	v_mfma_f32_16x16x32_bf16 v[114:117], v[210:213], v[164:167], v[114:117]
	v_mfma_f32_16x16x32_bf16 v[102:105], v[202:205], v[172:175], v[102:105]
	v_mfma_f32_16x16x32_bf16 v[98:101], v[210:213], v[172:175], v[98:101]
	v_mfma_f32_16x16x32_bf16 v[86:89], v[202:205], v[180:183], v[86:89]
	v_mfma_f32_16x16x32_bf16 v[82:85], v[210:213], v[180:183], v[82:85]
	v_mfma_f32_16x16x32_bf16 v[70:73], v[202:205], v[194:197], v[70:73]
	v_mfma_f32_16x16x32_bf16 v[66:69], v[210:213], v[194:197], v[66:69]
	v_mfma_f32_16x16x32_bf16 v[118:121], v[206:209], v[168:171], v[118:121]
	v_mfma_f32_16x16x32_bf16 v[114:117], v[214:217], v[168:171], v[114:117]
	v_mfma_f32_16x16x32_bf16 v[102:105], v[206:209], v[176:179], v[102:105]
	v_mfma_f32_16x16x32_bf16 v[98:101], v[214:217], v[176:179], v[98:101]
	v_mfma_f32_16x16x32_bf16 v[86:89], v[206:209], v[184:187], v[86:89]
	v_mfma_f32_16x16x32_bf16 v[82:85], v[214:217], v[184:187], v[82:85]
	v_mfma_f32_16x16x32_bf16 v[70:73], v[206:209], v[198:201], v[70:73]
	v_mfma_f32_16x16x32_bf16 v[66:69], v[214:217], v[198:201], v[66:69]
	s_setprio 0
	s_barrier
	ds_read_b128 v[164:167], v154 offset:16384
	ds_read_b128 v[168:171], v154 offset:17408
	ds_read_b128 v[172:175], v154 offset:18432
	ds_read_b128 v[176:179], v154 offset:19456
	ds_read_b128 v[180:183], v154 offset:20480
	ds_read_b128 v[184:187], v154 offset:21504
	ds_read_b128 v[194:197], v154 offset:22528
	ds_read_b128 v[198:201], v154 offset:23552
	s_mov_b32 s58, m0
	s_mov_b32 m0, s37
	s_nop 0
	global_load_lds_dwordx4 v1, s[26:27]
	s_mov_b32 m0, s58
	s_add_u32 s58, s26, 0x40000
	s_addc_u32 s59, s27, 0
	s_mov_b32 s60, m0
	s_mov_b32 m0, s40
	s_nop 0
	global_load_lds_dwordx4 v1, s[58:59]
	s_mov_b32 m0, s60
	s_barrier
	s_waitcnt lgkmcnt(0)
	s_setprio 1
	v_mfma_f32_16x16x32_bf16 v[62:65], v[130:133], v[164:167], v[62:65]
	v_mfma_f32_16x16x32_bf16 v[58:61], v[156:159], v[164:167], v[58:61]
	v_mfma_f32_16x16x32_bf16 v[46:49], v[130:133], v[172:175], v[46:49]
	v_mfma_f32_16x16x32_bf16 v[42:45], v[156:159], v[172:175], v[42:45]
	v_mfma_f32_16x16x32_bf16 v[30:33], v[130:133], v[180:183], v[30:33]
	v_mfma_f32_16x16x32_bf16 v[26:29], v[156:159], v[180:183], v[26:29]
	v_mfma_f32_16x16x32_bf16 v[14:17], v[130:133], v[194:197], v[14:17]
	v_mfma_f32_16x16x32_bf16 v[10:13], v[156:159], v[194:197], v[10:13]
	v_mfma_f32_16x16x32_bf16 v[62:65], v[134:137], v[168:171], v[62:65]
	v_mfma_f32_16x16x32_bf16 v[58:61], v[160:163], v[168:171], v[58:61]
	v_mfma_f32_16x16x32_bf16 v[46:49], v[134:137], v[176:179], v[46:49]
	v_mfma_f32_16x16x32_bf16 v[42:45], v[160:163], v[176:179], v[42:45]
	v_mfma_f32_16x16x32_bf16 v[30:33], v[134:137], v[184:187], v[30:33]
	v_mfma_f32_16x16x32_bf16 v[26:29], v[160:163], v[184:187], v[26:29]
	v_mfma_f32_16x16x32_bf16 v[14:17], v[134:137], v[198:201], v[14:17]
	v_mfma_f32_16x16x32_bf16 v[10:13], v[160:163], v[198:201], v[10:13]
	s_setprio 0
	s_barrier
; #define PG8_STAGE(bufoff, gbase, voff) do { _Pragma("unroll") for (int _i = 0; _i < 2; ++_i) glds16_s((const void*)((const char*)(gbase) + _i * r64), (voff), ldsb + (unsigned)(bufoff) + ldsw + _i * 8192u); } while (0)
; #define PG8_LDA(b, h) do { _Pragma("unroll") for (int m = 0; m < 4; ++m) { const int o_ = PG8_SA(b, h) + aoff + m * 2048; \
;         if constexpr (FP8) A8[m] = PG8_CAT8(o_); else { At[m][0] = PG8_LD16(o_); At[m][1] = PG8_LD16(o_ + 1024); } } } while (0)
; #define PG8_LDB(X, X8, b, h) do { _Pragma("unroll") for (int n = 0; n < 2; ++n) { const int o_ = PG8_SB(b, h) + boff + n * 2048; \
;         if constexpr (FP8) X8[n] = PG8_CAT8(o_); else { X[n][0] = PG8_LD16(o_); X[n][1] = PG8_LD16(o_ + 1024); } } } while (0)
; #define PG8_WAIT_V(n) asm volatile("s_waitcnt vmcnt(" #n ")" ::: "memory")
; #define PG8_WAIT_L(n) asm volatile("s_waitcnt lgkmcnt(" #n ")" ::: "memory")
; #define PG8_BAR __builtin_amdgcn_s_barrier()
; #define PG8_SCHED __builtin_amdgcn_sched_barrier(0)
; #define PG8_HI do { if constexpr (FP8) asm volatile("s_setprio 1"); } while (0)
; #define PG8_LO do { if constexpr (FP8) asm volatile("s_setprio 0"); } while (0)
; template <class Epi, class Sched, bool FP8 = false>
; __device__ __forceinline__ void gemm_phase(LAS unsigned char* lds, const int Kb, const int nt  , const Sched& S, const Epi& E) {
;     ...
;             PG8_STAGE(PG8_SB(0, 1), b2 + hstep, voffB);
;             PG8_WAIT_V(6); PG8_BAR; PG8_HI; PG8_MMA(1, 1, B1, B18); PG8_BAR; PG8_LO;
;             PG8_LDB(B0, B08, 1, 0); PG8_SCHED; PG8_LDA(1, 0); PG8_STAGE(PG8_SA(0, 1), a2 + hstep, voffA);
;             PG8_WAIT_L(8); PG8_BAR; PG8_HI; PG8_WAIT_L(0); PG8_MMA(0, 0, B0, B08); PG8_BAR; PG8_LO; PG8_SCHED;
;             PG8_LDB(B1, B18, 1, 1); PG8_STAGE(PG8_SB(1, 0), b3, voffB);
;             PG8_BAR; PG8_HI; PG8_WAIT_L(0); PG8_MMA(0, 1, B1, B18); PG8_BAR; PG8_LO;
	s_add_u32 s58, s24, 0x80000
	s_addc_u32 s59, s25, 0
	s_mov_b32 s60, m0
	s_mov_b32 m0, s41
	s_nop 0
	global_load_lds_dwordx4 v1, s[58:59]
	s_mov_b32 m0, s60
	s_add_u32 s58, s24, 0xc0000
	s_addc_u32 s59, s25, 0
	s_mov_b32 s60, m0
	s_mov_b32 m0, s42
	s_nop 0
	global_load_lds_dwordx4 v1, s[58:59]
	s_mov_b32 m0, s60
	s_waitcnt vmcnt(6)
	s_barrier
	s_setprio 1
	v_mfma_f32_16x16x32_bf16 v[54:57], v[202:205], v[164:167], v[54:57]
	v_mfma_f32_16x16x32_bf16 v[50:53], v[210:213], v[164:167], v[50:53]
	v_mfma_f32_16x16x32_bf16 v[38:41], v[202:205], v[172:175], v[38:41]
	v_mfma_f32_16x16x32_bf16 v[34:37], v[210:213], v[172:175], v[34:37]
	v_mfma_f32_16x16x32_bf16 v[22:25], v[202:205], v[180:183], v[22:25]
	v_mfma_f32_16x16x32_bf16 v[18:21], v[210:213], v[180:183], v[18:21]
	v_mfma_f32_16x16x32_bf16 v[6:9], v[202:205], v[194:197], v[6:9]
	v_mfma_f32_16x16x32_bf16 v[2:5], v[210:213], v[194:197], v[2:5]
	v_mfma_f32_16x16x32_bf16 v[54:57], v[206:209], v[168:171], v[54:57]
	v_mfma_f32_16x16x32_bf16 v[50:53], v[214:217], v[168:171], v[50:53]
	v_mfma_f32_16x16x32_bf16 v[38:41], v[206:209], v[176:179], v[38:41]
	v_mfma_f32_16x16x32_bf16 v[34:37], v[214:217], v[176:179], v[34:37]
	v_mfma_f32_16x16x32_bf16 v[22:25], v[206:209], v[184:187], v[22:25]
	v_mfma_f32_16x16x32_bf16 v[18:21], v[214:217], v[184:187], v[18:21]
	v_mfma_f32_16x16x32_bf16 v[6:9], v[206:209], v[198:201], v[6:9]
	v_mfma_f32_16x16x32_bf16 v[2:5], v[214:217], v[198:201], v[2:5]
	s_setprio 0
	s_barrier
	ds_read_b128 v[130:133], v146
	ds_read_b128 v[134:137], v147
	ds_read_b128 v[156:159], v148
	ds_read_b128 v[160:163], v149
	ds_read_b128 v[164:167], v154 offset:32768
	ds_read_b128 v[168:171], v154 offset:33792
	ds_read_b128 v[172:175], v154 offset:34816
	ds_read_b128 v[176:179], v154 offset:35840
	ds_read_b128 v[180:183], v154 offset:36864
	ds_read_b128 v[184:187], v154 offset:37888
	ds_read_b128 v[194:197], v154 offset:38912
	ds_read_b128 v[198:201], v154 offset:39936
	s_add_u32 s58, s26, 0x80000
	s_addc_u32 s59, s27, 0
	s_mov_b32 s60, m0
	s_mov_b32 m0, s43
	s_nop 0
	global_load_lds_dwordx4 v1, s[58:59]
	s_mov_b32 m0, s60
	s_add_u32 s58, s26, 0xc0000
	s_addc_u32 s59, s27, 0
	s_mov_b32 s60, m0
	s_mov_b32 m0, s44
	s_nop 0
	global_load_lds_dwordx4 v1, s[58:59]
	s_mov_b32 m0, s60
	s_waitcnt lgkmcnt(8)
	s_barrier
	s_waitcnt lgkmcnt(0)
	s_setprio 1
	v_mfma_f32_16x16x32_bf16 v[126:129], v[130:133], v[164:167], v[126:129]
	v_mfma_f32_16x16x32_bf16 v[122:125], v[156:159], v[164:167], v[122:125]
	v_mfma_f32_16x16x32_bf16 v[110:113], v[130:133], v[172:175], v[110:113]
	v_mfma_f32_16x16x32_bf16 v[106:109], v[156:159], v[172:175], v[106:109]
	v_mfma_f32_16x16x32_bf16 v[94:97], v[130:133], v[180:183], v[94:97]
	v_mfma_f32_16x16x32_bf16 v[90:93], v[156:159], v[180:183], v[90:93]
	v_mfma_f32_16x16x32_bf16 v[78:81], v[130:133], v[194:197], v[78:81]
	v_mfma_f32_16x16x32_bf16 v[74:77], v[156:159], v[194:197], v[74:77]
	v_mfma_f32_16x16x32_bf16 v[126:129], v[134:137], v[168:171], v[126:129]
	v_mfma_f32_16x16x32_bf16 v[122:125], v[160:163], v[168:171], v[122:125]
	v_mfma_f32_16x16x32_bf16 v[110:113], v[134:137], v[176:179], v[110:113]
	v_mfma_f32_16x16x32_bf16 v[106:109], v[160:163], v[176:179], v[106:109]
	v_mfma_f32_16x16x32_bf16 v[94:97], v[134:137], v[184:187], v[94:97]
	v_mfma_f32_16x16x32_bf16 v[90:93], v[160:163], v[184:187], v[90:93]
	v_mfma_f32_16x16x32_bf16 v[78:81], v[134:137], v[198:201], v[78:81]
	v_mfma_f32_16x16x32_bf16 v[74:77], v[160:163], v[198:201], v[74:77]
	s_setprio 0
	s_barrier
	ds_read_b128 v[202:205], v150
	ds_read_b128 v[206:209], v151
	ds_read_b128 v[210:213], v152
	ds_read_b128 v[214:217], v153
	s_add_u32 s58, s24, 0x80
	s_addc_u32 s59, s25, 0
	s_mov_b32 s60, m0
	s_mov_b32 m0, s47
	s_nop 0
	global_load_lds_dwordx4 v1, s[58:59]
	s_mov_b32 m0, s60
	s_add_u32 s58, s24, 0x40080
	s_addc_u32 s59, s25, 0
	s_mov_b32 s60, m0
	s_mov_b32 m0, s48
	s_nop 0
	global_load_lds_dwordx4 v1, s[58:59]
	s_mov_b32 m0, s60
	s_barrier
	s_waitcnt lgkmcnt(0)
	s_setprio 1
	v_mfma_f32_16x16x32_bf16 v[118:121], v[202:205], v[164:167], v[118:121]
	v_mfma_f32_16x16x32_bf16 v[114:117], v[210:213], v[164:167], v[114:117]
	v_mfma_f32_16x16x32_bf16 v[102:105], v[202:205], v[172:175], v[102:105]
	v_mfma_f32_16x16x32_bf16 v[98:101], v[210:213], v[172:175], v[98:101]
	v_mfma_f32_16x16x32_bf16 v[86:89], v[202:205], v[180:183], v[86:89]
	v_mfma_f32_16x16x32_bf16 v[82:85], v[210:213], v[180:183], v[82:85]
	v_mfma_f32_16x16x32_bf16 v[70:73], v[202:205], v[194:197], v[70:73]
	v_mfma_f32_16x16x32_bf16 v[66:69], v[210:213], v[194:197], v[66:69]
	v_mfma_f32_16x16x32_bf16 v[118:121], v[206:209], v[168:171], v[118:121]
	v_mfma_f32_16x16x32_bf16 v[114:117], v[214:217], v[168:171], v[114:117]
	v_mfma_f32_16x16x32_bf16 v[102:105], v[206:209], v[176:179], v[102:105]
	v_mfma_f32_16x16x32_bf16 v[98:101], v[214:217], v[176:179], v[98:101]
	v_mfma_f32_16x16x32_bf16 v[86:89], v[206:209], v[184:187], v[86:89]
	v_mfma_f32_16x16x32_bf16 v[82:85], v[214:217], v[184:187], v[82:85]
	v_mfma_f32_16x16x32_bf16 v[70:73], v[206:209], v[198:201], v[70:73]
	v_mfma_f32_16x16x32_bf16 v[66:69], v[214:217], v[198:201], v[66:69]
	s_setprio 0
	s_barrier
; #define PG8_STAGE(bufoff, gbase, voff) do { _Pragma("unroll") for (int _i = 0; _i < 2; ++_i) glds16_s((const void*)((const char*)(gbase) + _i * r64), (voff), ldsb + (unsigned)(bufoff) + ldsw + _i * 8192u); } while (0)
; #define PG8_LDA(b, h) do { _Pragma("unroll") for (int m = 0; m < 4; ++m) { const int o_ = PG8_SA(b, h) + aoff + m * 2048; \
;         if constexpr (FP8) A8[m] = PG8_CAT8(o_); else { At[m][0] = PG8_LD16(o_); At[m][1] = PG8_LD16(o_ + 1024); } } } while (0)
; #define PG8_WAIT_V(n) asm volatile("s_waitcnt vmcnt(" #n ")" ::: "memory")
; #define PG8_WAIT_L(n) asm volatile("s_waitcnt lgkmcnt(" #n ")" ::: "memory")
; #define PG8_BAR __builtin_amdgcn_s_barrier()
; #define PG8_SCHED __builtin_amdgcn_sched_barrier(0)
; #define PG8_HI do { if constexpr (FP8) asm volatile("s_setprio 1"); } while (0)
; #define PG8_LO do { if constexpr (FP8) asm volatile("s_setprio 0"); } while (0)
;     __device__ __forceinline__ void operator()(const f32x4 (&acc)[2][2][4][2], const Unit& u, int wr, int wc, int fr, int fq) const {
;     ...
;             for (int n = 0; n < 2; ++n) cs[bj][n] = (cscale ? *(const f32x4*)(cscale + col0 + bj * HALF + n * 16) : (f32x4){1.f, 1.f, 1.f, 1.f}) * ascale;
; #pragma unroll
;         for (int ai = 0; ai < 2; ++ai)
; #pragma unroll
;             for (int m = 0; m < 4; ++m) { const size_t off = (size_t)(row0 + ai * HALF + m * 16) * ldc + col0;
; #pragma unroll
;                 for (int bj = 0; bj < 2; ++bj)
; #pragma unroll
;                     for (int n = 0; n < 2; ++n) { f32x4 v = acc[ai][bj][m][n] * cs[bj][n];
;                         if (res) v += *(const f32x4*)(res + off + bj * HALF + n * 16);
; template <class Epi, class Sched, bool FP8 = false>
; __device__ __forceinline__ void gemm_phase(LAS unsigned char* lds, const int Kb, const int nt  , const Sched& S, const Epi& E) {
;     ...
;             PG8_LDA(1, 1); PG8_STAGE(PG8_SA(1, 0), a3, voffA);
;             PG8_BAR; PG8_HI; PG8_WAIT_L(0); PG8_MMA(1, 0, B0, B08); PG8_BAR; PG8_LO; PG8_SCHED;
;             PG8_STAGE(PG8_SB(1, 1), b3 + hstep, voffB);
;             PG8_WAIT_V(6); PG8_BAR; PG8_HI; PG8_MMA(1, 1, B1, B18); PG8_BAR; PG8_LO;
;         }
;         { int l_; asm volatile("v_mbcnt_lo_u32_b32 %0, -1, 0\n\tv_mbcnt_hi_u32_b32 %0, -1, %0" : "=v"(l_));
;           E(acc, cur, wr, wc, l_ & 15, l_ >> 4); }
	ds_read_b128 v[164:167], v154 offset:49152
	ds_read_b128 v[168:171], v154 offset:50176
	ds_read_b128 v[172:175], v154 offset:51200
	ds_read_b128 v[176:179], v154 offset:52224
	ds_read_b128 v[180:183], v154 offset:53248
	ds_read_b128 v[184:187], v154 offset:54272
	ds_read_b128 v[194:197], v154 offset:55296
	ds_read_b128 v[198:201], v154 offset:56320
	s_mov_b32 s58, m0
	s_mov_b32 m0, s49
	s_nop 0
	global_load_lds_dwordx4 v1, s[28:29]
	s_mov_b32 m0, s58
	s_add_u32 s26, s26, 0x40080
	s_addc_u32 s27, s27, 0
	s_mov_b32 s28, m0
	s_mov_b32 m0, s50
	s_nop 0
	global_load_lds_dwordx4 v1, s[26:27]
	s_mov_b32 m0, s28
	s_barrier
	s_waitcnt lgkmcnt(0)
	s_setprio 1
	v_mfma_f32_16x16x32_bf16 v[62:65], v[130:133], v[164:167], v[62:65]
	v_mfma_f32_16x16x32_bf16 v[58:61], v[156:159], v[164:167], v[58:61]
	v_mfma_f32_16x16x32_bf16 v[46:49], v[130:133], v[172:175], v[46:49]
	v_mfma_f32_16x16x32_bf16 v[42:45], v[156:159], v[172:175], v[42:45]
	v_mfma_f32_16x16x32_bf16 v[30:33], v[130:133], v[180:183], v[30:33]
	v_mfma_f32_16x16x32_bf16 v[26:29], v[156:159], v[180:183], v[26:29]
	v_mfma_f32_16x16x32_bf16 v[14:17], v[130:133], v[194:197], v[14:17]
	v_mfma_f32_16x16x32_bf16 v[10:13], v[156:159], v[194:197], v[10:13]
	v_mfma_f32_16x16x32_bf16 v[62:65], v[134:137], v[168:171], v[62:65]
	v_mfma_f32_16x16x32_bf16 v[58:61], v[160:163], v[168:171], v[58:61]
	v_mfma_f32_16x16x32_bf16 v[46:49], v[134:137], v[176:179], v[46:49]
	v_mfma_f32_16x16x32_bf16 v[42:45], v[160:163], v[176:179], v[42:45]
	v_mfma_f32_16x16x32_bf16 v[30:33], v[134:137], v[184:187], v[30:33]
	v_mfma_f32_16x16x32_bf16 v[26:29], v[160:163], v[184:187], v[26:29]
	v_mfma_f32_16x16x32_bf16 v[14:17], v[134:137], v[198:201], v[14:17]
	v_mfma_f32_16x16x32_bf16 v[10:13], v[160:163], v[198:201], v[10:13]
	s_setprio 0
	s_barrier
	s_add_u32 s26, s24, 0x80080
	s_addc_u32 s27, s25, 0
	s_mov_b32 s28, m0
	s_mov_b32 m0, s51
	s_nop 0
	global_load_lds_dwordx4 v1, s[26:27]
	s_mov_b32 m0, s28
	s_add_u32 s24, s24, 0xc0080
	s_addc_u32 s25, s25, 0
	s_mov_b32 s26, m0
	s_mov_b32 m0, s52
	s_nop 0
	global_load_lds_dwordx4 v1, s[24:25]
	s_mov_b32 m0, s26
	s_waitcnt vmcnt(6)
	s_barrier
	s_setprio 1
	v_mfma_f32_16x16x32_bf16 v[54:57], v[202:205], v[164:167], v[54:57]
	v_mfma_f32_16x16x32_bf16 v[50:53], v[210:213], v[164:167], v[50:53]
	v_mfma_f32_16x16x32_bf16 v[38:41], v[202:205], v[172:175], v[38:41]
	v_mfma_f32_16x16x32_bf16 v[34:37], v[210:213], v[172:175], v[34:37]
	v_mfma_f32_16x16x32_bf16 v[22:25], v[202:205], v[180:183], v[22:25]
	v_mfma_f32_16x16x32_bf16 v[18:21], v[210:213], v[180:183], v[18:21]
	v_mfma_f32_16x16x32_bf16 v[6:9], v[202:205], v[194:197], v[6:9]
	v_mfma_f32_16x16x32_bf16 v[2:5], v[210:213], v[194:197], v[2:5]
	v_mfma_f32_16x16x32_bf16 v[54:57], v[206:209], v[168:171], v[54:57]
	v_mfma_f32_16x16x32_bf16 v[50:53], v[214:217], v[168:171], v[50:53]
	v_mfma_f32_16x16x32_bf16 v[38:41], v[206:209], v[176:179], v[38:41]
	v_mfma_f32_16x16x32_bf16 v[34:37], v[214:217], v[176:179], v[34:37]
	v_mfma_f32_16x16x32_bf16 v[22:25], v[206:209], v[184:187], v[22:25]
	v_mfma_f32_16x16x32_bf16 v[18:21], v[214:217], v[184:187], v[18:21]
	v_mfma_f32_16x16x32_bf16 v[6:9], v[206:209], v[198:201], v[6:9]
	v_mfma_f32_16x16x32_bf16 v[2:5], v[214:217], v[198:201], v[2:5]
	s_setprio 0
	s_add_i32 s57, s57, 2
	s_add_u32 s22, s22, 0x100
	s_addc_u32 s23, s23, 0
	s_add_u32 s3, s3, 0x100
	s_addc_u32 s17, s17, 0
	s_cmp_gt_u32 s57, 29
	s_barrier
	s_cbranch_scc0 .LBB0_1715
	s_lshl_b32 s2, s2, 8
	v_mbcnt_lo_u32_b32 v132, -1, 0
	v_mbcnt_hi_u32_b32 v132, -1, v132
	s_add_i32 s2, s2, s45
	s_lshl_b32 s3, s56, 8
	v_ashrrev_i32_e32 v130, 2, v132
	s_or_b32 s3, s3, s46
	v_and_b32_e32 v130, -4, v130
	v_and_or_b32 v132, v132, 15, s2
	v_add_u32_e32 v130, s3, v130
	v_ashrrev_i32_e32 v133, 31, v132
	v_ashrrev_i32_e32 v131, 31, v130
	v_lshlrev_b64 v[134:135], 11, v[132:133]
	v_lshl_add_u64 v[136:137], v[134:135], 0, v[130:131]
	v_cndmask_b32_e64 v134, 0, 1, s[6:7]
	v_cmp_ne_u32_e64 s[2:3], 1, v134
	s_andn2_b64 vcc, exec, s[6:7]
	v_lshl_add_u64 v[134:135], v[136:137], 2, s[76:77]
	s_cbranch_vccnz .LBB0_1718
	global_load_dwordx4 v[156:159], v[134:135], off
	s_waitcnt vmcnt(0)
	v_pk_add_f32 v[128:129], v[128:129], v[158:159]
	v_pk_add_f32 v[126:127], v[126:127], v[156:157]

; #define PG8_STAGE(bufoff, gbase, voff) do { _Pragma("unroll") for (int _i = 0; _i < 2; ++_i) glds16_s((const void*)((const char*)(gbase) + _i * r64), (voff), ldsb + (unsigned)(bufoff) + ldsw + _i * 8192u); } while (0)
; #define PG8_LDA(b, h) do { _Pragma("unroll") for (int m = 0; m < 4; ++m) { const int o_ = PG8_SA(b, h) + aoff + m * 2048; \
;         if constexpr (FP8) A8[m] = PG8_CAT8(o_); else { At[m][0] = PG8_LD16(o_); At[m][1] = PG8_LD16(o_ + 1024); } } } while (0)
; #define PG8_LDB(X, X8, b, h) do { _Pragma("unroll") for (int n = 0; n < 2; ++n) { const int o_ = PG8_SB(b, h) + boff + n * 2048; \
;         if constexpr (FP8) X8[n] = PG8_CAT8(o_); else { X[n][0] = PG8_LD16(o_); X[n][1] = PG8_LD16(o_ + 1024); } } } while (0)
; #define PG8_WAIT_L(n) asm volatile("s_waitcnt lgkmcnt(" #n ")" ::: "memory")
; #define PG8_BAR __builtin_amdgcn_s_barrier()
; #define PG8_SCHED __builtin_amdgcn_sched_barrier(0)
; #define PG8_HI do { if constexpr (FP8) asm volatile("s_setprio 1"); } while (0)
; #define PG8_LO do { if constexpr (FP8) asm volatile("s_setprio 0"); } while (0)
; template <class Epi, class Sched, bool FP8 = false>
; __device__ __forceinline__ void gemm_phase(LAS unsigned char* lds, const int Kb, const int nt  , const Sched& S, const Epi& E) {
;     ...
;         for (int t = 0; t < nt; t += 2) {
;             const bool last = (t == nt - 2);
;             const char* a1 = cA + (size_t)(t + 1) * kstep;
;             const char* a2 = last ? nA : cA + (size_t)(t + 2) * kstep; const char* b2 = last ? nB : cB + (size_t)(t + 2) * kstep;
;             const char* a3 = a2 + kstep; const char* b3 = b2 + kstep;
;             PG8_LDB(B0, B08, 0, 0); PG8_SCHED; PG8_LDA(0, 0); PG8_STAGE(PG8_SA(1, 1), a1 + hstep, voffA);
;             PG8_WAIT_L(8); PG8_BAR; PG8_HI; PG8_WAIT_L(0); PG8_MMA(0, 0, B0, B08); PG8_BAR; PG8_LO; PG8_SCHED;
;             PG8_LDB(B1, B18, 0, 1); PG8_STAGE(PG8_SB(0, 0), b2, voffB);
;             PG8_BAR; PG8_HI; PG8_WAIT_L(0); PG8_MMA(0, 1, B1, B18); PG8_BAR; PG8_LO;
;             PG8_LDA(0, 1); PG8_STAGE(PG8_SA(0, 0), a2, voffA);
;             PG8_BAR; PG8_HI; PG8_WAIT_L(0); PG8_MMA(1, 0, B0, B08); PG8_BAR; PG8_LO; PG8_SCHED;
.LBB0_1946:
	ds_read_b128 v[150:153], v133
	ds_read_b128 v[154:157], v134
	ds_read_b128 v[158:161], v135
	ds_read_b128 v[162:165], v136
	s_add_u32 s16, s14, 0x100
	s_addc_u32 s17, s15, 0
	s_cmp_eq_u32 s53, 28
	s_cselect_b32 s20, s8, s16
	s_cselect_b32 s21, s9, s17
	s_cselect_b32 s18, s10, s5
	s_cselect_b32 s19, s11, s52
	s_add_u32 s22, s20, 0x80
	s_addc_u32 s23, s21, 0
	ds_read_b128 v[166:169], v149
	ds_read_b128 v[170:173], v149 offset:1024
	ds_read_b128 v[174:177], v149 offset:2048
	ds_read_b128 v[178:181], v149 offset:3072
	ds_read_b128 v[182:185], v149 offset:4096
	ds_read_b128 v[186:189], v149 offset:5120
	ds_read_b128 v[194:197], v149 offset:6144
	ds_read_b128 v[198:201], v149 offset:7168
	s_add_u32 s54, s14, 0x80080
	s_addc_u32 s55, s15, 0
	s_mov_b32 s56, m0
	s_mov_b32 m0, s47
	s_nop 0
	global_load_lds_dwordx4 v1, s[54:55]
	s_mov_b32 m0, s56
	s_add_u32 s14, s14, 0xc0080
	s_addc_u32 s15, s15, 0
	s_mov_b32 s54, m0
	s_mov_b32 m0, s48
	s_nop 0
	global_load_lds_dwordx4 v1, s[14:15]
	s_mov_b32 m0, s54
	s_waitcnt lgkmcnt(8)
	s_barrier
	s_waitcnt lgkmcnt(0)
	s_setprio 1
	v_mfma_f32_16x16x32_bf16 v[126:129], v[150:153], v[166:169], v[126:129]
	v_mfma_f32_16x16x32_bf16 v[122:125], v[158:161], v[166:169], v[122:125]
	v_mfma_f32_16x16x32_bf16 v[110:113], v[150:153], v[174:177], v[110:113]
	v_mfma_f32_16x16x32_bf16 v[106:109], v[158:161], v[174:177], v[106:109]
	v_mfma_f32_16x16x32_bf16 v[94:97], v[150:153], v[182:185], v[94:97]
	v_mfma_f32_16x16x32_bf16 v[90:93], v[158:161], v[182:185], v[90:93]
	v_mfma_f32_16x16x32_bf16 v[78:81], v[150:153], v[194:197], v[78:81]
	v_mfma_f32_16x16x32_bf16 v[74:77], v[158:161], v[194:197], v[74:77]
	v_mfma_f32_16x16x32_bf16 v[126:129], v[154:157], v[170:173], v[126:129]
	v_mfma_f32_16x16x32_bf16 v[122:125], v[162:165], v[170:173], v[122:125]
	v_mfma_f32_16x16x32_bf16 v[110:113], v[154:157], v[178:181], v[110:113]
	v_mfma_f32_16x16x32_bf16 v[106:109], v[162:165], v[178:181], v[106:109]
	v_mfma_f32_16x16x32_bf16 v[94:97], v[154:157], v[186:189], v[94:97]
	v_mfma_f32_16x16x32_bf16 v[90:93], v[162:165], v[186:189], v[90:93]
	v_mfma_f32_16x16x32_bf16 v[78:81], v[154:157], v[198:201], v[78:81]
	v_mfma_f32_16x16x32_bf16 v[74:77], v[162:165], v[198:201], v[74:77]
	s_setprio 0
	s_barrier
	ds_read_b128 v[202:205], v137
	ds_read_b128 v[206:209], v138
	ds_read_b128 v[210:213], v139
	ds_read_b128 v[214:217], v140
	s_mov_b32 s14, m0
	s_mov_b32 m0, s31
	s_nop 0
	global_load_lds_dwordx4 v132, s[18:19]
	s_mov_b32 m0, s14
	s_add_u32 s14, s18, 0x40000
	s_addc_u32 s15, s19, 0
	s_mov_b32 s54, m0
	s_mov_b32 m0, s33
	s_nop 0
	global_load_lds_dwordx4 v132, s[14:15]
	s_mov_b32 m0, s54
	s_barrier
	s_waitcnt lgkmcnt(0)
	s_setprio 1
	v_mfma_f32_16x16x32_bf16 v[118:121], v[202:205], v[166:169], v[118:121]
	v_mfma_f32_16x16x32_bf16 v[114:117], v[210:213], v[166:169], v[114:117]
	v_mfma_f32_16x16x32_bf16 v[102:105], v[202:205], v[174:177], v[102:105]
	v_mfma_f32_16x16x32_bf16 v[98:101], v[210:213], v[174:177], v[98:101]
	v_mfma_f32_16x16x32_bf16 v[86:89], v[202:205], v[182:185], v[86:89]
	v_mfma_f32_16x16x32_bf16 v[82:85], v[210:213], v[182:185], v[82:85]
	v_mfma_f32_16x16x32_bf16 v[70:73], v[202:205], v[194:197], v[70:73]
	v_mfma_f32_16x16x32_bf16 v[66:69], v[210:213], v[194:197], v[66:69]
	v_mfma_f32_16x16x32_bf16 v[118:121], v[206:209], v[170:173], v[118:121]
	v_mfma_f32_16x16x32_bf16 v[114:117], v[214:217], v[170:173], v[114:117]
	v_mfma_f32_16x16x32_bf16 v[102:105], v[206:209], v[178:181], v[102:105]
	v_mfma_f32_16x16x32_bf16 v[98:101], v[214:217], v[178:181], v[98:101]
	v_mfma_f32_16x16x32_bf16 v[86:89], v[206:209], v[186:189], v[86:89]
	v_mfma_f32_16x16x32_bf16 v[82:85], v[214:217], v[186:189], v[82:85]
	v_mfma_f32_16x16x32_bf16 v[70:73], v[206:209], v[198:201], v[70:73]
	v_mfma_f32_16x16x32_bf16 v[66:69], v[214:217], v[198:201], v[66:69]
	s_setprio 0
	s_barrier
	ds_read_b128 v[166:169], v149 offset:16384
	ds_read_b128 v[170:173], v149 offset:17408
	ds_read_b128 v[174:177], v149 offset:18432
	ds_read_b128 v[178:181], v149 offset:19456
	ds_read_b128 v[182:185], v149 offset:20480
	ds_read_b128 v[186:189], v149 offset:21504
	ds_read_b128 v[194:197], v149 offset:22528
	ds_read_b128 v[198:201], v149 offset:23552
	s_mov_b32 s14, m0
	s_mov_b32 m0, s13
	s_nop 0
	global_load_lds_dwordx4 v1, s[20:21]
	s_mov_b32 m0, s14
	s_add_u32 s14, s20, 0x40000
	s_addc_u32 s15, s21, 0
	s_mov_b32 s54, m0
	s_mov_b32 m0, s34
	s_nop 0
	global_load_lds_dwordx4 v1, s[14:15]
	s_mov_b32 m0, s54
	s_barrier
	s_waitcnt lgkmcnt(0)
	s_setprio 1
	v_mfma_f32_16x16x32_bf16 v[62:65], v[150:153], v[166:169], v[62:65]
	v_mfma_f32_16x16x32_bf16 v[58:61], v[158:161], v[166:169], v[58:61]
	v_mfma_f32_16x16x32_bf16 v[46:49], v[150:153], v[174:177], v[46:49]
	v_mfma_f32_16x16x32_bf16 v[42:45], v[158:161], v[174:177], v[42:45]
	v_mfma_f32_16x16x32_bf16 v[30:33], v[150:153], v[182:185], v[30:33]
	v_mfma_f32_16x16x32_bf16 v[26:29], v[158:161], v[182:185], v[26:29]
	v_mfma_f32_16x16x32_bf16 v[14:17], v[150:153], v[194:197], v[14:17]
	v_mfma_f32_16x16x32_bf16 v[10:13], v[158:161], v[194:197], v[10:13]
	v_mfma_f32_16x16x32_bf16 v[62:65], v[154:157], v[170:173], v[62:65]
	v_mfma_f32_16x16x32_bf16 v[58:61], v[162:165], v[170:173], v[58:61]
	v_mfma_f32_16x16x32_bf16 v[46:49], v[154:157], v[178:181], v[46:49]
	v_mfma_f32_16x16x32_bf16 v[42:45], v[162:165], v[178:181], v[42:45]
	v_mfma_f32_16x16x32_bf16 v[30:33], v[154:157], v[186:189], v[30:33]
	v_mfma_f32_16x16x32_bf16 v[26:29], v[162:165], v[186:189], v[26:29]
	v_mfma_f32_16x16x32_bf16 v[14:17], v[154:157], v[198:201], v[14:17]
	v_mfma_f32_16x16x32_bf16 v[10:13], v[162:165], v[198:201], v[10:13]
	s_setprio 0
	s_barrier
; #define PG8_STAGE(bufoff, gbase, voff) do { _Pragma("unroll") for (int _i = 0; _i < 2; ++_i) glds16_s((const void*)((const char*)(gbase) + _i * r64), (voff), ldsb + (unsigned)(bufoff) + ldsw + _i * 8192u); } while (0)
; #define PG8_LDA(b, h) do { _Pragma("unroll") for (int m = 0; m < 4; ++m) { const int o_ = PG8_SA(b, h) + aoff + m * 2048; \
;         if constexpr (FP8) A8[m] = PG8_CAT8(o_); else { At[m][0] = PG8_LD16(o_); At[m][1] = PG8_LD16(o_ + 1024); } } } while (0)
; #define PG8_LDB(X, X8, b, h) do { _Pragma("unroll") for (int n = 0; n < 2; ++n) { const int o_ = PG8_SB(b, h) + boff + n * 2048; \
;         if constexpr (FP8) X8[n] = PG8_CAT8(o_); else { X[n][0] = PG8_LD16(o_); X[n][1] = PG8_LD16(o_ + 1024); } } } while (0)
; #define PG8_WAIT_V(n) asm volatile("s_waitcnt vmcnt(" #n ")" ::: "memory")
; #define PG8_WAIT_L(n) asm volatile("s_waitcnt lgkmcnt(" #n ")" ::: "memory")
; #define PG8_BAR __builtin_amdgcn_s_barrier()
; #define PG8_SCHED __builtin_amdgcn_sched_barrier(0)
; #define PG8_HI do { if constexpr (FP8) asm volatile("s_setprio 1"); } while (0)
; #define PG8_LO do { if constexpr (FP8) asm volatile("s_setprio 0"); } while (0)
; template <class Epi, class Sched, bool FP8 = false>
; __device__ __forceinline__ void gemm_phase(LAS unsigned char* lds, const int Kb, const int nt  , const Sched& S, const Epi& E) {
;     ...
;             PG8_STAGE(PG8_SB(0, 1), b2 + hstep, voffB);
;             PG8_WAIT_V(6); PG8_BAR; PG8_HI; PG8_MMA(1, 1, B1, B18); PG8_BAR; PG8_LO;
;             PG8_LDB(B0, B08, 1, 0); PG8_SCHED; PG8_LDA(1, 0); PG8_STAGE(PG8_SA(0, 1), a2 + hstep, voffA);
;             PG8_WAIT_L(8); PG8_BAR; PG8_HI; PG8_WAIT_L(0); PG8_MMA(0, 0, B0, B08); PG8_BAR; PG8_LO; PG8_SCHED;
;             PG8_LDB(B1, B18, 1, 1); PG8_STAGE(PG8_SB(1, 0), b3, voffB);
;             PG8_BAR; PG8_HI; PG8_WAIT_L(0); PG8_MMA(0, 1, B1, B18); PG8_BAR; PG8_LO;
;             PG8_LDA(1, 1); PG8_STAGE(PG8_SA(1, 0), a3, voffA);
	s_add_u32 s14, s18, 0x80000
	s_addc_u32 s15, s19, 0
	s_mov_b32 s54, m0
	s_mov_b32 m0, s35
	s_nop 0
	global_load_lds_dwordx4 v132, s[14:15]
	s_mov_b32 m0, s54
	s_add_u32 s14, s18, 0xc0000
	s_addc_u32 s15, s19, 0
	s_mov_b32 s54, m0
	s_mov_b32 m0, s36
	s_nop 0
	global_load_lds_dwordx4 v132, s[14:15]
	s_mov_b32 m0, s54
	s_waitcnt vmcnt(6)
	s_barrier
	s_setprio 1
	v_mfma_f32_16x16x32_bf16 v[54:57], v[202:205], v[166:169], v[54:57]
	v_mfma_f32_16x16x32_bf16 v[50:53], v[210:213], v[166:169], v[50:53]
	v_mfma_f32_16x16x32_bf16 v[38:41], v[202:205], v[174:177], v[38:41]
	v_mfma_f32_16x16x32_bf16 v[34:37], v[210:213], v[174:177], v[34:37]
	v_mfma_f32_16x16x32_bf16 v[22:25], v[202:205], v[182:185], v[22:25]
	v_mfma_f32_16x16x32_bf16 v[18:21], v[210:213], v[182:185], v[18:21]
	v_mfma_f32_16x16x32_bf16 v[6:9], v[202:205], v[194:197], v[6:9]
	v_mfma_f32_16x16x32_bf16 v[2:5], v[210:213], v[194:197], v[2:5]
	v_mfma_f32_16x16x32_bf16 v[54:57], v[206:209], v[170:173], v[54:57]
	v_mfma_f32_16x16x32_bf16 v[50:53], v[214:217], v[170:173], v[50:53]
	v_mfma_f32_16x16x32_bf16 v[38:41], v[206:209], v[178:181], v[38:41]
	v_mfma_f32_16x16x32_bf16 v[34:37], v[214:217], v[178:181], v[34:37]
	v_mfma_f32_16x16x32_bf16 v[22:25], v[206:209], v[186:189], v[22:25]
	v_mfma_f32_16x16x32_bf16 v[18:21], v[214:217], v[186:189], v[18:21]
	v_mfma_f32_16x16x32_bf16 v[6:9], v[206:209], v[198:201], v[6:9]
	v_mfma_f32_16x16x32_bf16 v[2:5], v[214:217], v[198:201], v[2:5]
	s_setprio 0
	s_barrier
	ds_read_b128 v[150:153], v141
	ds_read_b128 v[154:157], v142
	ds_read_b128 v[158:161], v143
	ds_read_b128 v[162:165], v144
	ds_read_b128 v[166:169], v149 offset:32768
	ds_read_b128 v[170:173], v149 offset:33792
	ds_read_b128 v[174:177], v149 offset:34816
	ds_read_b128 v[178:181], v149 offset:35840
	ds_read_b128 v[182:185], v149 offset:36864
	ds_read_b128 v[186:189], v149 offset:37888
	ds_read_b128 v[194:197], v149 offset:38912
	ds_read_b128 v[198:201], v149 offset:39936
	s_add_u32 s14, s20, 0x80000
	s_addc_u32 s15, s21, 0
	s_mov_b32 s54, m0
	s_mov_b32 m0, s37
	s_nop 0
	global_load_lds_dwordx4 v1, s[14:15]
	s_mov_b32 m0, s54
	s_add_u32 s14, s20, 0xc0000
	s_addc_u32 s15, s21, 0
	s_mov_b32 s54, m0
	s_mov_b32 m0, s38
	s_nop 0
	global_load_lds_dwordx4 v1, s[14:15]
	s_mov_b32 m0, s54
	s_waitcnt lgkmcnt(8)
	s_barrier
	s_waitcnt lgkmcnt(0)
	s_setprio 1
	v_mfma_f32_16x16x32_bf16 v[126:129], v[150:153], v[166:169], v[126:129]
	v_mfma_f32_16x16x32_bf16 v[122:125], v[158:161], v[166:169], v[122:125]
	v_mfma_f32_16x16x32_bf16 v[110:113], v[150:153], v[174:177], v[110:113]
	v_mfma_f32_16x16x32_bf16 v[106:109], v[158:161], v[174:177], v[106:109]
	v_mfma_f32_16x16x32_bf16 v[94:97], v[150:153], v[182:185], v[94:97]
	v_mfma_f32_16x16x32_bf16 v[90:93], v[158:161], v[182:185], v[90:93]
	v_mfma_f32_16x16x32_bf16 v[78:81], v[150:153], v[194:197], v[78:81]
	v_mfma_f32_16x16x32_bf16 v[74:77], v[158:161], v[194:197], v[74:77]
	v_mfma_f32_16x16x32_bf16 v[126:129], v[154:157], v[170:173], v[126:129]
	v_mfma_f32_16x16x32_bf16 v[122:125], v[162:165], v[170:173], v[122:125]
	v_mfma_f32_16x16x32_bf16 v[110:113], v[154:157], v[178:181], v[110:113]
	v_mfma_f32_16x16x32_bf16 v[106:109], v[162:165], v[178:181], v[106:109]
	v_mfma_f32_16x16x32_bf16 v[94:97], v[154:157], v[186:189], v[94:97]
	v_mfma_f32_16x16x32_bf16 v[90:93], v[162:165], v[186:189], v[90:93]
	v_mfma_f32_16x16x32_bf16 v[78:81], v[154:157], v[198:201], v[78:81]
	v_mfma_f32_16x16x32_bf16 v[74:77], v[162:165], v[198:201], v[74:77]
	s_setprio 0
	s_barrier
	ds_read_b128 v[202:205], v145
	ds_read_b128 v[206:209], v146
	ds_read_b128 v[210:213], v147
	ds_read_b128 v[214:217], v148
	s_add_u32 s14, s18, 0x80
	s_addc_u32 s15, s19, 0
	s_mov_b32 s54, m0
	s_mov_b32 m0, s41
	s_nop 0
	global_load_lds_dwordx4 v132, s[14:15]
	s_mov_b32 m0, s54
	s_add_u32 s14, s18, 0x40080
	s_addc_u32 s15, s19, 0
	s_mov_b32 s54, m0
	s_mov_b32 m0, s42
	s_nop 0
	global_load_lds_dwordx4 v132, s[14:15]
	s_mov_b32 m0, s54
	s_barrier
	s_waitcnt lgkmcnt(0)
	s_setprio 1
	v_mfma_f32_16x16x32_bf16 v[118:121], v[202:205], v[166:169], v[118:121]
	v_mfma_f32_16x16x32_bf16 v[114:117], v[210:213], v[166:169], v[114:117]
	v_mfma_f32_16x16x32_bf16 v[102:105], v[202:205], v[174:177], v[102:105]
	v_mfma_f32_16x16x32_bf16 v[98:101], v[210:213], v[174:177], v[98:101]
	v_mfma_f32_16x16x32_bf16 v[86:89], v[202:205], v[182:185], v[86:89]
	v_mfma_f32_16x16x32_bf16 v[82:85], v[210:213], v[182:185], v[82:85]
	v_mfma_f32_16x16x32_bf16 v[70:73], v[202:205], v[194:197], v[70:73]
	v_mfma_f32_16x16x32_bf16 v[66:69], v[210:213], v[194:197], v[66:69]
	v_mfma_f32_16x16x32_bf16 v[118:121], v[206:209], v[170:173], v[118:121]
	v_mfma_f32_16x16x32_bf16 v[114:117], v[214:217], v[170:173], v[114:117]
	v_mfma_f32_16x16x32_bf16 v[102:105], v[206:209], v[178:181], v[102:105]
	v_mfma_f32_16x16x32_bf16 v[98:101], v[214:217], v[178:181], v[98:101]
	v_mfma_f32_16x16x32_bf16 v[86:89], v[206:209], v[186:189], v[86:89]
	v_mfma_f32_16x16x32_bf16 v[82:85], v[214:217], v[186:189], v[82:85]
	v_mfma_f32_16x16x32_bf16 v[70:73], v[206:209], v[198:201], v[70:73]
	v_mfma_f32_16x16x32_bf16 v[66:69], v[214:217], v[198:201], v[66:69]
	s_setprio 0
	s_barrier
	ds_read_b128 v[166:169], v149 offset:49152
	ds_read_b128 v[170:173], v149 offset:50176
	ds_read_b128 v[174:177], v149 offset:51200
	ds_read_b128 v[178:181], v149 offset:52224
	ds_read_b128 v[182:185], v149 offset:53248
	ds_read_b128 v[186:189], v149 offset:54272
	ds_read_b128 v[194:197], v149 offset:55296
	ds_read_b128 v[198:201], v149 offset:56320
	s_mov_b32 s14, m0
	s_mov_b32 m0, s43
	s_nop 0
	global_load_lds_dwordx4 v1, s[22:23]
	s_mov_b32 m0, s14
	s_add_u32 s14, s20, 0x40080
	s_addc_u32 s15, s21, 0
	s_mov_b32 s20, m0
	s_mov_b32 m0, s44
	s_nop 0
	global_load_lds_dwordx4 v1, s[14:15]
	s_mov_b32 m0, s20
	s_barrier
; __device__ __forceinline__ unsigned cvt_pk_bf16(float lo, float hi) { unsigned r; asm volatile("v_cvt_pk_bf16_f32 %0, %1, %2" : "=v"(r) : "v"(lo), "v"(hi)); return r; }
; #define PG8_STAGE(bufoff, gbase, voff) do { _Pragma("unroll") for (int _i = 0; _i < 2; ++_i) glds16_s((const void*)((const char*)(gbase) + _i * r64), (voff), ldsb + (unsigned)(bufoff) + ldsw + _i * 8192u); } while (0)
; #define PG8_WAIT_V(n) asm volatile("s_waitcnt vmcnt(" #n ")" ::: "memory")
; #define PG8_WAIT_L(n) asm volatile("s_waitcnt lgkmcnt(" #n ")" ::: "memory")
; #define PG8_BAR __builtin_amdgcn_s_barrier()
; #define PG8_SCHED __builtin_amdgcn_sched_barrier(0)
; #define PG8_HI do { if constexpr (FP8) asm volatile("s_setprio 1"); } while (0)
; #define PG8_LO do { if constexpr (FP8) asm volatile("s_setprio 0"); } while (0)
;     __device__ __forceinline__ void operator()(const f32x4 (&acc)[2][2][4][2], const Unit& u, int wr, int wc, int fr, int fq) const {
;         const int row0 = u.pm * BM + wr * 64 + fr, col0 = u.pn * HALF + wc * 32 + 8 * fq;
; #pragma unroll
;         for (int ai = 0; ai < 2; ++ai)
; #pragma unroll
;             for (int m = 0; m < 4; ++m) { bf16_t* rowp = O + (size_t)(row0 + ai * HALF + m * 16) * ldc + col0;
;                 f32x4 v[2];
; #pragma unroll
;                 for (int n = 0; n < 2; ++n) { const f32x4 g = acc[ai][0][m][n], up = acc[ai][1][m][n];
; #pragma unroll
;                     for (int j = 0; j < 4; ++j) { const float e = __builtin_amdgcn_exp2f(-1.4426950408889634f * g[j]); v[n][j] = g[j] * __builtin_amdgcn_rcpf(1.f + e) * up[j]; } }
;                 u32x4 w; w.x = cvt_pk_bf16(v[0][0], v[0][1]); w.y = cvt_pk_bf16(v[0][2], v[0][3]); w.z = cvt_pk_bf16(v[1][0], v[1][1]); w.w = cvt_pk_bf16(v[1][2], v[1][3]);
;                 *(u32x4*)rowp = w; }
; template <class Epi, class Sched, bool FP8 = false>
; __device__ __forceinline__ void gemm_phase(LAS unsigned char* lds, const int Kb, const int nt  , const Sched& S, const Epi& E) {
;     ...
;             PG8_BAR; PG8_HI; PG8_WAIT_L(0); PG8_MMA(1, 0, B0, B08); PG8_BAR; PG8_LO; PG8_SCHED;
;             PG8_STAGE(PG8_SB(1, 1), b3 + hstep, voffB);
;             PG8_WAIT_V(6); PG8_BAR; PG8_HI; PG8_MMA(1, 1, B1, B18); PG8_BAR; PG8_LO;
;         }
;         { int l_; asm volatile("v_mbcnt_lo_u32_b32 %0, -1, 0\n\tv_mbcnt_hi_u32_b32 %0, -1, %0" : "=v"(l_));
;           E(acc, cur, wr, wc, l_ & 15, l_ >> 4); }
	s_waitcnt lgkmcnt(0)
	s_setprio 1
	v_mfma_f32_16x16x32_bf16 v[62:65], v[150:153], v[166:169], v[62:65]
	v_mfma_f32_16x16x32_bf16 v[58:61], v[158:161], v[166:169], v[58:61]
	v_mfma_f32_16x16x32_bf16 v[46:49], v[150:153], v[174:177], v[46:49]
	v_mfma_f32_16x16x32_bf16 v[42:45], v[158:161], v[174:177], v[42:45]
	v_mfma_f32_16x16x32_bf16 v[30:33], v[150:153], v[182:185], v[30:33]
	v_mfma_f32_16x16x32_bf16 v[26:29], v[158:161], v[182:185], v[26:29]
	v_mfma_f32_16x16x32_bf16 v[14:17], v[150:153], v[194:197], v[14:17]
	v_mfma_f32_16x16x32_bf16 v[10:13], v[158:161], v[194:197], v[10:13]
	v_mfma_f32_16x16x32_bf16 v[62:65], v[154:157], v[170:173], v[62:65]
	v_mfma_f32_16x16x32_bf16 v[58:61], v[162:165], v[170:173], v[58:61]
	v_mfma_f32_16x16x32_bf16 v[46:49], v[154:157], v[178:181], v[46:49]
	v_mfma_f32_16x16x32_bf16 v[42:45], v[162:165], v[178:181], v[42:45]
	v_mfma_f32_16x16x32_bf16 v[30:33], v[154:157], v[186:189], v[30:33]
	v_mfma_f32_16x16x32_bf16 v[26:29], v[162:165], v[186:189], v[26:29]
	v_mfma_f32_16x16x32_bf16 v[14:17], v[154:157], v[198:201], v[14:17]
	v_mfma_f32_16x16x32_bf16 v[10:13], v[162:165], v[198:201], v[10:13]
	s_setprio 0
	s_barrier
	s_add_u32 s14, s18, 0x80080
	s_addc_u32 s15, s19, 0
	s_mov_b32 s20, m0
	s_mov_b32 m0, s45
	s_nop 0
	global_load_lds_dwordx4 v132, s[14:15]
	s_mov_b32 m0, s20
	s_add_u32 s14, s18, 0xc0080
	s_addc_u32 s15, s19, 0
	s_mov_b32 s18, m0
	s_mov_b32 m0, s46
	s_nop 0
	global_load_lds_dwordx4 v132, s[14:15]
	s_mov_b32 m0, s18
	s_waitcnt vmcnt(6)
	s_barrier
	s_setprio 1
	v_mfma_f32_16x16x32_bf16 v[54:57], v[202:205], v[166:169], v[54:57]
	v_mfma_f32_16x16x32_bf16 v[50:53], v[210:213], v[166:169], v[50:53]
	v_mfma_f32_16x16x32_bf16 v[38:41], v[202:205], v[174:177], v[38:41]
	v_mfma_f32_16x16x32_bf16 v[34:37], v[210:213], v[174:177], v[34:37]
	v_mfma_f32_16x16x32_bf16 v[22:25], v[202:205], v[182:185], v[22:25]
	v_mfma_f32_16x16x32_bf16 v[18:21], v[210:213], v[182:185], v[18:21]
	v_mfma_f32_16x16x32_bf16 v[6:9], v[202:205], v[194:197], v[6:9]
	v_mfma_f32_16x16x32_bf16 v[2:5], v[210:213], v[194:197], v[2:5]
	v_mfma_f32_16x16x32_bf16 v[54:57], v[206:209], v[170:173], v[54:57]
	v_mfma_f32_16x16x32_bf16 v[50:53], v[214:217], v[170:173], v[50:53]
	v_mfma_f32_16x16x32_bf16 v[38:41], v[206:209], v[178:181], v[38:41]
	v_mfma_f32_16x16x32_bf16 v[34:37], v[214:217], v[178:181], v[34:37]
	v_mfma_f32_16x16x32_bf16 v[22:25], v[206:209], v[186:189], v[22:25]
	v_mfma_f32_16x16x32_bf16 v[18:21], v[214:217], v[186:189], v[18:21]
	v_mfma_f32_16x16x32_bf16 v[6:9], v[206:209], v[198:201], v[6:9]
	v_mfma_f32_16x16x32_bf16 v[2:5], v[214:217], v[198:201], v[2:5]
	s_setprio 0
	s_add_i32 s53, s53, 2
	s_add_u32 s5, s5, 0x100
	s_addc_u32 s52, s52, 0
	s_cmp_gt_u32 s53, 29
	s_mov_b64 s[14:15], s[16:17]
	s_barrier
	s_cbranch_scc0 .LBB0_1946
	s_lshl_b32 s5, s12, 8
	v_mbcnt_lo_u32_b32 v130, -1, 0
	v_mbcnt_hi_u32_b32 v130, -1, v130
	s_add_i32 s5, s5, s39
	v_and_or_b32 v150, v130, 15, s5
	s_lshl_b32 s5, s51, 7
	v_ashrrev_i32_e32 v130, 1, v130
	s_or_b32 s5, s5, s40
	v_and_b32_e32 v130, -8, v130
	v_add_u32_e32 v152, s5, v130
	v_mul_f32_e32 v130, 0xbfb8aa3b, v126
	v_exp_f32_e32 v151, v130
	v_mul_f32_e32 v130, 0xbfb8aa3b, v127
	v_exp_f32_e32 v154, v130
	v_ashrrev_i32_e32 v153, 31, v152
	v_add_f32_e32 v151, 1.0, v151
	v_rcp_f32_e32 v151, v151
	v_add_f32_e32 v154, 1.0, v154
	v_rcp_f32_e32 v156, v154
	v_mov_b64_e32 v[130:131], s[2:3]
	v_mul_f32_e32 v126, v126, v151
	v_mul_f32_e32 v118, v126, v118
	v_mul_f32_e32 v126, v127, v156
	v_mul_f32_e32 v127, 0xbfb8aa3b, v128
	v_exp_f32_e32 v127, v127
	v_mul_f32_e32 v151, 0xbfb8aa3b, v129
	v_exp_f32_e32 v151, v151
	v_mul_f32_e32 v119, v126, v119
	v_add_f32_e32 v126, 1.0, v127
	v_rcp_f32_e32 v126, v126
	v_add_f32_e32 v127, 1.0, v151
	v_mul_f32_e32 v151, 0xbfb8aa3b, v122
	v_rcp_f32_e32 v127, v127
	v_exp_f32_e32 v151, v151
	v_mul_f32_e32 v126, v128, v126
	v_mul_f32_e32 v126, v126, v120
	v_mul_f32_e32 v120, v129, v127
	v_add_f32_e32 v127, 1.0, v151
	v_rcp_f32_e32 v127, v127
	v_mul_f32_e32 v128, 0xbfb8aa3b, v123
	v_mul_f32_e32 v129, v120, v121
	v_exp_f32_e32 v128, v128
	v_mul_f32_e32 v120, v122, v127
	v_mul_f32_e32 v122, v120, v114
	v_mul_f32_e32 v120, 0xbfb8aa3b, v124
	v_exp_f32_e32 v120, v120
	v_mul_f32_e32 v121, 0xbfb8aa3b, v125
	v_exp_f32_e32 v121, v121
	v_add_f32_e32 v114, 1.0, v128
	v_rcp_f32_e32 v114, v114
	v_add_f32_e32 v120, 1.0, v120
	v_rcp_f32_e32 v120, v120
	v_add_f32_e32 v121, 1.0, v121
	v_rcp_f32_e32 v121, v121
	v_mul_f32_e32 v114, v123, v114
	v_mul_f32_e32 v123, v114, v115
	v_mul_f32_e32 v114, v124, v120
	v_mul_f32_e32 v124, v114, v116
	v_mul_f32_e32 v114, v125, v121
	v_mad_i64_i32 v[154:155], s[14:15], v150, s49, v[130:131]
	v_mul_f32_e32 v125, v114, v117
	v_lshlrev_b64 v[114:115], 1, v[152:153]
	v_lshl_add_u64 v[120:121], v[154:155], 0, v[114:115]
	v_cvt_pk_bf16_f32 v116, v118, v119
	v_cvt_pk_bf16_f32 v117, v126, v129
	v_cvt_pk_bf16_f32 v118, v122, v123
	v_cvt_pk_bf16_f32 v119, v124, v125
	global_store_dwordx4 v[120:121], v[116:119], off
	s_and_b64 vcc, exec, s[6:7]
	s_mov_b32 s51, s50
	v_mul_f32_e32 v116, 0xbfb8aa3b, v110
	v_exp_f32_e32 v116, v116
	v_mul_f32_e32 v117, 0xbfb8aa3b, v111
	v_exp_f32_e32 v117, v117
	v_or_b32_e32 v118, 16, v150
	v_add_f32_e32 v116, 1.0, v116
	v_rcp_f32_e32 v119, v116
	v_add_f32_e32 v116, 1.0, v117
	v_rcp_f32_e32 v120, v116
	v_mad_i64_i32 v[116:117], s[14:15], v118, s49, v[130:131]
	v_mul_f32_e32 v110, v110, v119
	v_mul_f32_e32 v110, v110, v102
	v_mul_f32_e32 v102, v111, v120
	v_mul_f32_e32 v111, 0xbfb8aa3b, v112
	v_exp_f32_e32 v111, v111
	v_mul_f32_e32 v118, 0xbfb8aa3b, v113
	v_exp_f32_e32 v118, v118
	v_mul_f32_e32 v119, v102, v103
	v_add_f32_e32 v102, 1.0, v111
; __device__ __forceinline__ unsigned cvt_pk_bf16(float lo, float hi) { unsigned r; asm volatile("v_cvt_pk_bf16_f32 %0, %1, %2" : "=v"(r) : "v"(lo), "v"(hi)); return r; }
;     __device__ __forceinline__ void operator()(const f32x4 (&acc)[2][2][4][2], const Unit& u, int wr, int wc, int fr, int fq) const {
;     ...
;         for (int ai = 0; ai < 2; ++ai)
; #pragma unroll
;             for (int m = 0; m < 4; ++m) { bf16_t* rowp = O + (size_t)(row0 + ai * HALF + m * 16) * ldc + col0;
;                 f32x4 v[2];
; #pragma unroll
;                 for (int n = 0; n < 2; ++n) { const f32x4 g = acc[ai][0][m][n], up = acc[ai][1][m][n];
; #pragma unroll
;                     for (int j = 0; j < 4; ++j) { const float e = __builtin_amdgcn_exp2f(-1.4426950408889634f * g[j]); v[n][j] = g[j] * __builtin_amdgcn_rcpf(1.f + e) * up[j]; } }
;                 u32x4 w; w.x = cvt_pk_bf16(v[0][0], v[0][1]); w.y = cvt_pk_bf16(v[0][2], v[0][3]); w.z = cvt_pk_bf16(v[1][0], v[1][1]); w.w = cvt_pk_bf16(v[1][2], v[1][3]);
;                 *(u32x4*)rowp = w; }
	v_rcp_f32_e32 v102, v102
	v_add_f32_e32 v103, 1.0, v118
	v_mul_f32_e32 v111, 0xbfb8aa3b, v106
	v_rcp_f32_e32 v103, v103
	v_exp_f32_e32 v111, v111
	v_mul_f32_e32 v102, v112, v102
	v_mul_f32_e32 v104, v102, v104
	v_mul_f32_e32 v102, v113, v103
	v_add_f32_e32 v103, 1.0, v111
	v_rcp_f32_e32 v103, v103
	v_mul_f32_e32 v111, 0xbfb8aa3b, v107
	v_mul_f32_e32 v105, v102, v105
	v_exp_f32_e32 v111, v111
	v_mul_f32_e32 v102, v106, v103
	v_mul_f32_e32 v106, v102, v98
	v_mul_f32_e32 v102, 0xbfb8aa3b, v108
	v_exp_f32_e32 v102, v102
	v_mul_f32_e32 v103, 0xbfb8aa3b, v109
	v_exp_f32_e32 v103, v103
	v_add_f32_e32 v98, 1.0, v111
	v_rcp_f32_e32 v98, v98
	v_add_f32_e32 v102, 1.0, v102
	v_rcp_f32_e32 v102, v102
	v_add_f32_e32 v103, 1.0, v103
	v_rcp_f32_e32 v103, v103
	v_mul_f32_e32 v98, v107, v98
	v_mul_f32_e32 v107, v98, v99
	v_mul_f32_e32 v98, v108, v102
	v_mul_f32_e32 v108, v98, v100
	v_mul_f32_e32 v98, v109, v103
	v_mul_f32_e32 v101, v98, v101
	v_lshl_add_u64 v[102:103], v[116:117], 0, v[114:115]
	v_cvt_pk_bf16_f32 v98, v110, v119
	v_cvt_pk_bf16_f32 v99, v104, v105
	v_cvt_pk_bf16_f32 v100, v106, v107
	v_cvt_pk_bf16_f32 v101, v108, v101
	global_store_dwordx4 v[102:103], v[98:101], off
	s_mov_b32 s12, s4
	s_mov_b64 s[16:17], s[10:11]
	v_mul_f32_e32 v98, 0xbfb8aa3b, v94
	v_exp_f32_e32 v98, v98
	v_mul_f32_e32 v99, 0xbfb8aa3b, v95
	v_exp_f32_e32 v99, v99
	v_or_b32_e32 v100, 32, v150
	v_add_f32_e32 v98, 1.0, v98
	v_rcp_f32_e32 v101, v98
	v_add_f32_e32 v98, 1.0, v99
	v_rcp_f32_e32 v102, v98
	v_mad_i64_i32 v[98:99], s[14:15], v100, s49, v[130:131]
	v_mul_f32_e32 v94, v94, v101
	v_mul_f32_e32 v94, v94, v86
	v_mul_f32_e32 v86, v95, v102
	v_mul_f32_e32 v95, 0xbfb8aa3b, v96
	v_exp_f32_e32 v95, v95
	v_mul_f32_e32 v100, 0xbfb8aa3b, v97
	v_exp_f32_e32 v100, v100
	v_mul_f32_e32 v101, v86, v87
	v_add_f32_e32 v86, 1.0, v95
	v_rcp_f32_e32 v86, v86
	v_add_f32_e32 v87, 1.0, v100
	v_mul_f32_e32 v95, 0xbfb8aa3b, v90
	v_rcp_f32_e32 v87, v87
	v_exp_f32_e32 v95, v95
	v_mul_f32_e32 v86, v96, v86
	v_mul_f32_e32 v88, v86, v88
	v_mul_f32_e32 v86, v97, v87
	v_add_f32_e32 v87, 1.0, v95
	v_rcp_f32_e32 v87, v87
	v_mul_f32_e32 v95, 0xbfb8aa3b, v91
	v_mul_f32_e32 v89, v86, v89
	v_exp_f32_e32 v95, v95
	v_mul_f32_e32 v86, v90, v87
	v_mul_f32_e32 v90, v86, v82
	v_mul_f32_e32 v86, 0xbfb8aa3b, v92
	v_exp_f32_e32 v86, v86
	v_mul_f32_e32 v87, 0xbfb8aa3b, v93
	v_exp_f32_e32 v87, v87
	v_add_f32_e32 v82, 1.0, v95
	v_rcp_f32_e32 v82, v82
	v_add_f32_e32 v86, 1.0, v86
	v_rcp_f32_e32 v86, v86
	v_add_f32_e32 v87, 1.0, v87
	v_rcp_f32_e32 v87, v87
	v_mul_f32_e32 v82, v91, v82
	v_mul_f32_e32 v91, v82, v83
	v_mul_f32_e32 v82, v92, v86
	v_mul_f32_e32 v92, v82, v84
	v_mul_f32_e32 v82, v93, v87
	v_mul_f32_e32 v85, v82, v85
	v_lshl_add_u64 v[86:87], v[98:99], 0, v[114:115]
	v_cvt_pk_bf16_f32 v82, v94, v101
	v_cvt_pk_bf16_f32 v83, v88, v89
	v_cvt_pk_bf16_f32 v84, v90, v91
	v_cvt_pk_bf16_f32 v85, v92, v85
	global_store_dwordx4 v[86:87], v[82:85], off
	s_nop 1
	v_mul_f32_e32 v82, 0xbfb8aa3b, v78
	v_exp_f32_e32 v82, v82
	v_mul_f32_e32 v83, 0xbfb8aa3b, v79
	v_exp_f32_e32 v83, v83
	v_or_b32_e32 v84, 48, v150
	v_add_f32_e32 v82, 1.0, v82
	v_rcp_f32_e32 v85, v82
	v_add_f32_e32 v82, 1.0, v83
	v_rcp_f32_e32 v86, v82
	v_mad_i64_i32 v[82:83], s[14:15], v84, s49, v[130:131]
	v_mul_f32_e32 v78, v78, v85
	v_mul_f32_e32 v78, v78, v70
	v_mul_f32_e32 v70, v79, v86
	v_mul_f32_e32 v79, 0xbfb8aa3b, v80
	v_exp_f32_e32 v79, v79
	v_mul_f32_e32 v84, 0xbfb8aa3b, v81
	v_exp_f32_e32 v84, v84
	v_mul_f32_e32 v85, v70, v71
	v_add_f32_e32 v70, 1.0, v79
	v_rcp_f32_e32 v70, v70
	v_add_f32_e32 v71, 1.0, v84
	v_mul_f32_e32 v79, 0xbfb8aa3b, v74
	v_rcp_f32_e32 v71, v71
	v_exp_f32_e32 v79, v79
	v_mul_f32_e32 v70, v80, v70
	v_mul_f32_e32 v72, v70, v72
	v_mul_f32_e32 v70, v81, v71
	v_add_f32_e32 v71, 1.0, v79
	v_rcp_f32_e32 v71, v71
	v_mul_f32_e32 v79, 0xbfb8aa3b, v75
	v_mul_f32_e32 v73, v70, v73
	v_exp_f32_e32 v79, v79
	v_mul_f32_e32 v70, v74, v71
	v_mul_f32_e32 v74, v70, v66
	v_mul_f32_e32 v70, 0xbfb8aa3b, v76
	v_exp_f32_e32 v70, v70
	v_mul_f32_e32 v71, 0xbfb8aa3b, v77
	v_exp_f32_e32 v71, v71
	v_add_f32_e32 v66, 1.0, v79
	v_rcp_f32_e32 v66, v66
	v_add_f32_e32 v70, 1.0, v70
	v_rcp_f32_e32 v70, v70
	v_add_f32_e32 v71, 1.0, v71
	v_rcp_f32_e32 v71, v71
	v_mul_f32_e32 v66, v75, v66
	v_mul_f32_e32 v75, v66, v67
	v_mul_f32_e32 v66, v76, v70
	v_mul_f32_e32 v76, v66, v68
	v_mul_f32_e32 v66, v77, v71
	v_mul_f32_e32 v69, v66, v69
	v_lshl_add_u64 v[70:71], v[82:83], 0, v[114:115]
	v_cvt_pk_bf16_f32 v66, v78, v85
	v_cvt_pk_bf16_f32 v67, v72, v73
	v_cvt_pk_bf16_f32 v68, v74, v75
	v_cvt_pk_bf16_f32 v69, v76, v69
	global_store_dwordx4 v[70:71], v[66:69], off
	s_nop 1
	v_mul_f32_e32 v66, 0xbfb8aa3b, v62
	v_exp_f32_e32 v66, v66
	v_mul_f32_e32 v67, 0xbfb8aa3b, v63
	v_exp_f32_e32 v67, v67
	v_add_u32_e32 v68, 0x80, v150
	v_add_f32_e32 v66, 1.0, v66
	v_rcp_f32_e32 v69, v66
	v_add_f32_e32 v66, 1.0, v67
	v_rcp_f32_e32 v70, v66
	v_mad_i64_i32 v[66:67], s[14:15], v68, s49, v[130:131]
	v_mul_f32_e32 v62, v62, v69
	v_mul_f32_e32 v62, v62, v54
	v_mul_f32_e32 v54, v63, v70
	v_mul_f32_e32 v63, 0xbfb8aa3b, v64
	v_exp_f32_e32 v63, v63
	v_mul_f32_e32 v68, 0xbfb8aa3b, v65
	v_exp_f32_e32 v68, v68
	v_mul_f32_e32 v69, v54, v55
	v_add_f32_e32 v54, 1.0, v63
	v_rcp_f32_e32 v54, v54
	v_add_f32_e32 v55, 1.0, v68
	v_mul_f32_e32 v63, 0xbfb8aa3b, v58
	v_rcp_f32_e32 v55, v55
	v_exp_f32_e32 v63, v63
	v_mul_f32_e32 v54, v64, v54
	v_mul_f32_e32 v56, v54, v56
	v_mul_f32_e32 v54, v65, v55
	v_add_f32_e32 v55, 1.0, v63
	v_rcp_f32_e32 v55, v55
	v_mul_f32_e32 v63, 0xbfb8aa3b, v59
	v_mul_f32_e32 v57, v54, v57
	v_exp_f32_e32 v63, v63
	v_mul_f32_e32 v54, v58, v55
	v_mul_f32_e32 v58, v54, v50
; __device__ __forceinline__ unsigned cvt_pk_bf16(float lo, float hi) { unsigned r; asm volatile("v_cvt_pk_bf16_f32 %0, %1, %2" : "=v"(r) : "v"(lo), "v"(hi)); return r; }
; #define PG8_WAIT_V(n) asm volatile("s_waitcnt vmcnt(" #n ")" ::: "memory")
; #define PG8_BAR __builtin_amdgcn_s_barrier()
;     __device__ __forceinline__ void operator()(const f32x4 (&acc)[2][2][4][2], const Unit& u, int wr, int wc, int fr, int fq) const {
;     ...
;             for (int m = 0; m < 4; ++m) { bf16_t* rowp = O + (size_t)(row0 + ai * HALF + m * 16) * ldc + col0;
;                 f32x4 v[2];
; #pragma unroll
;                 for (int n = 0; n < 2; ++n) { const f32x4 g = acc[ai][0][m][n], up = acc[ai][1][m][n];
; #pragma unroll
;                     for (int j = 0; j < 4; ++j) { const float e = __builtin_amdgcn_exp2f(-1.4426950408889634f * g[j]); v[n][j] = g[j] * __builtin_amdgcn_rcpf(1.f + e) * up[j]; } }
;                 u32x4 w; w.x = cvt_pk_bf16(v[0][0], v[0][1]); w.y = cvt_pk_bf16(v[0][2], v[0][3]); w.z = cvt_pk_bf16(v[1][0], v[1][1]); w.w = cvt_pk_bf16(v[1][2], v[1][3]);
;                 *(u32x4*)rowp = w; }
; template <class Epi, class Sched, bool FP8 = false>
; __device__ __forceinline__ void gemm_phase(LAS unsigned char* lds, const int Kb, const int nt  , const Sched& S, const Epi& E) {
;     ...
;         if (!has_next) break;
; #pragma unroll
;         for (int a = 0; a < 2; ++a)
; #pragma unroll
;             for (int b = 0; b < 2; ++b)
; #pragma unroll
;                 for (int m = 0; m < 4; ++m)
; #pragma unroll
;                     for (int n = 0; n < 2; ++n) acc[a][b][m][n] = (f32x4){0.f, 0.f, 0.f, 0.f};
;         cur = nxt; cA = nA; cB = nB; ++ui;
;     }
;     PG8_WAIT_V(0);
;     if (wr == 0) PG8_BAR;
;     PG8_BAR;
	v_mul_f32_e32 v54, 0xbfb8aa3b, v60
	v_exp_f32_e32 v54, v54
	v_mul_f32_e32 v55, 0xbfb8aa3b, v61
	v_exp_f32_e32 v55, v55
	v_add_f32_e32 v50, 1.0, v63
	v_rcp_f32_e32 v50, v50
	v_add_f32_e32 v54, 1.0, v54
	v_rcp_f32_e32 v54, v54
	v_add_f32_e32 v55, 1.0, v55
	v_rcp_f32_e32 v55, v55
	v_mul_f32_e32 v50, v59, v50
	v_mul_f32_e32 v59, v50, v51
	v_mul_f32_e32 v50, v60, v54
	v_mul_f32_e32 v60, v50, v52
	v_mul_f32_e32 v50, v61, v55
	v_mul_f32_e32 v53, v50, v53
	v_lshl_add_u64 v[54:55], v[66:67], 0, v[114:115]
	v_cvt_pk_bf16_f32 v50, v62, v69
	v_cvt_pk_bf16_f32 v51, v56, v57
	v_cvt_pk_bf16_f32 v52, v58, v59
	v_cvt_pk_bf16_f32 v53, v60, v53
	global_store_dwordx4 v[54:55], v[50:53], off
	s_nop 1
	v_mul_f32_e32 v50, 0xbfb8aa3b, v46
	v_exp_f32_e32 v50, v50
	v_mul_f32_e32 v51, 0xbfb8aa3b, v47
	v_exp_f32_e32 v51, v51
	v_add_u32_e32 v52, 0x90, v150
	v_add_f32_e32 v50, 1.0, v50
	v_rcp_f32_e32 v53, v50
	v_add_f32_e32 v50, 1.0, v51
	v_rcp_f32_e32 v54, v50
	v_mad_i64_i32 v[50:51], s[14:15], v52, s49, v[130:131]
	v_mul_f32_e32 v46, v46, v53
	v_mul_f32_e32 v46, v46, v38
	v_mul_f32_e32 v38, v47, v54
	v_mul_f32_e32 v47, 0xbfb8aa3b, v48
	v_exp_f32_e32 v47, v47
	v_mul_f32_e32 v52, 0xbfb8aa3b, v49
	v_exp_f32_e32 v52, v52
	v_mul_f32_e32 v53, v38, v39
	v_add_f32_e32 v38, 1.0, v47
	v_rcp_f32_e32 v38, v38
	v_add_f32_e32 v39, 1.0, v52
	v_mul_f32_e32 v47, 0xbfb8aa3b, v42
	v_rcp_f32_e32 v39, v39
	v_exp_f32_e32 v47, v47
	v_mul_f32_e32 v38, v48, v38
	v_mul_f32_e32 v40, v38, v40
	v_mul_f32_e32 v38, v49, v39
	v_add_f32_e32 v39, 1.0, v47
	v_rcp_f32_e32 v39, v39
	v_mul_f32_e32 v47, 0xbfb8aa3b, v43
	v_mul_f32_e32 v41, v38, v41
	v_exp_f32_e32 v47, v47
	v_mul_f32_e32 v38, v42, v39
	v_mul_f32_e32 v42, v38, v34
	v_mul_f32_e32 v38, 0xbfb8aa3b, v44
	v_exp_f32_e32 v38, v38
	v_mul_f32_e32 v39, 0xbfb8aa3b, v45
	v_exp_f32_e32 v39, v39
	v_add_f32_e32 v34, 1.0, v47
	v_rcp_f32_e32 v34, v34
	v_add_f32_e32 v38, 1.0, v38
	v_rcp_f32_e32 v38, v38
	v_add_f32_e32 v39, 1.0, v39
	v_rcp_f32_e32 v39, v39
	v_mul_f32_e32 v34, v43, v34
	v_mul_f32_e32 v43, v34, v35
	v_mul_f32_e32 v34, v44, v38
	v_mul_f32_e32 v44, v34, v36
	v_mul_f32_e32 v34, v45, v39
	v_mul_f32_e32 v37, v34, v37
	v_lshl_add_u64 v[38:39], v[50:51], 0, v[114:115]
	v_cvt_pk_bf16_f32 v34, v46, v53
	v_cvt_pk_bf16_f32 v35, v40, v41
	v_cvt_pk_bf16_f32 v36, v42, v43
	v_cvt_pk_bf16_f32 v37, v44, v37
	global_store_dwordx4 v[38:39], v[34:37], off
	s_nop 1
	v_mul_f32_e32 v34, 0xbfb8aa3b, v30
	v_exp_f32_e32 v34, v34
	v_mul_f32_e32 v35, 0xbfb8aa3b, v31
	v_exp_f32_e32 v35, v35
	v_add_u32_e32 v36, 0xa0, v150
	v_add_f32_e32 v34, 1.0, v34
	v_rcp_f32_e32 v37, v34
	v_add_f32_e32 v34, 1.0, v35
	v_rcp_f32_e32 v38, v34
	v_mad_i64_i32 v[34:35], s[14:15], v36, s49, v[130:131]
	v_mul_f32_e32 v30, v30, v37
	v_mul_f32_e32 v30, v30, v22
	v_mul_f32_e32 v22, v31, v38
	v_mul_f32_e32 v31, 0xbfb8aa3b, v32
	v_exp_f32_e32 v31, v31
	v_mul_f32_e32 v36, 0xbfb8aa3b, v33
	v_exp_f32_e32 v36, v36
	v_mul_f32_e32 v37, v22, v23
	v_add_f32_e32 v22, 1.0, v31
	v_rcp_f32_e32 v22, v22
	v_add_f32_e32 v23, 1.0, v36
	v_mul_f32_e32 v31, 0xbfb8aa3b, v26
	v_rcp_f32_e32 v23, v23
	v_exp_f32_e32 v31, v31
	v_mul_f32_e32 v22, v32, v22
	v_mul_f32_e32 v24, v22, v24
	v_mul_f32_e32 v22, v33, v23
	v_add_f32_e32 v23, 1.0, v31
	v_rcp_f32_e32 v23, v23
	v_mul_f32_e32 v31, 0xbfb8aa3b, v27
	v_mul_f32_e32 v25, v22, v25
	v_exp_f32_e32 v31, v31
	v_mul_f32_e32 v22, v26, v23
	v_mul_f32_e32 v26, v22, v18
	v_mul_f32_e32 v22, 0xbfb8aa3b, v28
	v_exp_f32_e32 v22, v22
	v_mul_f32_e32 v23, 0xbfb8aa3b, v29
	v_exp_f32_e32 v23, v23
	v_add_f32_e32 v18, 1.0, v31
	v_rcp_f32_e32 v18, v18
	v_add_f32_e32 v22, 1.0, v22
	v_rcp_f32_e32 v22, v22
	v_add_f32_e32 v23, 1.0, v23
	v_rcp_f32_e32 v23, v23
	v_mul_f32_e32 v18, v27, v18
	v_mul_f32_e32 v27, v18, v19
	v_mul_f32_e32 v18, v28, v22
	v_mul_f32_e32 v28, v18, v20
	v_mul_f32_e32 v18, v29, v23
	v_mul_f32_e32 v21, v18, v21
	v_lshl_add_u64 v[22:23], v[34:35], 0, v[114:115]
	v_cvt_pk_bf16_f32 v18, v30, v37
	v_cvt_pk_bf16_f32 v19, v24, v25
	v_cvt_pk_bf16_f32 v20, v26, v27
	v_cvt_pk_bf16_f32 v21, v28, v21
	global_store_dwordx4 v[22:23], v[18:21], off
	s_nop 1
	v_mul_f32_e32 v18, 0xbfb8aa3b, v14
	v_exp_f32_e32 v18, v18
	v_mul_f32_e32 v19, 0xbfb8aa3b, v15
	v_exp_f32_e32 v19, v19
	v_add_u32_e32 v20, 0xb0, v150
	v_add_f32_e32 v18, 1.0, v18
	v_rcp_f32_e32 v21, v18
	v_add_f32_e32 v18, 1.0, v19
	v_rcp_f32_e32 v22, v18
	v_mad_i64_i32 v[18:19], s[14:15], v20, s49, v[130:131]
	v_mul_f32_e32 v14, v14, v21
	v_mul_f32_e32 v14, v14, v6
	v_mul_f32_e32 v6, v15, v22
	v_mul_f32_e32 v15, 0xbfb8aa3b, v16
	v_exp_f32_e32 v15, v15
	v_mul_f32_e32 v20, 0xbfb8aa3b, v17
	v_exp_f32_e32 v20, v20
	v_mul_f32_e32 v21, v6, v7
	v_add_f32_e32 v6, 1.0, v15
	v_rcp_f32_e32 v6, v6
	v_add_f32_e32 v7, 1.0, v20
	v_mul_f32_e32 v15, 0xbfb8aa3b, v10
	v_rcp_f32_e32 v7, v7
	v_exp_f32_e32 v15, v15
	v_mul_f32_e32 v6, v16, v6
	v_mul_f32_e32 v8, v6, v8
	v_mul_f32_e32 v6, v17, v7
	v_add_f32_e32 v7, 1.0, v15
	v_rcp_f32_e32 v7, v7
	v_mul_f32_e32 v15, 0xbfb8aa3b, v11
	v_mul_f32_e32 v9, v6, v9
	v_exp_f32_e32 v15, v15
	v_mul_f32_e32 v6, v10, v7
	v_mul_f32_e32 v10, v6, v2
	v_mul_f32_e32 v6, 0xbfb8aa3b, v12
	v_exp_f32_e32 v6, v6
	v_mul_f32_e32 v7, 0xbfb8aa3b, v13
	v_exp_f32_e32 v7, v7
	v_add_f32_e32 v2, 1.0, v15
	v_rcp_f32_e32 v2, v2
	v_add_f32_e32 v6, 1.0, v6
	v_rcp_f32_e32 v6, v6
	v_add_f32_e32 v7, 1.0, v7
	v_rcp_f32_e32 v7, v7
	v_mul_f32_e32 v2, v11, v2
	v_mul_f32_e32 v11, v2, v3
	v_mul_f32_e32 v2, v12, v6
	v_mul_f32_e32 v12, v2, v4
	v_mul_f32_e32 v2, v13, v7
	v_mul_f32_e32 v5, v2, v5
	v_lshl_add_u64 v[6:7], v[18:19], 0, v[114:115]
	s_mov_b64 s[14:15], s[8:9]
	v_cvt_pk_bf16_f32 v2, v14, v21
	v_cvt_pk_bf16_f32 v3, v8, v9
	v_cvt_pk_bf16_f32 v4, v10, v11
	v_cvt_pk_bf16_f32 v5, v12, v5
	global_store_dwordx4 v[6:7], v[2:5], off
	s_cbranch_vccz .LBB0_1943
	s_waitcnt vmcnt(0)
	s_cmpk_gt_u32 s24, 0xff
	s_cbranch_scc1 .LBB0_1950
	s_barrier

; #define PG8_STAGE(bufoff, gbase, voff) do { _Pragma("unroll") for (int _i = 0; _i < 2; ++_i) glds16_s((const void*)((const char*)(gbase) + _i * r64), (voff), ldsb + (unsigned)(bufoff) + ldsw + _i * 8192u); } while (0)
; #define PG8_LDA(b, h) do { _Pragma("unroll") for (int m = 0; m < 4; ++m) { const int o_ = PG8_SA(b, h) + aoff + m * 2048; \
;         if constexpr (FP8) A8[m] = PG8_CAT8(o_); else { At[m][0] = PG8_LD16(o_); At[m][1] = PG8_LD16(o_ + 1024); } } } while (0)
; #define PG8_LDB(X, X8, b, h) do { _Pragma("unroll") for (int n = 0; n < 2; ++n) { const int o_ = PG8_SB(b, h) + boff + n * 2048; \
;         if constexpr (FP8) X8[n] = PG8_CAT8(o_); else { X[n][0] = PG8_LD16(o_); X[n][1] = PG8_LD16(o_ + 1024); } } } while (0)
; #define PG8_WAIT_L(n) asm volatile("s_waitcnt lgkmcnt(" #n ")" ::: "memory")
; #define PG8_BAR __builtin_amdgcn_s_barrier()
; #define PG8_SCHED __builtin_amdgcn_sched_barrier(0)
; #define PG8_HI do { if constexpr (FP8) asm volatile("s_setprio 1"); } while (0)
; #define PG8_LO do { if constexpr (FP8) asm volatile("s_setprio 0"); } while (0)
; template <class Epi, class Sched, bool FP8 = false>
; __device__ __forceinline__ void gemm_phase(LAS unsigned char* lds, const int Kb, const int nt  , const Sched& S, const Epi& E) {
;     ...
;         for (int t = 0; t < nt; t += 2) {
;             const bool last = (t == nt - 2);
;             const char* a1 = cA + (size_t)(t + 1) * kstep;
;             const char* a2 = last ? nA : cA + (size_t)(t + 2) * kstep; const char* b2 = last ? nB : cB + (size_t)(t + 2) * kstep;
;             const char* a3 = a2 + kstep; const char* b3 = b2 + kstep;
;             PG8_LDB(B0, B08, 0, 0); PG8_SCHED; PG8_LDA(0, 0); PG8_STAGE(PG8_SA(1, 1), a1 + hstep, voffA);
;             PG8_WAIT_L(8); PG8_BAR; PG8_HI; PG8_WAIT_L(0); PG8_MMA(0, 0, B0, B08); PG8_BAR; PG8_LO; PG8_SCHED;
;             PG8_LDB(B1, B18, 0, 1); PG8_STAGE(PG8_SB(0, 0), b2, voffB);
;             PG8_BAR; PG8_HI; PG8_WAIT_L(0); PG8_MMA(0, 1, B1, B18); PG8_BAR; PG8_LO;
;             PG8_LDA(0, 1); PG8_STAGE(PG8_SA(0, 0), a2, voffA);
;             PG8_BAR; PG8_HI; PG8_WAIT_L(0); PG8_MMA(1, 0, B0, B08); PG8_BAR; PG8_LO; PG8_SCHED;
.LBB0_2043:
	ds_read_b128 v[150:153], v132
	ds_read_b128 v[154:157], v133
	ds_read_b128 v[158:161], v134
	ds_read_b128 v[162:165], v135
	s_add_u32 s22, s20, 0xffea0080
	s_addc_u32 s23, s21, -1
	s_cmpk_eq_i32 s59, 0x54
	s_cselect_b32 s24, s16, s22
	s_cselect_b32 s25, s17, s23
	s_cselect_b32 s22, s18, s57
	s_cselect_b32 s23, s19, s58
	s_add_u32 s26, s24, 0x80
	s_addc_u32 s27, s25, 0
	ds_read_b128 v[166:169], v148
	ds_read_b128 v[170:173], v148 offset:1024
	ds_read_b128 v[174:177], v148 offset:2048
	ds_read_b128 v[178:181], v148 offset:3072
	ds_read_b128 v[182:185], v148 offset:4096
	ds_read_b128 v[186:189], v148 offset:5120
	ds_read_b128 v[194:197], v148 offset:6144
	ds_read_b128 v[198:201], v148 offset:7168
	s_mov_b32 s60, m0
	s_mov_b32 m0, s51
	s_nop 0
	global_load_lds_dwordx4 v1, s[20:21]
	s_mov_b32 m0, s60
	s_add_u32 s60, s20, 0xb0000
	s_addc_u32 s61, s21, 0
	s_mov_b32 s62, m0
	s_mov_b32 m0, s52
	s_nop 0
	global_load_lds_dwordx4 v1, s[60:61]
	s_mov_b32 m0, s62
	s_waitcnt lgkmcnt(8)
	s_barrier
	s_waitcnt lgkmcnt(0)
	s_setprio 1
	v_mfma_f32_16x16x32_bf16 v[126:129], v[150:153], v[166:169], v[126:129]
	v_mfma_f32_16x16x32_bf16 v[122:125], v[158:161], v[166:169], v[122:125]
	v_mfma_f32_16x16x32_bf16 v[110:113], v[150:153], v[174:177], v[110:113]
	v_mfma_f32_16x16x32_bf16 v[106:109], v[158:161], v[174:177], v[106:109]
	v_mfma_f32_16x16x32_bf16 v[94:97], v[150:153], v[182:185], v[94:97]
	v_mfma_f32_16x16x32_bf16 v[90:93], v[158:161], v[182:185], v[90:93]
	v_mfma_f32_16x16x32_bf16 v[78:81], v[150:153], v[194:197], v[78:81]
	v_mfma_f32_16x16x32_bf16 v[74:77], v[158:161], v[194:197], v[74:77]
	v_mfma_f32_16x16x32_bf16 v[126:129], v[154:157], v[170:173], v[126:129]
	v_mfma_f32_16x16x32_bf16 v[122:125], v[162:165], v[170:173], v[122:125]
	v_mfma_f32_16x16x32_bf16 v[110:113], v[154:157], v[178:181], v[110:113]
	v_mfma_f32_16x16x32_bf16 v[106:109], v[162:165], v[178:181], v[106:109]
	v_mfma_f32_16x16x32_bf16 v[94:97], v[154:157], v[186:189], v[94:97]
	v_mfma_f32_16x16x32_bf16 v[90:93], v[162:165], v[186:189], v[90:93]
	v_mfma_f32_16x16x32_bf16 v[78:81], v[154:157], v[198:201], v[78:81]
	v_mfma_f32_16x16x32_bf16 v[74:77], v[162:165], v[198:201], v[74:77]
	s_setprio 0
	s_barrier
	ds_read_b128 v[202:205], v136
	ds_read_b128 v[206:209], v137
	ds_read_b128 v[210:213], v138
	ds_read_b128 v[214:217], v139
	s_mov_b32 s60, m0
	s_mov_b32 m0, s36
	s_nop 0
	global_load_lds_dwordx4 v1, s[22:23]
	s_mov_b32 m0, s60
	s_add_u32 s60, s22, 0xb0000
	s_addc_u32 s61, s23, 0
	s_mov_b32 s62, m0
	s_mov_b32 m0, s37
	s_nop 0
	global_load_lds_dwordx4 v1, s[60:61]
	s_mov_b32 m0, s62
	s_barrier
	s_waitcnt lgkmcnt(0)
	s_setprio 1
	v_mfma_f32_16x16x32_bf16 v[118:121], v[202:205], v[166:169], v[118:121]
	v_mfma_f32_16x16x32_bf16 v[114:117], v[210:213], v[166:169], v[114:117]
	v_mfma_f32_16x16x32_bf16 v[102:105], v[202:205], v[174:177], v[102:105]
	v_mfma_f32_16x16x32_bf16 v[98:101], v[210:213], v[174:177], v[98:101]
	v_mfma_f32_16x16x32_bf16 v[86:89], v[202:205], v[182:185], v[86:89]
	v_mfma_f32_16x16x32_bf16 v[82:85], v[210:213], v[182:185], v[82:85]
	v_mfma_f32_16x16x32_bf16 v[70:73], v[202:205], v[194:197], v[70:73]
	v_mfma_f32_16x16x32_bf16 v[66:69], v[210:213], v[194:197], v[66:69]
	v_mfma_f32_16x16x32_bf16 v[118:121], v[206:209], v[170:173], v[118:121]
	v_mfma_f32_16x16x32_bf16 v[114:117], v[214:217], v[170:173], v[114:117]
	v_mfma_f32_16x16x32_bf16 v[102:105], v[206:209], v[178:181], v[102:105]
	v_mfma_f32_16x16x32_bf16 v[98:101], v[214:217], v[178:181], v[98:101]
	v_mfma_f32_16x16x32_bf16 v[86:89], v[206:209], v[186:189], v[86:89]
	v_mfma_f32_16x16x32_bf16 v[82:85], v[214:217], v[186:189], v[82:85]
	v_mfma_f32_16x16x32_bf16 v[70:73], v[206:209], v[198:201], v[70:73]
	v_mfma_f32_16x16x32_bf16 v[66:69], v[214:217], v[198:201], v[66:69]
	s_setprio 0
	s_barrier
	ds_read_b128 v[166:169], v148 offset:16384
	ds_read_b128 v[170:173], v148 offset:17408
	ds_read_b128 v[174:177], v148 offset:18432
	ds_read_b128 v[178:181], v148 offset:19456
	ds_read_b128 v[182:185], v148 offset:20480
	ds_read_b128 v[186:189], v148 offset:21504
	ds_read_b128 v[194:197], v148 offset:22528
	ds_read_b128 v[198:201], v148 offset:23552
	s_mov_b32 s60, m0
	s_mov_b32 m0, s35
	s_nop 0
	global_load_lds_dwordx4 v1, s[24:25]
	s_mov_b32 m0, s60
	s_add_u32 s60, s24, 0xb0000
	s_addc_u32 s61, s25, 0
	s_mov_b32 s62, m0
	s_mov_b32 m0, s38
	s_nop 0
	global_load_lds_dwordx4 v1, s[60:61]
	s_mov_b32 m0, s62
	s_barrier
	s_waitcnt lgkmcnt(0)
	s_setprio 1
	v_mfma_f32_16x16x32_bf16 v[62:65], v[150:153], v[166:169], v[62:65]
	v_mfma_f32_16x16x32_bf16 v[58:61], v[158:161], v[166:169], v[58:61]
	v_mfma_f32_16x16x32_bf16 v[46:49], v[150:153], v[174:177], v[46:49]
	v_mfma_f32_16x16x32_bf16 v[42:45], v[158:161], v[174:177], v[42:45]
	v_mfma_f32_16x16x32_bf16 v[30:33], v[150:153], v[182:185], v[30:33]
	v_mfma_f32_16x16x32_bf16 v[26:29], v[158:161], v[182:185], v[26:29]
	v_mfma_f32_16x16x32_bf16 v[14:17], v[150:153], v[194:197], v[14:17]
	v_mfma_f32_16x16x32_bf16 v[10:13], v[158:161], v[194:197], v[10:13]
	v_mfma_f32_16x16x32_bf16 v[62:65], v[154:157], v[170:173], v[62:65]
	v_mfma_f32_16x16x32_bf16 v[58:61], v[162:165], v[170:173], v[58:61]
	v_mfma_f32_16x16x32_bf16 v[46:49], v[154:157], v[178:181], v[46:49]
	v_mfma_f32_16x16x32_bf16 v[42:45], v[162:165], v[178:181], v[42:45]
	v_mfma_f32_16x16x32_bf16 v[30:33], v[154:157], v[186:189], v[30:33]
	v_mfma_f32_16x16x32_bf16 v[26:29], v[162:165], v[186:189], v[26:29]
	v_mfma_f32_16x16x32_bf16 v[14:17], v[154:157], v[198:201], v[14:17]
	v_mfma_f32_16x16x32_bf16 v[10:13], v[162:165], v[198:201], v[10:13]
	s_setprio 0
	s_barrier
; #define PG8_STAGE(bufoff, gbase, voff) do { _Pragma("unroll") for (int _i = 0; _i < 2; ++_i) glds16_s((const void*)((const char*)(gbase) + _i * r64), (voff), ldsb + (unsigned)(bufoff) + ldsw + _i * 8192u); } while (0)
; #define PG8_LDA(b, h) do { _Pragma("unroll") for (int m = 0; m < 4; ++m) { const int o_ = PG8_SA(b, h) + aoff + m * 2048; \
;         if constexpr (FP8) A8[m] = PG8_CAT8(o_); else { At[m][0] = PG8_LD16(o_); At[m][1] = PG8_LD16(o_ + 1024); } } } while (0)
; #define PG8_LDB(X, X8, b, h) do { _Pragma("unroll") for (int n = 0; n < 2; ++n) { const int o_ = PG8_SB(b, h) + boff + n * 2048; \
;         if constexpr (FP8) X8[n] = PG8_CAT8(o_); else { X[n][0] = PG8_LD16(o_); X[n][1] = PG8_LD16(o_ + 1024); } } } while (0)
; #define PG8_WAIT_V(n) asm volatile("s_waitcnt vmcnt(" #n ")" ::: "memory")
; #define PG8_WAIT_L(n) asm volatile("s_waitcnt lgkmcnt(" #n ")" ::: "memory")
; #define PG8_BAR __builtin_amdgcn_s_barrier()
; #define PG8_SCHED __builtin_amdgcn_sched_barrier(0)
; #define PG8_HI do { if constexpr (FP8) asm volatile("s_setprio 1"); } while (0)
; #define PG8_LO do { if constexpr (FP8) asm volatile("s_setprio 0"); } while (0)
; template <class Epi, class Sched, bool FP8 = false>
; __device__ __forceinline__ void gemm_phase(LAS unsigned char* lds, const int Kb, const int nt  , const Sched& S, const Epi& E) {
;     ...
;             PG8_STAGE(PG8_SB(0, 1), b2 + hstep, voffB);
;             PG8_WAIT_V(6); PG8_BAR; PG8_HI; PG8_MMA(1, 1, B1, B18); PG8_BAR; PG8_LO;
;             PG8_LDB(B0, B08, 1, 0); PG8_SCHED; PG8_LDA(1, 0); PG8_STAGE(PG8_SA(0, 1), a2 + hstep, voffA);
;             PG8_WAIT_L(8); PG8_BAR; PG8_HI; PG8_WAIT_L(0); PG8_MMA(0, 0, B0, B08); PG8_BAR; PG8_LO; PG8_SCHED;
;             PG8_LDB(B1, B18, 1, 1); PG8_STAGE(PG8_SB(1, 0), b3, voffB);
;             PG8_BAR; PG8_HI; PG8_WAIT_L(0); PG8_MMA(0, 1, B1, B18); PG8_BAR; PG8_LO;
;             PG8_LDA(1, 1); PG8_STAGE(PG8_SA(1, 0), a3, voffA);
	s_add_u32 s60, s22, 0x160000
	s_addc_u32 s61, s23, 0
	s_mov_b32 s62, m0
	s_mov_b32 m0, s39
	s_nop 0
	global_load_lds_dwordx4 v1, s[60:61]
	s_mov_b32 m0, s62
	s_add_u32 s60, s22, 0x210000
	s_addc_u32 s61, s23, 0
	s_mov_b32 s62, m0
	s_mov_b32 m0, s40
	s_nop 0
	global_load_lds_dwordx4 v1, s[60:61]
	s_mov_b32 m0, s62
	s_waitcnt vmcnt(6)
	s_barrier
	s_setprio 1
	v_mfma_f32_16x16x32_bf16 v[54:57], v[202:205], v[166:169], v[54:57]
	v_mfma_f32_16x16x32_bf16 v[50:53], v[210:213], v[166:169], v[50:53]
	v_mfma_f32_16x16x32_bf16 v[38:41], v[202:205], v[174:177], v[38:41]
	v_mfma_f32_16x16x32_bf16 v[34:37], v[210:213], v[174:177], v[34:37]
	v_mfma_f32_16x16x32_bf16 v[22:25], v[202:205], v[182:185], v[22:25]
	v_mfma_f32_16x16x32_bf16 v[18:21], v[210:213], v[182:185], v[18:21]
	v_mfma_f32_16x16x32_bf16 v[6:9], v[202:205], v[194:197], v[6:9]
	v_mfma_f32_16x16x32_bf16 v[2:5], v[210:213], v[194:197], v[2:5]
	v_mfma_f32_16x16x32_bf16 v[54:57], v[206:209], v[170:173], v[54:57]
	v_mfma_f32_16x16x32_bf16 v[50:53], v[214:217], v[170:173], v[50:53]
	v_mfma_f32_16x16x32_bf16 v[38:41], v[206:209], v[178:181], v[38:41]
	v_mfma_f32_16x16x32_bf16 v[34:37], v[214:217], v[178:181], v[34:37]
	v_mfma_f32_16x16x32_bf16 v[22:25], v[206:209], v[186:189], v[22:25]
	v_mfma_f32_16x16x32_bf16 v[18:21], v[214:217], v[186:189], v[18:21]
	v_mfma_f32_16x16x32_bf16 v[6:9], v[206:209], v[198:201], v[6:9]
	v_mfma_f32_16x16x32_bf16 v[2:5], v[214:217], v[198:201], v[2:5]
	s_setprio 0
	s_barrier
	ds_read_b128 v[150:153], v140
	ds_read_b128 v[154:157], v141
	ds_read_b128 v[158:161], v142
	ds_read_b128 v[162:165], v143
	ds_read_b128 v[166:169], v148 offset:32768
	ds_read_b128 v[170:173], v148 offset:33792
	ds_read_b128 v[174:177], v148 offset:34816
	ds_read_b128 v[178:181], v148 offset:35840
	ds_read_b128 v[182:185], v148 offset:36864
	ds_read_b128 v[186:189], v148 offset:37888
	ds_read_b128 v[194:197], v148 offset:38912
	ds_read_b128 v[198:201], v148 offset:39936
	s_add_u32 s60, s24, 0x160000
	s_addc_u32 s61, s25, 0
	s_mov_b32 s62, m0
	s_mov_b32 m0, s41
	s_nop 0
	global_load_lds_dwordx4 v1, s[60:61]
	s_mov_b32 m0, s62
	s_add_u32 s60, s24, 0x210000
	s_addc_u32 s61, s25, 0
	s_mov_b32 s62, m0
	s_mov_b32 m0, s42
	s_nop 0
	global_load_lds_dwordx4 v1, s[60:61]
	s_mov_b32 m0, s62
	s_waitcnt lgkmcnt(8)
	s_barrier
	s_waitcnt lgkmcnt(0)
	s_setprio 1
	v_mfma_f32_16x16x32_bf16 v[126:129], v[150:153], v[166:169], v[126:129]
	v_mfma_f32_16x16x32_bf16 v[122:125], v[158:161], v[166:169], v[122:125]
	v_mfma_f32_16x16x32_bf16 v[110:113], v[150:153], v[174:177], v[110:113]
	v_mfma_f32_16x16x32_bf16 v[106:109], v[158:161], v[174:177], v[106:109]
	v_mfma_f32_16x16x32_bf16 v[94:97], v[150:153], v[182:185], v[94:97]
	v_mfma_f32_16x16x32_bf16 v[90:93], v[158:161], v[182:185], v[90:93]
	v_mfma_f32_16x16x32_bf16 v[78:81], v[150:153], v[194:197], v[78:81]
	v_mfma_f32_16x16x32_bf16 v[74:77], v[158:161], v[194:197], v[74:77]
	v_mfma_f32_16x16x32_bf16 v[126:129], v[154:157], v[170:173], v[126:129]
	v_mfma_f32_16x16x32_bf16 v[122:125], v[162:165], v[170:173], v[122:125]
	v_mfma_f32_16x16x32_bf16 v[110:113], v[154:157], v[178:181], v[110:113]
	v_mfma_f32_16x16x32_bf16 v[106:109], v[162:165], v[178:181], v[106:109]
	v_mfma_f32_16x16x32_bf16 v[94:97], v[154:157], v[186:189], v[94:97]
	v_mfma_f32_16x16x32_bf16 v[90:93], v[162:165], v[186:189], v[90:93]
	v_mfma_f32_16x16x32_bf16 v[78:81], v[154:157], v[198:201], v[78:81]
	v_mfma_f32_16x16x32_bf16 v[74:77], v[162:165], v[198:201], v[74:77]
	s_setprio 0
	s_barrier
	ds_read_b128 v[202:205], v144
	ds_read_b128 v[206:209], v145
	ds_read_b128 v[210:213], v146
	ds_read_b128 v[214:217], v147
	s_add_u32 s60, s22, 0x80
	s_addc_u32 s61, s23, 0
	s_mov_b32 s62, m0
	s_mov_b32 m0, s45
	s_nop 0
	global_load_lds_dwordx4 v1, s[60:61]
	s_mov_b32 m0, s62
	s_add_u32 s60, s22, 0xb0080
	s_addc_u32 s61, s23, 0
	s_mov_b32 s62, m0
	s_mov_b32 m0, s46
	s_nop 0
	global_load_lds_dwordx4 v1, s[60:61]
	s_mov_b32 m0, s62
	s_barrier
	s_waitcnt lgkmcnt(0)
	s_setprio 1
	v_mfma_f32_16x16x32_bf16 v[118:121], v[202:205], v[166:169], v[118:121]
	v_mfma_f32_16x16x32_bf16 v[114:117], v[210:213], v[166:169], v[114:117]
	v_mfma_f32_16x16x32_bf16 v[102:105], v[202:205], v[174:177], v[102:105]
	v_mfma_f32_16x16x32_bf16 v[98:101], v[210:213], v[174:177], v[98:101]
	v_mfma_f32_16x16x32_bf16 v[86:89], v[202:205], v[182:185], v[86:89]
	v_mfma_f32_16x16x32_bf16 v[82:85], v[210:213], v[182:185], v[82:85]
	v_mfma_f32_16x16x32_bf16 v[70:73], v[202:205], v[194:197], v[70:73]
	v_mfma_f32_16x16x32_bf16 v[66:69], v[210:213], v[194:197], v[66:69]
	v_mfma_f32_16x16x32_bf16 v[118:121], v[206:209], v[170:173], v[118:121]
	v_mfma_f32_16x16x32_bf16 v[114:117], v[214:217], v[170:173], v[114:117]
	v_mfma_f32_16x16x32_bf16 v[102:105], v[206:209], v[178:181], v[102:105]
	v_mfma_f32_16x16x32_bf16 v[98:101], v[214:217], v[178:181], v[98:101]
	v_mfma_f32_16x16x32_bf16 v[86:89], v[206:209], v[186:189], v[86:89]
	v_mfma_f32_16x16x32_bf16 v[82:85], v[214:217], v[186:189], v[82:85]
	v_mfma_f32_16x16x32_bf16 v[70:73], v[206:209], v[198:201], v[70:73]
	v_mfma_f32_16x16x32_bf16 v[66:69], v[214:217], v[198:201], v[66:69]
	s_setprio 0
	s_barrier
	ds_read_b128 v[166:169], v148 offset:49152
	ds_read_b128 v[170:173], v148 offset:50176
	ds_read_b128 v[174:177], v148 offset:51200
	ds_read_b128 v[178:181], v148 offset:52224
	ds_read_b128 v[182:185], v148 offset:53248
	ds_read_b128 v[186:189], v148 offset:54272
	ds_read_b128 v[194:197], v148 offset:55296
	ds_read_b128 v[198:201], v148 offset:56320
	s_mov_b32 s60, m0
	s_mov_b32 m0, s47
	s_nop 0
	global_load_lds_dwordx4 v1, s[26:27]
	s_mov_b32 m0, s60
	s_add_u32 s24, s24, 0xb0080
	s_addc_u32 s25, s25, 0
	s_mov_b32 s26, m0
	s_mov_b32 m0, s48
	s_nop 0
	global_load_lds_dwordx4 v1, s[24:25]
	s_mov_b32 m0, s26
	s_barrier
; #define PG8_STAGE(bufoff, gbase, voff) do { _Pragma("unroll") for (int _i = 0; _i < 2; ++_i) glds16_s((const void*)((const char*)(gbase) + _i * r64), (voff), ldsb + (unsigned)(bufoff) + ldsw + _i * 8192u); } while (0)
; #define PG8_WAIT_V(n) asm volatile("s_waitcnt vmcnt(" #n ")" ::: "memory")
; #define PG8_WAIT_L(n) asm volatile("s_waitcnt lgkmcnt(" #n ")" ::: "memory")
; #define PG8_BAR __builtin_amdgcn_s_barrier()
; #define PG8_SCHED __builtin_amdgcn_sched_barrier(0)
; #define PG8_HI do { if constexpr (FP8) asm volatile("s_setprio 1"); } while (0)
; #define PG8_LO do { if constexpr (FP8) asm volatile("s_setprio 0"); } while (0)
;     __device__ __forceinline__ void operator()(const f32x4 (&acc)[2][2][4][2], const Unit& u, int wr, int wc, int fr, int fq) const {
;     ...
;         for (int ai = 0; ai < 2; ++ai)
; #pragma unroll
;             for (int m = 0; m < 4; ++m) { const size_t off = (size_t)(row0 + ai * HALF + m * 16) * ldc + col0;
; #pragma unroll
;                 for (int bj = 0; bj < 2; ++bj)
; #pragma unroll
;                     for (int n = 0; n < 2; ++n) { f32x4 v = acc[ai][bj][m][n] * cs[bj][n];
;                         if (res) v += *(const f32x4*)(res + off + bj * HALF + n * 16);
;                         *(f32x4*)(out + off + bj * HALF + n * 16) = v; }
; template <class Epi, class Sched, bool FP8 = false>
; __device__ __forceinline__ void gemm_phase(LAS unsigned char* lds, const int Kb, const int nt  , const Sched& S, const Epi& E) {
;     ...
;             PG8_BAR; PG8_HI; PG8_WAIT_L(0); PG8_MMA(1, 0, B0, B08); PG8_BAR; PG8_LO; PG8_SCHED;
;             PG8_STAGE(PG8_SB(1, 1), b3 + hstep, voffB);
;             PG8_WAIT_V(6); PG8_BAR; PG8_HI; PG8_MMA(1, 1, B1, B18); PG8_BAR; PG8_LO;
;         }
;         { int l_; asm volatile("v_mbcnt_lo_u32_b32 %0, -1, 0\n\tv_mbcnt_hi_u32_b32 %0, -1, %0" : "=v"(l_));
;           E(acc, cur, wr, wc, l_ & 15, l_ >> 4); }
	s_waitcnt lgkmcnt(0)
	s_setprio 1
	v_mfma_f32_16x16x32_bf16 v[62:65], v[150:153], v[166:169], v[62:65]
	v_mfma_f32_16x16x32_bf16 v[58:61], v[158:161], v[166:169], v[58:61]
	v_mfma_f32_16x16x32_bf16 v[46:49], v[150:153], v[174:177], v[46:49]
	v_mfma_f32_16x16x32_bf16 v[42:45], v[158:161], v[174:177], v[42:45]
	v_mfma_f32_16x16x32_bf16 v[30:33], v[150:153], v[182:185], v[30:33]
	v_mfma_f32_16x16x32_bf16 v[26:29], v[158:161], v[182:185], v[26:29]
	v_mfma_f32_16x16x32_bf16 v[14:17], v[150:153], v[194:197], v[14:17]
	v_mfma_f32_16x16x32_bf16 v[10:13], v[158:161], v[194:197], v[10:13]
	v_mfma_f32_16x16x32_bf16 v[62:65], v[154:157], v[170:173], v[62:65]
	v_mfma_f32_16x16x32_bf16 v[58:61], v[162:165], v[170:173], v[58:61]
	v_mfma_f32_16x16x32_bf16 v[46:49], v[154:157], v[178:181], v[46:49]
	v_mfma_f32_16x16x32_bf16 v[42:45], v[162:165], v[178:181], v[42:45]
	v_mfma_f32_16x16x32_bf16 v[30:33], v[154:157], v[186:189], v[30:33]
	v_mfma_f32_16x16x32_bf16 v[26:29], v[162:165], v[186:189], v[26:29]
	v_mfma_f32_16x16x32_bf16 v[14:17], v[154:157], v[198:201], v[14:17]
	v_mfma_f32_16x16x32_bf16 v[10:13], v[162:165], v[198:201], v[10:13]
	s_setprio 0
	s_barrier
	s_add_u32 s24, s22, 0x160080
	s_addc_u32 s25, s23, 0
	s_mov_b32 s26, m0
	s_mov_b32 m0, s49
	s_nop 0
	global_load_lds_dwordx4 v1, s[24:25]
	s_mov_b32 m0, s26
	s_add_u32 s22, s22, 0x210080
	s_addc_u32 s23, s23, 0
	s_mov_b32 s24, m0
	s_mov_b32 m0, s50
	s_nop 0
	global_load_lds_dwordx4 v1, s[22:23]
	s_mov_b32 m0, s24
	s_waitcnt vmcnt(6)
	s_barrier
	s_setprio 1
	v_mfma_f32_16x16x32_bf16 v[54:57], v[202:205], v[166:169], v[54:57]
	v_mfma_f32_16x16x32_bf16 v[50:53], v[210:213], v[166:169], v[50:53]
	v_mfma_f32_16x16x32_bf16 v[38:41], v[202:205], v[174:177], v[38:41]
	v_mfma_f32_16x16x32_bf16 v[34:37], v[210:213], v[174:177], v[34:37]
	v_mfma_f32_16x16x32_bf16 v[22:25], v[202:205], v[182:185], v[22:25]
	v_mfma_f32_16x16x32_bf16 v[18:21], v[210:213], v[182:185], v[18:21]
	v_mfma_f32_16x16x32_bf16 v[6:9], v[202:205], v[194:197], v[6:9]
	v_mfma_f32_16x16x32_bf16 v[2:5], v[210:213], v[194:197], v[2:5]
	v_mfma_f32_16x16x32_bf16 v[54:57], v[206:209], v[170:173], v[54:57]
	v_mfma_f32_16x16x32_bf16 v[50:53], v[214:217], v[170:173], v[50:53]
	v_mfma_f32_16x16x32_bf16 v[38:41], v[206:209], v[178:181], v[38:41]
	v_mfma_f32_16x16x32_bf16 v[34:37], v[214:217], v[178:181], v[34:37]
	v_mfma_f32_16x16x32_bf16 v[22:25], v[206:209], v[186:189], v[22:25]
	v_mfma_f32_16x16x32_bf16 v[18:21], v[214:217], v[186:189], v[18:21]
	v_mfma_f32_16x16x32_bf16 v[6:9], v[206:209], v[198:201], v[6:9]
	v_mfma_f32_16x16x32_bf16 v[2:5], v[214:217], v[198:201], v[2:5]
	s_setprio 0
	s_add_i32 s59, s59, 2
	s_add_u32 s20, s20, 0x100
	s_addc_u32 s21, s21, 0
	s_add_u32 s57, s57, 0x100
	s_addc_u32 s58, s58, 0
	s_cmpk_gt_u32 s59, 0x55
	s_barrier
	s_cbranch_scc0 .LBB0_2043
	s_lshl_b32 s20, s55, 8
	v_mbcnt_lo_u32_b32 v130, -1, 0
	v_mbcnt_hi_u32_b32 v130, -1, v130
	s_add_i32 s20, s20, s43
	s_lshl_b32 s21, s56, 8
	v_ashrrev_i32_e32 v131, 2, v130
	s_or_b32 s21, s21, s44
	v_and_b32_e32 v131, -4, v131
	v_and_or_b32 v168, v130, 15, s20
	v_add_u32_e32 v166, s21, v131
	v_ashrrev_i32_e32 v169, 31, v168
	v_ashrrev_i32_e32 v167, 31, v166
	v_lshlrev_b64 v[130:131], 11, v[168:169]
	v_lshl_add_u64 v[130:131], v[130:131], 0, v[166:167]
	v_lshlrev_b64 v[130:131], 2, v[130:131]
	v_lshl_add_u64 v[162:163], s[4:5], 0, v[130:131]
	global_load_dwordx4 v[150:153], v[162:163], off
	global_load_dwordx4 v[154:157], v[162:163], off offset:64
	global_load_dwordx4 v[158:161], v[162:163], off offset:512
	s_nop 0
	global_load_dwordx4 v[162:165], v[162:163], off offset:576
	v_or_b32_e32 v170, 16, v168
	v_ashrrev_i32_e32 v171, 31, v170
	v_lshlrev_b64 v[170:171], 11, v[170:171]
	v_lshl_add_u64 v[170:171], v[170:171], 0, v[166:167]
	v_lshl_add_u64 v[172:173], s[6:7], 0, v[130:131]
	v_lshlrev_b64 v[170:171], 2, v[170:171]
	v_lshl_add_u64 v[174:175], s[4:5], 0, v[170:171]
	s_and_b64 vcc, exec, s[14:15]
	s_mov_b32 s56, s54
	s_mov_b32 s55, s53
	s_mov_b64 s[22:23], s[18:19]
	s_mov_b64 s[20:21], s[16:17]
	s_waitcnt vmcnt(3)
	v_pk_add_f32 v[128:129], v[128:129], v[152:153]
	v_pk_add_f32 v[126:127], v[126:127], v[150:151]
	s_waitcnt vmcnt(2)
	v_pk_add_f32 v[124:125], v[124:125], v[156:157]
	v_pk_add_f32 v[122:123], v[122:123], v[154:155]
	s_waitcnt vmcnt(1)
	v_pk_add_f32 v[120:121], v[120:121], v[160:161]
	v_pk_add_f32 v[118:119], v[118:119], v[158:159]
	s_waitcnt vmcnt(0)
	v_pk_add_f32 v[116:117], v[116:117], v[164:165]
	v_pk_add_f32 v[114:115], v[114:115], v[162:163]
	global_store_dwordx4 v[172:173], v[126:129], off
	global_store_dwordx4 v[172:173], v[122:125], off offset:64
	global_store_dwordx4 v[172:173], v[118:121], off offset:512
	global_store_dwordx4 v[172:173], v[114:117], off offset:576
	global_load_dwordx4 v[114:117], v[174:175], off
	global_load_dwordx4 v[118:121], v[174:175], off offset:64
	global_load_dwordx4 v[122:125], v[174:175], off offset:512
	global_load_dwordx4 v[126:129], v[174:175], off offset:576
	v_or_b32_e32 v150, 32, v168
	v_ashrrev_i32_e32 v151, 31, v150
	v_lshlrev_b64 v[150:151], 11, v[150:151]
	v_lshl_add_u64 v[150:151], v[150:151], 0, v[166:167]
	v_lshl_add_u64 v[152:153], s[6:7], 0, v[170:171]
	v_lshlrev_b64 v[150:151], 2, v[150:151]
	v_lshl_add_u64 v[154:155], s[4:5], 0, v[150:151]
	s_waitcnt vmcnt(3)
	v_pk_add_f32 v[112:113], v[112:113], v[116:117]
	v_pk_add_f32 v[110:111], v[110:111], v[114:115]
	s_waitcnt vmcnt(2)
	v_pk_add_f32 v[108:109], v[108:109], v[120:121]
	v_pk_add_f32 v[106:107], v[106:107], v[118:119]
	s_waitcnt vmcnt(1)
	v_pk_add_f32 v[104:105], v[104:105], v[124:125]
	v_pk_add_f32 v[102:103], v[102:103], v[122:123]
	s_waitcnt vmcnt(0)
; #define PG8_WAIT_V(n) asm volatile("s_waitcnt vmcnt(" #n ")" ::: "memory")
; #define PG8_BAR __builtin_amdgcn_s_barrier()
;     __device__ __forceinline__ void operator()(const f32x4 (&acc)[2][2][4][2], const Unit& u, int wr, int wc, int fr, int fq) const {
;     ...
;         for (int ai = 0; ai < 2; ++ai)
; #pragma unroll
;             for (int m = 0; m < 4; ++m) { const size_t off = (size_t)(row0 + ai * HALF + m * 16) * ldc + col0;
; #pragma unroll
;                 for (int bj = 0; bj < 2; ++bj)
; #pragma unroll
;                     for (int n = 0; n < 2; ++n) { f32x4 v = acc[ai][bj][m][n] * cs[bj][n];
;                         if (res) v += *(const f32x4*)(res + off + bj * HALF + n * 16);
;                         *(f32x4*)(out + off + bj * HALF + n * 16) = v; }
;                 asm volatile("" ::: "memory"); }
;     }
; template <class Epi, class Sched, bool FP8 = false>
; __device__ __forceinline__ void gemm_phase(LAS unsigned char* lds, const int Kb, const int nt  , const Sched& S, const Epi& E) {
;     ...
;         if (!has_next) break;
; #pragma unroll
;         for (int a = 0; a < 2; ++a)
; #pragma unroll
;             for (int b = 0; b < 2; ++b)
; #pragma unroll
;                 for (int m = 0; m < 4; ++m)
; #pragma unroll
;                     for (int n = 0; n < 2; ++n) acc[a][b][m][n] = (f32x4){0.f, 0.f, 0.f, 0.f};
;         cur = nxt; cA = nA; cB = nB; ++ui;
;     }
;     PG8_WAIT_V(0);
;     if (wr == 0) PG8_BAR;
;     PG8_BAR;
	v_pk_add_f32 v[100:101], v[100:101], v[128:129]
	v_pk_add_f32 v[98:99], v[98:99], v[126:127]
	global_store_dwordx4 v[152:153], v[110:113], off
	global_store_dwordx4 v[152:153], v[106:109], off offset:64
	global_store_dwordx4 v[152:153], v[102:105], off offset:512
	global_store_dwordx4 v[152:153], v[98:101], off offset:576
	global_load_dwordx4 v[98:101], v[154:155], off
	global_load_dwordx4 v[102:105], v[154:155], off offset:64
	global_load_dwordx4 v[106:109], v[154:155], off offset:512
	global_load_dwordx4 v[110:113], v[154:155], off offset:576
	v_or_b32_e32 v114, 48, v168
	v_ashrrev_i32_e32 v115, 31, v114
	v_lshlrev_b64 v[114:115], 11, v[114:115]
	v_lshl_add_u64 v[114:115], v[114:115], 0, v[166:167]
	v_lshl_add_u64 v[116:117], s[6:7], 0, v[150:151]
	v_lshlrev_b64 v[114:115], 2, v[114:115]
	v_lshl_add_u64 v[118:119], s[4:5], 0, v[114:115]
	s_waitcnt vmcnt(3)
	v_pk_add_f32 v[96:97], v[96:97], v[100:101]
	v_pk_add_f32 v[94:95], v[94:95], v[98:99]
	s_waitcnt vmcnt(2)
	v_pk_add_f32 v[92:93], v[92:93], v[104:105]
	v_pk_add_f32 v[90:91], v[90:91], v[102:103]
	s_waitcnt vmcnt(1)
	v_pk_add_f32 v[88:89], v[88:89], v[108:109]
	v_pk_add_f32 v[86:87], v[86:87], v[106:107]
	s_waitcnt vmcnt(0)
	v_pk_add_f32 v[84:85], v[84:85], v[112:113]
	v_pk_add_f32 v[82:83], v[82:83], v[110:111]
	global_store_dwordx4 v[116:117], v[94:97], off
	global_store_dwordx4 v[116:117], v[90:93], off offset:64
	global_store_dwordx4 v[116:117], v[86:89], off offset:512
	global_store_dwordx4 v[116:117], v[82:85], off offset:576
	global_load_dwordx4 v[82:85], v[118:119], off
	global_load_dwordx4 v[86:89], v[118:119], off offset:64
	global_load_dwordx4 v[90:93], v[118:119], off offset:512
	global_load_dwordx4 v[94:97], v[118:119], off offset:576
	v_lshl_add_u64 v[100:101], s[6:7], 0, v[114:115]
	v_lshl_add_u64 v[98:99], v[130:131], 0, s[8:9]
	v_lshl_add_u64 v[102:103], s[4:5], 0, v[98:99]
	s_waitcnt vmcnt(3)
	v_pk_add_f32 v[80:81], v[80:81], v[84:85]
	v_pk_add_f32 v[78:79], v[78:79], v[82:83]
	s_waitcnt vmcnt(2)
	v_pk_add_f32 v[76:77], v[76:77], v[88:89]
	v_pk_add_f32 v[74:75], v[74:75], v[86:87]
	s_waitcnt vmcnt(1)
	v_pk_add_f32 v[72:73], v[72:73], v[92:93]
	v_pk_add_f32 v[70:71], v[70:71], v[90:91]
	s_waitcnt vmcnt(0)
	v_pk_add_f32 v[68:69], v[68:69], v[96:97]
	v_pk_add_f32 v[66:67], v[66:67], v[94:95]
	global_store_dwordx4 v[100:101], v[78:81], off
	global_store_dwordx4 v[100:101], v[74:77], off offset:64
	global_store_dwordx4 v[100:101], v[70:73], off offset:512
	global_store_dwordx4 v[100:101], v[66:69], off offset:576
	global_load_dwordx4 v[66:69], v[102:103], off
	global_load_dwordx4 v[70:73], v[102:103], off offset:64
	global_load_dwordx4 v[74:77], v[102:103], off offset:512
	global_load_dwordx4 v[78:81], v[102:103], off offset:576
	v_lshl_add_u64 v[84:85], s[6:7], 0, v[98:99]
	v_lshl_add_u64 v[82:83], v[130:131], 0, s[10:11]
	v_lshl_add_u64 v[86:87], s[4:5], 0, v[82:83]
	s_waitcnt vmcnt(3)
	v_pk_add_f32 v[64:65], v[64:65], v[68:69]
	v_pk_add_f32 v[62:63], v[62:63], v[66:67]
	s_waitcnt vmcnt(2)
	v_pk_add_f32 v[60:61], v[60:61], v[72:73]
	v_pk_add_f32 v[58:59], v[58:59], v[70:71]
	s_waitcnt vmcnt(1)
	v_pk_add_f32 v[56:57], v[56:57], v[76:77]
	v_pk_add_f32 v[54:55], v[54:55], v[74:75]
	s_waitcnt vmcnt(0)
	v_pk_add_f32 v[52:53], v[52:53], v[80:81]
	v_pk_add_f32 v[50:51], v[50:51], v[78:79]
	global_store_dwordx4 v[84:85], v[62:65], off
	global_store_dwordx4 v[84:85], v[58:61], off offset:64
	global_store_dwordx4 v[84:85], v[54:57], off offset:512
	global_store_dwordx4 v[84:85], v[50:53], off offset:576
	global_load_dwordx4 v[50:53], v[86:87], off
	global_load_dwordx4 v[54:57], v[86:87], off offset:64
	global_load_dwordx4 v[58:61], v[86:87], off offset:512
	global_load_dwordx4 v[62:65], v[86:87], off offset:576
	v_lshl_add_u64 v[68:69], s[6:7], 0, v[82:83]
	v_lshl_add_u64 v[66:67], v[130:131], 0, s[12:13]
	v_lshl_add_u64 v[70:71], s[4:5], 0, v[66:67]
	s_waitcnt vmcnt(3)
	v_pk_add_f32 v[48:49], v[48:49], v[52:53]
	v_pk_add_f32 v[46:47], v[46:47], v[50:51]
	s_waitcnt vmcnt(2)
	v_pk_add_f32 v[44:45], v[44:45], v[56:57]
	v_pk_add_f32 v[42:43], v[42:43], v[54:55]
	s_waitcnt vmcnt(1)
	v_pk_add_f32 v[40:41], v[40:41], v[60:61]
	v_pk_add_f32 v[38:39], v[38:39], v[58:59]
	s_waitcnt vmcnt(0)
	v_pk_add_f32 v[36:37], v[36:37], v[64:65]
	v_pk_add_f32 v[34:35], v[34:35], v[62:63]
	global_store_dwordx4 v[68:69], v[46:49], off
	global_store_dwordx4 v[68:69], v[42:45], off offset:64
	global_store_dwordx4 v[68:69], v[38:41], off offset:512
	global_store_dwordx4 v[68:69], v[34:37], off offset:576
	global_load_dwordx4 v[34:37], v[70:71], off
	global_load_dwordx4 v[38:41], v[70:71], off offset:64
	global_load_dwordx4 v[42:45], v[70:71], off offset:512
	global_load_dwordx4 v[46:49], v[70:71], off offset:576
	v_lshl_add_u64 v[52:53], s[6:7], 0, v[66:67]
	v_lshl_add_u64 v[50:51], v[130:131], 0, s[2:3]
	v_lshl_add_u64 v[54:55], s[4:5], 0, v[50:51]
	s_waitcnt vmcnt(3)
	v_pk_add_f32 v[32:33], v[32:33], v[36:37]
	v_pk_add_f32 v[30:31], v[30:31], v[34:35]
	s_waitcnt vmcnt(2)
	v_pk_add_f32 v[28:29], v[28:29], v[40:41]
	v_pk_add_f32 v[26:27], v[26:27], v[38:39]
	s_waitcnt vmcnt(1)
	v_pk_add_f32 v[24:25], v[24:25], v[44:45]
	v_pk_add_f32 v[22:23], v[22:23], v[42:43]
	s_waitcnt vmcnt(0)
	v_pk_add_f32 v[20:21], v[20:21], v[48:49]
	v_pk_add_f32 v[18:19], v[18:19], v[46:47]
	global_store_dwordx4 v[52:53], v[30:33], off
	global_store_dwordx4 v[52:53], v[26:29], off offset:64
	global_store_dwordx4 v[52:53], v[22:25], off offset:512
	global_store_dwordx4 v[52:53], v[18:21], off offset:576
	global_load_dwordx4 v[18:21], v[54:55], off
	global_load_dwordx4 v[22:25], v[54:55], off offset:64
	global_load_dwordx4 v[26:29], v[54:55], off offset:512
	global_load_dwordx4 v[30:33], v[54:55], off offset:576
	v_lshl_add_u64 v[34:35], s[6:7], 0, v[50:51]
	s_waitcnt vmcnt(3)
	v_pk_add_f32 v[16:17], v[16:17], v[20:21]
	v_pk_add_f32 v[14:15], v[14:15], v[18:19]
	s_waitcnt vmcnt(2)
	v_pk_add_f32 v[12:13], v[12:13], v[24:25]
	v_pk_add_f32 v[10:11], v[10:11], v[22:23]
	s_waitcnt vmcnt(1)
	v_pk_add_f32 v[8:9], v[8:9], v[28:29]
	v_pk_add_f32 v[6:7], v[6:7], v[26:27]
	s_waitcnt vmcnt(0)
	v_pk_add_f32 v[4:5], v[4:5], v[32:33]
	v_pk_add_f32 v[2:3], v[2:3], v[30:31]
	global_store_dwordx4 v[34:35], v[14:17], off
	global_store_dwordx4 v[34:35], v[10:13], off offset:64
	global_store_dwordx4 v[34:35], v[6:9], off offset:512
	global_store_dwordx4 v[34:35], v[2:5], off offset:576
	s_cbranch_vccz .LBB0_2036
	s_waitcnt vmcnt(0)
	s_cmpk_gt_u32 s28, 0xff
	s_cbranch_scc1 .LBB0_2047
	s_barrier

; #define PG8_STAGE(bufoff, gbase, voff) do { _Pragma("unroll") for (int _i = 0; _i < 2; ++_i) glds16_s((const void*)((const char*)(gbase) + _i * r64), (voff), ldsb + (unsigned)(bufoff) + ldsw + _i * 8192u); } while (0)
; #define PG8_LDA(b, h) do { _Pragma("unroll") for (int m = 0; m < 4; ++m) { const int o_ = PG8_SA(b, h) + aoff + m * 2048; \
;         if constexpr (FP8) A8[m] = PG8_CAT8(o_); else { At[m][0] = PG8_LD16(o_); At[m][1] = PG8_LD16(o_ + 1024); } } } while (0)
; #define PG8_LDB(X, X8, b, h) do { _Pragma("unroll") for (int n = 0; n < 2; ++n) { const int o_ = PG8_SB(b, h) + boff + n * 2048; \
;         if constexpr (FP8) X8[n] = PG8_CAT8(o_); else { X[n][0] = PG8_LD16(o_); X[n][1] = PG8_LD16(o_ + 1024); } } } while (0)
; #define PG8_WAIT_L(n) asm volatile("s_waitcnt lgkmcnt(" #n ")" ::: "memory")
; #define PG8_BAR __builtin_amdgcn_s_barrier()
; #define PG8_SCHED __builtin_amdgcn_sched_barrier(0)
; #define PG8_HI do { if constexpr (FP8) asm volatile("s_setprio 1"); } while (0)
; #define PG8_LO do { if constexpr (FP8) asm volatile("s_setprio 0"); } while (0)
; template <class Epi, class Sched, bool FP8 = false>
; __device__ __forceinline__ void gemm_phase(LAS unsigned char* lds, const int Kb, const int nt  , const Sched& S, const Epi& E) {
;     ...
;         for (int t = 0; t < nt; t += 2) {
;             const bool last = (t == nt - 2);
;             const char* a1 = cA + (size_t)(t + 1) * kstep;
;             const char* a2 = last ? nA : cA + (size_t)(t + 2) * kstep; const char* b2 = last ? nB : cB + (size_t)(t + 2) * kstep;
;             const char* a3 = a2 + kstep; const char* b3 = b2 + kstep;
;             PG8_LDB(B0, B08, 0, 0); PG8_SCHED; PG8_LDA(0, 0); PG8_STAGE(PG8_SA(1, 1), a1 + hstep, voffA);
;             PG8_WAIT_L(8); PG8_BAR; PG8_HI; PG8_WAIT_L(0); PG8_MMA(0, 0, B0, B08); PG8_BAR; PG8_LO; PG8_SCHED;
;             PG8_LDB(B1, B18, 0, 1); PG8_STAGE(PG8_SB(0, 0), b2, voffB);
;             PG8_BAR; PG8_HI; PG8_WAIT_L(0); PG8_MMA(0, 1, B1, B18); PG8_BAR; PG8_LO;
;             PG8_LDA(0, 1); PG8_STAGE(PG8_SA(0, 0), a2, voffA);
;             PG8_BAR; PG8_HI; PG8_WAIT_L(0); PG8_MMA(1, 0, B0, B08); PG8_BAR; PG8_LO; PG8_SCHED;
.LBB0_2332:
	ds_read_b128 v[130:133], v150
	ds_read_b128 v[134:137], v151
	ds_read_b128 v[138:141], v152
	ds_read_b128 v[142:145], v153
	s_add_u32 s28, s0, 0x100
	s_addc_u32 s29, s1, 0
	s_cmp_eq_u32 s63, 4
	s_cselect_b32 s34, s22, s28
	s_cselect_b32 s35, s23, s29
	s_cselect_b32 s30, s24, s21
	s_cselect_b32 s31, s25, s62
	s_add_u32 s36, s34, 0x80
	s_addc_u32 s37, s35, 0
	ds_read_b128 v[146:149], v166
	ds_read_b128 v[168:171], v166 offset:1024
	ds_read_b128 v[172:175], v166 offset:2048
	ds_read_b128 v[176:179], v166 offset:3072
	ds_read_b128 v[180:183], v166 offset:4096
	ds_read_b128 v[184:187], v166 offset:5120
	ds_read_b128 v[194:197], v166 offset:6144
	ds_read_b128 v[198:201], v166 offset:7168
	s_add_u32 s64, s0, 0x20080
	s_addc_u32 s65, s1, 0
	s_mov_b32 s66, m0
	s_mov_b32 m0, s58
	s_nop 0
	global_load_lds_dwordx4 v1, s[64:65]
	s_mov_b32 m0, s66
	s_add_u32 s0, s0, 0x30080
	s_addc_u32 s1, s1, 0
	s_mov_b32 s64, m0
	s_mov_b32 m0, s59
	s_nop 0
	global_load_lds_dwordx4 v1, s[0:1]
	s_mov_b32 m0, s64
	s_waitcnt lgkmcnt(8)
	s_barrier
	s_waitcnt lgkmcnt(0)
	s_setprio 1
	v_mfma_f32_16x16x32_bf16 v[126:129], v[130:133], v[146:149], v[126:129]
	v_mfma_f32_16x16x32_bf16 v[122:125], v[138:141], v[146:149], v[122:125]
	v_mfma_f32_16x16x32_bf16 v[110:113], v[130:133], v[172:175], v[110:113]
	v_mfma_f32_16x16x32_bf16 v[106:109], v[138:141], v[172:175], v[106:109]
	v_mfma_f32_16x16x32_bf16 v[94:97], v[130:133], v[180:183], v[94:97]
	v_mfma_f32_16x16x32_bf16 v[90:93], v[138:141], v[180:183], v[90:93]
	v_mfma_f32_16x16x32_bf16 v[78:81], v[130:133], v[194:197], v[78:81]
	v_mfma_f32_16x16x32_bf16 v[74:77], v[138:141], v[194:197], v[74:77]
	v_mfma_f32_16x16x32_bf16 v[126:129], v[134:137], v[168:171], v[126:129]
	v_mfma_f32_16x16x32_bf16 v[122:125], v[142:145], v[168:171], v[122:125]
	v_mfma_f32_16x16x32_bf16 v[110:113], v[134:137], v[176:179], v[110:113]
	v_mfma_f32_16x16x32_bf16 v[106:109], v[142:145], v[176:179], v[106:109]
	v_mfma_f32_16x16x32_bf16 v[94:97], v[134:137], v[184:187], v[94:97]
	v_mfma_f32_16x16x32_bf16 v[90:93], v[142:145], v[184:187], v[90:93]
	v_mfma_f32_16x16x32_bf16 v[78:81], v[134:137], v[198:201], v[78:81]
	v_mfma_f32_16x16x32_bf16 v[74:77], v[142:145], v[198:201], v[74:77]
	s_setprio 0
	s_barrier
	ds_read_b128 v[202:205], v154
	ds_read_b128 v[206:209], v155
	ds_read_b128 v[210:213], v156
	ds_read_b128 v[214:217], v157
	s_mov_b32 s0, m0
	s_mov_b32 m0, s43
	s_nop 0
	global_load_lds_dwordx4 v1, s[30:31]
	s_mov_b32 m0, s0
	s_add_u32 s0, s30, 0x10000
	s_addc_u32 s1, s31, 0
	s_mov_b32 s64, m0
	s_mov_b32 m0, s44
	s_nop 0
	global_load_lds_dwordx4 v1, s[0:1]
	s_mov_b32 m0, s64
	s_barrier
	s_waitcnt lgkmcnt(0)
	s_setprio 1
	v_mfma_f32_16x16x32_bf16 v[118:121], v[202:205], v[146:149], v[118:121]
	v_mfma_f32_16x16x32_bf16 v[114:117], v[210:213], v[146:149], v[114:117]
	v_mfma_f32_16x16x32_bf16 v[102:105], v[202:205], v[172:175], v[102:105]
	v_mfma_f32_16x16x32_bf16 v[98:101], v[210:213], v[172:175], v[98:101]
	v_mfma_f32_16x16x32_bf16 v[86:89], v[202:205], v[180:183], v[86:89]
	v_mfma_f32_16x16x32_bf16 v[82:85], v[210:213], v[180:183], v[82:85]
	v_mfma_f32_16x16x32_bf16 v[70:73], v[202:205], v[194:197], v[70:73]
	v_mfma_f32_16x16x32_bf16 v[66:69], v[210:213], v[194:197], v[66:69]
	v_mfma_f32_16x16x32_bf16 v[118:121], v[206:209], v[168:171], v[118:121]
	v_mfma_f32_16x16x32_bf16 v[114:117], v[214:217], v[168:171], v[114:117]
	v_mfma_f32_16x16x32_bf16 v[102:105], v[206:209], v[176:179], v[102:105]
	v_mfma_f32_16x16x32_bf16 v[98:101], v[214:217], v[176:179], v[98:101]
	v_mfma_f32_16x16x32_bf16 v[86:89], v[206:209], v[184:187], v[86:89]
	v_mfma_f32_16x16x32_bf16 v[82:85], v[214:217], v[184:187], v[82:85]
	v_mfma_f32_16x16x32_bf16 v[70:73], v[206:209], v[198:201], v[70:73]
	v_mfma_f32_16x16x32_bf16 v[66:69], v[214:217], v[198:201], v[66:69]
	s_setprio 0
	s_barrier
	ds_read_b128 v[146:149], v166 offset:16384
	ds_read_b128 v[168:171], v166 offset:17408
	ds_read_b128 v[172:175], v166 offset:18432
	ds_read_b128 v[176:179], v166 offset:19456
	ds_read_b128 v[180:183], v166 offset:20480
	ds_read_b128 v[184:187], v166 offset:21504
	ds_read_b128 v[194:197], v166 offset:22528
	ds_read_b128 v[198:201], v166 offset:23552
	s_mov_b32 s0, m0
	s_mov_b32 m0, s42
	s_nop 0
	global_load_lds_dwordx4 v1, s[34:35]
	s_mov_b32 m0, s0
	s_add_u32 s0, s34, 0x10000
	s_addc_u32 s1, s35, 0
	s_mov_b32 s64, m0
	s_mov_b32 m0, s45
	s_nop 0
	global_load_lds_dwordx4 v1, s[0:1]
	s_mov_b32 m0, s64
	s_barrier
	s_waitcnt lgkmcnt(0)
	s_setprio 1
	v_mfma_f32_16x16x32_bf16 v[62:65], v[130:133], v[146:149], v[62:65]
	v_mfma_f32_16x16x32_bf16 v[58:61], v[138:141], v[146:149], v[58:61]
	v_mfma_f32_16x16x32_bf16 v[46:49], v[130:133], v[172:175], v[46:49]
	v_mfma_f32_16x16x32_bf16 v[42:45], v[138:141], v[172:175], v[42:45]
	v_mfma_f32_16x16x32_bf16 v[30:33], v[130:133], v[180:183], v[30:33]
	v_mfma_f32_16x16x32_bf16 v[26:29], v[138:141], v[180:183], v[26:29]
	v_mfma_f32_16x16x32_bf16 v[14:17], v[130:133], v[194:197], v[14:17]
	v_mfma_f32_16x16x32_bf16 v[10:13], v[138:141], v[194:197], v[10:13]
	v_mfma_f32_16x16x32_bf16 v[62:65], v[134:137], v[168:171], v[62:65]
	v_mfma_f32_16x16x32_bf16 v[58:61], v[142:145], v[168:171], v[58:61]
	v_mfma_f32_16x16x32_bf16 v[46:49], v[134:137], v[176:179], v[46:49]
	v_mfma_f32_16x16x32_bf16 v[42:45], v[142:145], v[176:179], v[42:45]
	v_mfma_f32_16x16x32_bf16 v[30:33], v[134:137], v[184:187], v[30:33]
	v_mfma_f32_16x16x32_bf16 v[26:29], v[142:145], v[184:187], v[26:29]
	v_mfma_f32_16x16x32_bf16 v[14:17], v[134:137], v[198:201], v[14:17]
	v_mfma_f32_16x16x32_bf16 v[10:13], v[142:145], v[198:201], v[10:13]
	s_setprio 0
	s_barrier
; #define PG8_STAGE(bufoff, gbase, voff) do { _Pragma("unroll") for (int _i = 0; _i < 2; ++_i) glds16_s((const void*)((const char*)(gbase) + _i * r64), (voff), ldsb + (unsigned)(bufoff) + ldsw + _i * 8192u); } while (0)
; #define PG8_LDA(b, h) do { _Pragma("unroll") for (int m = 0; m < 4; ++m) { const int o_ = PG8_SA(b, h) + aoff + m * 2048; \
;         if constexpr (FP8) A8[m] = PG8_CAT8(o_); else { At[m][0] = PG8_LD16(o_); At[m][1] = PG8_LD16(o_ + 1024); } } } while (0)
; #define PG8_LDB(X, X8, b, h) do { _Pragma("unroll") for (int n = 0; n < 2; ++n) { const int o_ = PG8_SB(b, h) + boff + n * 2048; \
;         if constexpr (FP8) X8[n] = PG8_CAT8(o_); else { X[n][0] = PG8_LD16(o_); X[n][1] = PG8_LD16(o_ + 1024); } } } while (0)
; #define PG8_WAIT_V(n) asm volatile("s_waitcnt vmcnt(" #n ")" ::: "memory")
; #define PG8_WAIT_L(n) asm volatile("s_waitcnt lgkmcnt(" #n ")" ::: "memory")
; #define PG8_BAR __builtin_amdgcn_s_barrier()
; #define PG8_SCHED __builtin_amdgcn_sched_barrier(0)
; #define PG8_HI do { if constexpr (FP8) asm volatile("s_setprio 1"); } while (0)
; #define PG8_LO do { if constexpr (FP8) asm volatile("s_setprio 0"); } while (0)
; template <class Epi, class Sched, bool FP8 = false>
; __device__ __forceinline__ void gemm_phase(LAS unsigned char* lds, const int Kb, const int nt  , const Sched& S, const Epi& E) {
;     ...
;             PG8_STAGE(PG8_SB(0, 1), b2 + hstep, voffB);
;             PG8_WAIT_V(6); PG8_BAR; PG8_HI; PG8_MMA(1, 1, B1, B18); PG8_BAR; PG8_LO;
;             PG8_LDB(B0, B08, 1, 0); PG8_SCHED; PG8_LDA(1, 0); PG8_STAGE(PG8_SA(0, 1), a2 + hstep, voffA);
;             PG8_WAIT_L(8); PG8_BAR; PG8_HI; PG8_WAIT_L(0); PG8_MMA(0, 0, B0, B08); PG8_BAR; PG8_LO; PG8_SCHED;
;             PG8_LDB(B1, B18, 1, 1); PG8_STAGE(PG8_SB(1, 0), b3, voffB);
;             PG8_BAR; PG8_HI; PG8_WAIT_L(0); PG8_MMA(0, 1, B1, B18); PG8_BAR; PG8_LO;
	s_add_u32 s0, s30, 0x20000
	s_addc_u32 s1, s31, 0
	s_mov_b32 s64, m0
	s_mov_b32 m0, s46
	s_nop 0
	global_load_lds_dwordx4 v1, s[0:1]
	s_mov_b32 m0, s64
	s_add_u32 s0, s30, 0x30000
	s_addc_u32 s1, s31, 0
	s_mov_b32 s64, m0
	s_mov_b32 m0, s47
	s_nop 0
	global_load_lds_dwordx4 v1, s[0:1]
	s_mov_b32 m0, s64
	s_waitcnt vmcnt(6)
	s_barrier
	s_setprio 1
	v_mfma_f32_16x16x32_bf16 v[54:57], v[202:205], v[146:149], v[54:57]
	v_mfma_f32_16x16x32_bf16 v[50:53], v[210:213], v[146:149], v[50:53]
	v_mfma_f32_16x16x32_bf16 v[38:41], v[202:205], v[172:175], v[38:41]
	v_mfma_f32_16x16x32_bf16 v[34:37], v[210:213], v[172:175], v[34:37]
	v_mfma_f32_16x16x32_bf16 v[22:25], v[202:205], v[180:183], v[22:25]
	v_mfma_f32_16x16x32_bf16 v[18:21], v[210:213], v[180:183], v[18:21]
	v_mfma_f32_16x16x32_bf16 v[6:9], v[202:205], v[194:197], v[6:9]
	v_mfma_f32_16x16x32_bf16 v[2:5], v[210:213], v[194:197], v[2:5]
	v_mfma_f32_16x16x32_bf16 v[54:57], v[206:209], v[168:171], v[54:57]
	v_mfma_f32_16x16x32_bf16 v[50:53], v[214:217], v[168:171], v[50:53]
	v_mfma_f32_16x16x32_bf16 v[38:41], v[206:209], v[176:179], v[38:41]
	v_mfma_f32_16x16x32_bf16 v[34:37], v[214:217], v[176:179], v[34:37]
	v_mfma_f32_16x16x32_bf16 v[22:25], v[206:209], v[184:187], v[22:25]
	v_mfma_f32_16x16x32_bf16 v[18:21], v[214:217], v[184:187], v[18:21]
	v_mfma_f32_16x16x32_bf16 v[6:9], v[206:209], v[198:201], v[6:9]
	v_mfma_f32_16x16x32_bf16 v[2:5], v[214:217], v[198:201], v[2:5]
	s_setprio 0
	s_barrier
	ds_read_b128 v[130:133], v158
	ds_read_b128 v[134:137], v159
	ds_read_b128 v[138:141], v160
	ds_read_b128 v[142:145], v161
	ds_read_b128 v[146:149], v166 offset:32768
	ds_read_b128 v[168:171], v166 offset:33792
	ds_read_b128 v[172:175], v166 offset:34816
	ds_read_b128 v[176:179], v166 offset:35840
	ds_read_b128 v[180:183], v166 offset:36864
	ds_read_b128 v[184:187], v166 offset:37888
	ds_read_b128 v[194:197], v166 offset:38912
	ds_read_b128 v[198:201], v166 offset:39936
	s_add_u32 s0, s34, 0x20000
	s_addc_u32 s1, s35, 0
	s_mov_b32 s64, m0
	s_mov_b32 m0, s48
	s_nop 0
	global_load_lds_dwordx4 v1, s[0:1]
	s_mov_b32 m0, s64
	s_add_u32 s0, s34, 0x30000
	s_addc_u32 s1, s35, 0
	s_mov_b32 s64, m0
	s_mov_b32 m0, s49
	s_nop 0
	global_load_lds_dwordx4 v1, s[0:1]
	s_mov_b32 m0, s64
	s_waitcnt lgkmcnt(8)
	s_barrier
	s_waitcnt lgkmcnt(0)
	s_setprio 1
	v_mfma_f32_16x16x32_bf16 v[126:129], v[130:133], v[146:149], v[126:129]
	v_mfma_f32_16x16x32_bf16 v[122:125], v[138:141], v[146:149], v[122:125]
	v_mfma_f32_16x16x32_bf16 v[110:113], v[130:133], v[172:175], v[110:113]
	v_mfma_f32_16x16x32_bf16 v[106:109], v[138:141], v[172:175], v[106:109]
	v_mfma_f32_16x16x32_bf16 v[94:97], v[130:133], v[180:183], v[94:97]
	v_mfma_f32_16x16x32_bf16 v[90:93], v[138:141], v[180:183], v[90:93]
	v_mfma_f32_16x16x32_bf16 v[78:81], v[130:133], v[194:197], v[78:81]
	v_mfma_f32_16x16x32_bf16 v[74:77], v[138:141], v[194:197], v[74:77]
	v_mfma_f32_16x16x32_bf16 v[126:129], v[134:137], v[168:171], v[126:129]
	v_mfma_f32_16x16x32_bf16 v[122:125], v[142:145], v[168:171], v[122:125]
	v_mfma_f32_16x16x32_bf16 v[110:113], v[134:137], v[176:179], v[110:113]
	v_mfma_f32_16x16x32_bf16 v[106:109], v[142:145], v[176:179], v[106:109]
	v_mfma_f32_16x16x32_bf16 v[94:97], v[134:137], v[184:187], v[94:97]
	v_mfma_f32_16x16x32_bf16 v[90:93], v[142:145], v[184:187], v[90:93]
	v_mfma_f32_16x16x32_bf16 v[78:81], v[134:137], v[198:201], v[78:81]
	v_mfma_f32_16x16x32_bf16 v[74:77], v[142:145], v[198:201], v[74:77]
	s_setprio 0
	s_barrier
	ds_read_b128 v[202:205], v162
	ds_read_b128 v[206:209], v163
	ds_read_b128 v[210:213], v164
	ds_read_b128 v[214:217], v165
	s_add_u32 s0, s30, 0x80
	s_addc_u32 s1, s31, 0
	s_mov_b32 s64, m0
	s_mov_b32 m0, s52
	s_nop 0
	global_load_lds_dwordx4 v1, s[0:1]
	s_mov_b32 m0, s64
	s_add_u32 s0, s30, 0x10080
	s_addc_u32 s1, s31, 0
	s_mov_b32 s64, m0
	s_mov_b32 m0, s53
	s_nop 0
	global_load_lds_dwordx4 v1, s[0:1]
	s_mov_b32 m0, s64
	s_barrier
	s_waitcnt lgkmcnt(0)
	s_setprio 1
	v_mfma_f32_16x16x32_bf16 v[118:121], v[202:205], v[146:149], v[118:121]
	v_mfma_f32_16x16x32_bf16 v[114:117], v[210:213], v[146:149], v[114:117]
	v_mfma_f32_16x16x32_bf16 v[102:105], v[202:205], v[172:175], v[102:105]
	v_mfma_f32_16x16x32_bf16 v[98:101], v[210:213], v[172:175], v[98:101]
	v_mfma_f32_16x16x32_bf16 v[86:89], v[202:205], v[180:183], v[86:89]
	v_mfma_f32_16x16x32_bf16 v[82:85], v[210:213], v[180:183], v[82:85]
	v_mfma_f32_16x16x32_bf16 v[70:73], v[202:205], v[194:197], v[70:73]
	v_mfma_f32_16x16x32_bf16 v[66:69], v[210:213], v[194:197], v[66:69]
	v_mfma_f32_16x16x32_bf16 v[118:121], v[206:209], v[168:171], v[118:121]
	v_mfma_f32_16x16x32_bf16 v[114:117], v[214:217], v[168:171], v[114:117]
	v_mfma_f32_16x16x32_bf16 v[102:105], v[206:209], v[176:179], v[102:105]
	v_mfma_f32_16x16x32_bf16 v[98:101], v[214:217], v[176:179], v[98:101]
	v_mfma_f32_16x16x32_bf16 v[86:89], v[206:209], v[184:187], v[86:89]
	v_mfma_f32_16x16x32_bf16 v[82:85], v[214:217], v[184:187], v[82:85]
	v_mfma_f32_16x16x32_bf16 v[70:73], v[206:209], v[198:201], v[70:73]
	v_mfma_f32_16x16x32_bf16 v[66:69], v[214:217], v[198:201], v[66:69]
	s_setprio 0
	s_barrier
; #define PG8_STAGE(bufoff, gbase, voff) do { _Pragma("unroll") for (int _i = 0; _i < 2; ++_i) glds16_s((const void*)((const char*)(gbase) + _i * r64), (voff), ldsb + (unsigned)(bufoff) + ldsw + _i * 8192u); } while (0)
; #define PG8_LDA(b, h) do { _Pragma("unroll") for (int m = 0; m < 4; ++m) { const int o_ = PG8_SA(b, h) + aoff + m * 2048; \
;         if constexpr (FP8) A8[m] = PG8_CAT8(o_); else { At[m][0] = PG8_LD16(o_); At[m][1] = PG8_LD16(o_ + 1024); } } } while (0)
; #define PG8_WAIT_V(n) asm volatile("s_waitcnt vmcnt(" #n ")" ::: "memory")
; #define PG8_WAIT_L(n) asm volatile("s_waitcnt lgkmcnt(" #n ")" ::: "memory")
; #define PG8_BAR __builtin_amdgcn_s_barrier()
; #define PG8_SCHED __builtin_amdgcn_sched_barrier(0)
; #define PG8_HI do { if constexpr (FP8) asm volatile("s_setprio 1"); } while (0)
; #define PG8_LO do { if constexpr (FP8) asm volatile("s_setprio 0"); } while (0)
;     __device__ __forceinline__ void operator()(const f32x4 (&acc)[2][2][4][2], const Unit& u, int wr, int wc, int fr, int fq) const {
;         const int row0 = u.pm * BM + wr * 64 + fr, col0 = u.pn * BM + wc * 32 + 4 * fq;
;         f32x4 cs[2][2];
; #pragma unroll
;         for (int bj = 0; bj < 2; ++bj)
; #pragma unroll
;             for (int n = 0; n < 2; ++n) cs[bj][n] = (cscale ? *(const f32x4*)(cscale + col0 + bj * HALF + n * 16) : (f32x4){1.f, 1.f, 1.f, 1.f}) * ascale;
; template <class Epi, class Sched, bool FP8 = false>
; __device__ __forceinline__ void gemm_phase(LAS unsigned char* lds, const int Kb, const int nt  , const Sched& S, const Epi& E) {
;     ...
;             PG8_LDA(1, 1); PG8_STAGE(PG8_SA(1, 0), a3, voffA);
;             PG8_BAR; PG8_HI; PG8_WAIT_L(0); PG8_MMA(1, 0, B0, B08); PG8_BAR; PG8_LO; PG8_SCHED;
;             PG8_STAGE(PG8_SB(1, 1), b3 + hstep, voffB);
;             PG8_WAIT_V(6); PG8_BAR; PG8_HI; PG8_MMA(1, 1, B1, B18); PG8_BAR; PG8_LO;
	ds_read_b128 v[146:149], v166 offset:49152
	ds_read_b128 v[168:171], v166 offset:50176
	ds_read_b128 v[172:175], v166 offset:51200
	ds_read_b128 v[176:179], v166 offset:52224
	ds_read_b128 v[180:183], v166 offset:53248
	ds_read_b128 v[184:187], v166 offset:54272
	ds_read_b128 v[194:197], v166 offset:55296
	ds_read_b128 v[198:201], v166 offset:56320
	s_mov_b32 s0, m0
	s_mov_b32 m0, s54
	s_nop 0
	global_load_lds_dwordx4 v1, s[36:37]
	s_mov_b32 m0, s0
	s_add_u32 s0, s34, 0x10080
	s_addc_u32 s1, s35, 0
	s_mov_b32 s34, m0
	s_mov_b32 m0, s55
	s_nop 0
	global_load_lds_dwordx4 v1, s[0:1]
	s_mov_b32 m0, s34
	s_barrier
	s_waitcnt lgkmcnt(0)
	s_setprio 1
	v_mfma_f32_16x16x32_bf16 v[62:65], v[130:133], v[146:149], v[62:65]
	v_mfma_f32_16x16x32_bf16 v[58:61], v[138:141], v[146:149], v[58:61]
	v_mfma_f32_16x16x32_bf16 v[46:49], v[130:133], v[172:175], v[46:49]
	v_mfma_f32_16x16x32_bf16 v[42:45], v[138:141], v[172:175], v[42:45]
	v_mfma_f32_16x16x32_bf16 v[30:33], v[130:133], v[180:183], v[30:33]
	v_mfma_f32_16x16x32_bf16 v[26:29], v[138:141], v[180:183], v[26:29]
	v_mfma_f32_16x16x32_bf16 v[14:17], v[130:133], v[194:197], v[14:17]
	v_mfma_f32_16x16x32_bf16 v[10:13], v[138:141], v[194:197], v[10:13]
	v_mfma_f32_16x16x32_bf16 v[62:65], v[134:137], v[168:171], v[62:65]
	v_mfma_f32_16x16x32_bf16 v[58:61], v[142:145], v[168:171], v[58:61]
	v_mfma_f32_16x16x32_bf16 v[46:49], v[134:137], v[176:179], v[46:49]
	v_mfma_f32_16x16x32_bf16 v[42:45], v[142:145], v[176:179], v[42:45]
	v_mfma_f32_16x16x32_bf16 v[30:33], v[134:137], v[184:187], v[30:33]
	v_mfma_f32_16x16x32_bf16 v[26:29], v[142:145], v[184:187], v[26:29]
	v_mfma_f32_16x16x32_bf16 v[14:17], v[134:137], v[198:201], v[14:17]
	v_mfma_f32_16x16x32_bf16 v[10:13], v[142:145], v[198:201], v[10:13]
	s_setprio 0
	s_barrier
	s_add_u32 s0, s30, 0x20080
	s_addc_u32 s1, s31, 0
	s_mov_b32 s34, m0
	s_mov_b32 m0, s56
	s_nop 0
	global_load_lds_dwordx4 v1, s[0:1]
	s_mov_b32 m0, s34
	s_add_u32 s0, s30, 0x30080
	s_addc_u32 s1, s31, 0
	s_mov_b32 s30, m0
	s_mov_b32 m0, s57
	s_nop 0
	global_load_lds_dwordx4 v1, s[0:1]
	s_mov_b32 m0, s30
	s_waitcnt vmcnt(6)
	s_barrier
	s_setprio 1
	v_mfma_f32_16x16x32_bf16 v[54:57], v[202:205], v[146:149], v[54:57]
	v_mfma_f32_16x16x32_bf16 v[50:53], v[210:213], v[146:149], v[50:53]
	v_mfma_f32_16x16x32_bf16 v[38:41], v[202:205], v[172:175], v[38:41]
	v_mfma_f32_16x16x32_bf16 v[34:37], v[210:213], v[172:175], v[34:37]
	v_mfma_f32_16x16x32_bf16 v[22:25], v[202:205], v[180:183], v[22:25]
	v_mfma_f32_16x16x32_bf16 v[18:21], v[210:213], v[180:183], v[18:21]
	v_mfma_f32_16x16x32_bf16 v[6:9], v[202:205], v[194:197], v[6:9]
	v_mfma_f32_16x16x32_bf16 v[2:5], v[210:213], v[194:197], v[2:5]
	v_mfma_f32_16x16x32_bf16 v[54:57], v[206:209], v[168:171], v[54:57]
	v_mfma_f32_16x16x32_bf16 v[50:53], v[214:217], v[168:171], v[50:53]
	v_mfma_f32_16x16x32_bf16 v[38:41], v[206:209], v[176:179], v[38:41]
	v_mfma_f32_16x16x32_bf16 v[34:37], v[214:217], v[176:179], v[34:37]
	v_mfma_f32_16x16x32_bf16 v[22:25], v[206:209], v[184:187], v[22:25]
	v_mfma_f32_16x16x32_bf16 v[18:21], v[214:217], v[184:187], v[18:21]
	v_mfma_f32_16x16x32_bf16 v[6:9], v[206:209], v[198:201], v[6:9]
	v_mfma_f32_16x16x32_bf16 v[2:5], v[214:217], v[198:201], v[2:5]
	s_setprio 0
	s_add_i32 s63, s63, 2
	s_add_u32 s21, s21, 0x100
	s_addc_u32 s62, s62, 0
	s_cmp_gt_u32 s63, 5
	s_mov_b64 s[0:1], s[28:29]
	s_barrier
	s_cbranch_scc0 .LBB0_2332
	v_mbcnt_lo_u32_b32 v167, -1, 0
	v_mbcnt_hi_u32_b32 v167, -1, v167
	s_lshl_b32 s0, s61, 8
	v_ashrrev_i32_e32 v130, 2, v167
	s_or_b32 s0, s0, s51
	v_and_b32_e32 v130, -4, v130
	v_add_u32_e32 v148, s0, v130
	v_readlane_b32 s80, v241, 26
	v_ashrrev_i32_e32 v149, 31, v148
	v_readlane_b32 s94, v241, 40
	v_readlane_b32 s95, v241, 41
	v_cndmask_b32_e64 v131, 0, 1, s[8:9]
	v_mov_b32_e32 v130, 1.0
	v_lshl_add_u64 v[146:147], v[148:149], 2, s[94:95]
	v_cmp_ne_u32_e64 s[0:1], 1, v131
	s_andn2_b64 vcc, exec, s[8:9]
	v_mov_b32_e32 v134, 1.0
	v_mov_b32_e32 v135, 1.0
	v_mov_b32_e32 v136, 1.0
	v_mov_b32_e32 v137, 1.0
	v_readlane_b32 s81, v241, 27
	v_readlane_b32 s82, v241, 28
	v_readlane_b32 s83, v241, 29
	v_readlane_b32 s84, v241, 30
	v_readlane_b32 s85, v241, 31
	v_readlane_b32 s86, v241, 32
	v_readlane_b32 s87, v241, 33
	v_readlane_b32 s88, v241, 34
	v_readlane_b32 s89, v241, 35
	v_readlane_b32 s90, v241, 36
	v_readlane_b32 s91, v241, 37
	v_readlane_b32 s92, v241, 38
	v_readlane_b32 s93, v241, 39
	s_cbranch_vccnz .LBB0_2335
	global_load_dwordx4 v[134:137], v[146:147], off
